# nt hint also on the router's XB row loads (P4)
# baseline (speedup 1.0000x reference)
.LBB0_435:
	v_add_u32_e32 v166, s3, v171
	v_ashrrev_i32_e32 v167, 31, v166
	v_lshlrev_b64 v[2:3], 11, v[166:167]
	v_lshl_add_u64 v[2:3], v[140:141], 0, v[2:3]
	global_load_dwordx4 v[126:129], v[2:3], off nt
	global_load_dwordx4 v[122:125], v[2:3], off offset:64 nt
	global_load_dwordx4 v[118:121], v[2:3], off offset:128 nt
	global_load_dwordx4 v[114:117], v[2:3], off offset:192 nt
	global_load_dwordx4 v[110:113], v[2:3], off offset:256 nt
	global_load_dwordx4 v[106:109], v[2:3], off offset:320 nt
	global_load_dwordx4 v[102:105], v[2:3], off offset:384 nt
	global_load_dwordx4 v[98:101], v[2:3], off offset:448 nt
	global_load_dwordx4 v[94:97], v[2:3], off offset:512 nt
	global_load_dwordx4 v[90:93], v[2:3], off offset:576 nt
	global_load_dwordx4 v[86:89], v[2:3], off offset:640 nt
	global_load_dwordx4 v[82:85], v[2:3], off offset:704 nt
	global_load_dwordx4 v[78:81], v[2:3], off offset:768 nt
	global_load_dwordx4 v[74:77], v[2:3], off offset:832 nt
	global_load_dwordx4 v[70:73], v[2:3], off offset:896 nt
	global_load_dwordx4 v[66:69], v[2:3], off offset:960 nt
	global_load_dwordx4 v[62:65], v[2:3], off offset:1024 nt
	global_load_dwordx4 v[58:61], v[2:3], off offset:1088 nt
	global_load_dwordx4 v[54:57], v[2:3], off offset:1152 nt
	global_load_dwordx4 v[50:53], v[2:3], off offset:1216 nt
	global_load_dwordx4 v[46:49], v[2:3], off offset:1280 nt
	global_load_dwordx4 v[42:45], v[2:3], off offset:1344 nt
	global_load_dwordx4 v[38:41], v[2:3], off offset:1408 nt
	global_load_dwordx4 v[34:37], v[2:3], off offset:1472 nt
	global_load_dwordx4 v[30:33], v[2:3], off offset:1536 nt
	global_load_dwordx4 v[26:29], v[2:3], off offset:1600 nt
	global_load_dwordx4 v[22:25], v[2:3], off offset:1664 nt
	global_load_dwordx4 v[18:21], v[2:3], off offset:1728 nt
	global_load_dwordx4 v[14:17], v[2:3], off offset:1792 nt
	global_load_dwordx4 v[10:13], v[2:3], off offset:1856 nt
	global_load_dwordx4 v[6:9], v[2:3], off offset:1920 nt
	s_nop 0
	global_load_dwordx4 v[2:5], v[2:3], off offset:1984 nt
	ds_read_b128 v[130:133], v175 offset:33024
	ds_read_b128 v[134:137], v175 offset:33088
	ds_read_b128 v[210:213], v175
	ds_read_b128 v[214:217], v175 offset:64
	ds_read_b128 v[218:221], v174 offset:33024
	ds_read_b128 v[222:225], v174 offset:33088
	ds_read_b128 v[226:229], v174
	ds_read_b128 v[230:233], v174 offset:64
	v_lshlrev_b64 v[168:169], 10, v[166:167]
	s_waitcnt vmcnt(31) lgkmcnt(1)
	v_mfma_f32_16x16x32_bf16 v[226:229], v[126:129], v[226:229], 0
	v_and_b32_e32 v147, 0xffff0000, v126
	v_and_b32_e32 v151, 0xffff0000, v127
	v_lshlrev_b32_e32 v145, 16, v126
	v_mfma_f32_16x16x32_bf16 v[218:221], v[126:129], v[218:221], 0
	v_lshlrev_b32_e32 v149, 16, v127
	v_and_b32_e32 v155, 0xffff0000, v128
	v_mul_f32_e32 v147, v147, v147
	v_mul_f32_e32 v151, v151, v151
	v_mfma_f32_16x16x32_bf16 v[210:213], v[126:129], v[210:213], v[226:229]
	v_lshlrev_b32_e32 v153, 16, v128
	v_and_b32_e32 v159, 0xffff0000, v129
	v_mul_f32_e32 v155, v155, v155
	v_mfma_f32_16x16x32_bf16 v[130:133], v[126:129], v[130:133], v[218:221]
	v_fmac_f32_e32 v147, v145, v145
	v_fmac_f32_e32 v151, v149, v149
	v_lshlrev_b32_e32 v157, 16, v129
	s_waitcnt vmcnt(30)
	v_and_b32_e32 v234, 0xffff0000, v122
	v_mul_f32_e32 v159, v159, v159
	v_fmac_f32_e32 v155, v153, v153
	v_add_f32_e32 v145, v147, v151
	v_lshlrev_b32_e32 v167, 16, v122
	v_and_b32_e32 v236, 0xffff0000, v123
	v_mul_f32_e32 v234, v234, v234
	v_fmac_f32_e32 v159, v157, v157
	v_add_f32_e32 v145, v155, v145
	v_lshlrev_b32_e32 v235, 16, v123
	v_and_b32_e32 v238, 0xffff0000, v124
	v_mul_f32_e32 v236, v236, v236
	v_fmac_f32_e32 v234, v167, v167
	s_waitcnt lgkmcnt(0)
	v_mfma_f32_16x16x32_bf16 v[210:213], v[122:125], v[230:233], v[210:213]
	v_add_f32_e32 v145, v159, v145
	v_lshlrev_b32_e32 v237, 16, v124
	v_and_b32_e32 v240, 0xffff0000, v125
	v_mfma_f32_16x16x32_bf16 v[130:133], v[122:125], v[222:225], v[130:133]
	v_mul_f32_e32 v238, v238, v238
	v_fmac_f32_e32 v236, v235, v235
	v_add_f32_e32 v145, v234, v145
	v_lshlrev_b32_e32 v239, 16, v125
	v_mul_f32_e32 v240, v240, v240
	v_fmac_f32_e32 v238, v237, v237
	v_add_f32_e32 v145, v236, v145
	v_fmac_f32_e32 v240, v239, v239
	v_add_f32_e32 v145, v238, v145
	v_mfma_f32_16x16x32_bf16 v[210:213], v[122:125], v[214:217], v[210:213]
	v_add_f32_e32 v145, v240, v145
	v_mfma_f32_16x16x32_bf16 v[130:133], v[122:125], v[134:137], v[130:133]
	s_waitcnt vmcnt(29)
	v_and_b32_e32 v149, 0xffff0000, v118
	v_lshlrev_b32_e32 v147, 16, v118
	v_mul_f32_e32 v149, v149, v149
	v_fmac_f32_e32 v149, v147, v147
	v_add_f32_e32 v145, v149, v145
	v_and_b32_e32 v149, 0xffff0000, v119
	v_lshlrev_b32_e32 v147, 16, v119
	v_mul_f32_e32 v149, v149, v149
	v_fmac_f32_e32 v149, v147, v147
	v_add_f32_e32 v145, v149, v145
	v_and_b32_e32 v149, 0xffff0000, v120
	v_lshlrev_b32_e32 v147, 16, v120
	v_mul_f32_e32 v149, v149, v149
	v_fmac_f32_e32 v149, v147, v147
	v_add_f32_e32 v145, v149, v145
	v_and_b32_e32 v149, 0xffff0000, v121
	ds_read_b128 v[134:137], v174 offset:128
	ds_read_b128 v[214:217], v174 offset:33152
	ds_read_b128 v[218:221], v175 offset:128
	ds_read_b128 v[222:225], v175 offset:33152
	ds_read_b128 v[226:229], v174 offset:192
	v_lshlrev_b32_e32 v147, 16, v121
	v_mul_f32_e32 v149, v149, v149
	s_waitcnt lgkmcnt(4)
	v_mfma_f32_16x16x32_bf16 v[134:137], v[118:121], v[134:137], v[210:213]
	v_fmac_f32_e32 v149, v147, v147
	v_add_f32_e32 v145, v149, v145
	s_waitcnt vmcnt(28)
	v_and_b32_e32 v149, 0xffff0000, v114
	s_waitcnt lgkmcnt(3)
	v_mfma_f32_16x16x32_bf16 v[130:133], v[118:121], v[214:217], v[130:133]
	v_lshlrev_b32_e32 v147, 16, v114
	v_mul_f32_e32 v149, v149, v149
	v_fmac_f32_e32 v149, v147, v147
	s_waitcnt lgkmcnt(2)
	v_mfma_f32_16x16x32_bf16 v[134:137], v[118:121], v[218:221], v[134:137]
	ds_read_b128 v[218:221], v174 offset:33216
	ds_read_b128 v[214:217], v175 offset:33216
	v_add_f32_e32 v145, v149, v145
	v_and_b32_e32 v149, 0xffff0000, v115
	s_waitcnt lgkmcnt(3)
	v_mfma_f32_16x16x32_bf16 v[130:133], v[118:121], v[222:225], v[130:133]
	v_lshlrev_b32_e32 v147, 16, v115
	v_mul_f32_e32 v149, v149, v149
	v_fmac_f32_e32 v149, v147, v147
	v_add_f32_e32 v145, v149, v145
	v_and_b32_e32 v149, 0xffff0000, v116
	ds_read_b128 v[210:213], v175 offset:192
	v_lshlrev_b32_e32 v147, 16, v116
	v_mul_f32_e32 v149, v149, v149
	s_waitcnt lgkmcnt(3)
	v_mfma_f32_16x16x32_bf16 v[134:137], v[114:117], v[226:229], v[134:137]
	v_fmac_f32_e32 v149, v147, v147
	v_add_f32_e32 v145, v149, v145
	v_and_b32_e32 v149, 0xffff0000, v117
	s_waitcnt lgkmcnt(2)
	v_mfma_f32_16x16x32_bf16 v[130:133], v[114:117], v[218:221], v[130:133]
	v_lshlrev_b32_e32 v147, 16, v117
	v_mul_f32_e32 v149, v149, v149
	v_fmac_f32_e32 v149, v147, v147
	s_waitcnt lgkmcnt(0)
	v_mfma_f32_16x16x32_bf16 v[134:137], v[114:117], v[210:213], v[134:137]
	v_add_f32_e32 v145, v149, v145
	v_mfma_f32_16x16x32_bf16 v[130:133], v[114:117], v[214:217], v[130:133]
	s_waitcnt vmcnt(27)
	v_and_b32_e32 v149, 0xffff0000, v110
	v_lshlrev_b32_e32 v147, 16, v110
	v_mul_f32_e32 v149, v149, v149
	v_fmac_f32_e32 v149, v147, v147
	v_add_f32_e32 v145, v149, v145
	v_and_b32_e32 v149, 0xffff0000, v111
	v_lshlrev_b32_e32 v147, 16, v111
	v_mul_f32_e32 v149, v149, v149
	v_fmac_f32_e32 v149, v147, v147
	v_add_f32_e32 v145, v149, v145
	v_and_b32_e32 v149, 0xffff0000, v112
	v_lshlrev_b32_e32 v147, 16, v112
	v_mul_f32_e32 v149, v149, v149
	v_fmac_f32_e32 v149, v147, v147
	v_add_f32_e32 v145, v149, v145
	v_and_b32_e32 v149, 0xffff0000, v113
	ds_read_b128 v[210:213], v174 offset:256
	ds_read_b128 v[214:217], v174 offset:33280
	ds_read_b128 v[218:221], v175 offset:256
	ds_read_b128 v[222:225], v175 offset:33280
	ds_read_b128 v[226:229], v174 offset:320
	v_lshlrev_b32_e32 v147, 16, v113
	v_mul_f32_e32 v149, v149, v149
	s_waitcnt lgkmcnt(4)
	v_mfma_f32_16x16x32_bf16 v[134:137], v[110:113], v[210:213], v[134:137]
	v_fmac_f32_e32 v149, v147, v147
	v_add_f32_e32 v145, v149, v145
	s_waitcnt vmcnt(26)
	v_and_b32_e32 v149, 0xffff0000, v106
	s_waitcnt lgkmcnt(3)
	v_mfma_f32_16x16x32_bf16 v[130:133], v[110:113], v[214:217], v[130:133]
	v_lshlrev_b32_e32 v147, 16, v106
	v_mul_f32_e32 v149, v149, v149
	v_fmac_f32_e32 v149, v147, v147
	s_waitcnt lgkmcnt(2)
	v_mfma_f32_16x16x32_bf16 v[134:137], v[110:113], v[218:221], v[134:137]
	ds_read_b128 v[218:221], v174 offset:33344
	ds_read_b128 v[214:217], v175 offset:33344
	v_add_f32_e32 v145, v149, v145
	v_and_b32_e32 v149, 0xffff0000, v107
	s_waitcnt lgkmcnt(3)
	v_mfma_f32_16x16x32_bf16 v[130:133], v[110:113], v[222:225], v[130:133]
	v_lshlrev_b32_e32 v147, 16, v107
	v_mul_f32_e32 v149, v149, v149
	v_fmac_f32_e32 v149, v147, v147
	v_add_f32_e32 v145, v149, v145
	v_and_b32_e32 v149, 0xffff0000, v108
	ds_read_b128 v[210:213], v175 offset:320
	v_lshlrev_b32_e32 v147, 16, v108
	v_mul_f32_e32 v149, v149, v149
	s_waitcnt lgkmcnt(3)
	v_mfma_f32_16x16x32_bf16 v[134:137], v[106:109], v[226:229], v[134:137]
	v_fmac_f32_e32 v149, v147, v147
	v_add_f32_e32 v145, v149, v145
	v_and_b32_e32 v149, 0xffff0000, v109
	s_waitcnt lgkmcnt(2)
	v_mfma_f32_16x16x32_bf16 v[130:133], v[106:109], v[218:221], v[130:133]
	v_lshlrev_b32_e32 v147, 16, v109
	v_mul_f32_e32 v149, v149, v149
	v_fmac_f32_e32 v149, v147, v147
	s_waitcnt lgkmcnt(0)
	v_mfma_f32_16x16x32_bf16 v[134:137], v[106:109], v[210:213], v[134:137]
	v_add_f32_e32 v145, v149, v145
	v_mfma_f32_16x16x32_bf16 v[130:133], v[106:109], v[214:217], v[130:133]
	s_waitcnt vmcnt(25)
	v_and_b32_e32 v149, 0xffff0000, v102
	v_lshlrev_b32_e32 v147, 16, v102
	v_mul_f32_e32 v149, v149, v149
	v_fmac_f32_e32 v149, v147, v147
	v_add_f32_e32 v145, v149, v145
	v_and_b32_e32 v149, 0xffff0000, v103
	v_lshlrev_b32_e32 v147, 16, v103
	v_mul_f32_e32 v149, v149, v149
	v_fmac_f32_e32 v149, v147, v147
	v_add_f32_e32 v145, v149, v145
	v_and_b32_e32 v149, 0xffff0000, v104
	v_lshlrev_b32_e32 v147, 16, v104
	v_mul_f32_e32 v149, v149, v149
	v_fmac_f32_e32 v149, v147, v147
	v_add_f32_e32 v145, v149, v145
	v_and_b32_e32 v149, 0xffff0000, v105
	ds_read_b128 v[210:213], v174 offset:384
	ds_read_b128 v[214:217], v174 offset:33408
	ds_read_b128 v[218:221], v175 offset:384
	ds_read_b128 v[222:225], v175 offset:33408
	ds_read_b128 v[226:229], v174 offset:448
	v_lshlrev_b32_e32 v147, 16, v105
	v_mul_f32_e32 v149, v149, v149
	s_waitcnt lgkmcnt(4)
	v_mfma_f32_16x16x32_bf16 v[134:137], v[102:105], v[210:213], v[134:137]
	v_fmac_f32_e32 v149, v147, v147
	v_add_f32_e32 v145, v149, v145
	s_waitcnt vmcnt(24)
	v_and_b32_e32 v149, 0xffff0000, v98
	s_waitcnt lgkmcnt(3)
	v_mfma_f32_16x16x32_bf16 v[130:133], v[102:105], v[214:217], v[130:133]
	v_lshlrev_b32_e32 v147, 16, v98
	v_mul_f32_e32 v149, v149, v149
	v_fmac_f32_e32 v149, v147, v147
	s_waitcnt lgkmcnt(2)
	v_mfma_f32_16x16x32_bf16 v[134:137], v[102:105], v[218:221], v[134:137]
	ds_read_b128 v[218:221], v174 offset:33472
	ds_read_b128 v[214:217], v175 offset:33472
	v_add_f32_e32 v145, v149, v145
	v_and_b32_e32 v149, 0xffff0000, v99
	s_waitcnt lgkmcnt(3)
	v_mfma_f32_16x16x32_bf16 v[130:133], v[102:105], v[222:225], v[130:133]
	v_lshlrev_b32_e32 v147, 16, v99
	v_mul_f32_e32 v149, v149, v149
	v_fmac_f32_e32 v149, v147, v147
	v_add_f32_e32 v145, v149, v145
	v_and_b32_e32 v149, 0xffff0000, v100
	ds_read_b128 v[210:213], v175 offset:448
	v_lshlrev_b32_e32 v147, 16, v100
	v_mul_f32_e32 v149, v149, v149
	s_waitcnt lgkmcnt(3)
	v_mfma_f32_16x16x32_bf16 v[134:137], v[98:101], v[226:229], v[134:137]
	v_fmac_f32_e32 v149, v147, v147
	v_add_f32_e32 v145, v149, v145
	v_and_b32_e32 v149, 0xffff0000, v101
	s_waitcnt lgkmcnt(2)
	v_mfma_f32_16x16x32_bf16 v[130:133], v[98:101], v[218:221], v[130:133]
	v_lshlrev_b32_e32 v147, 16, v101
	v_mul_f32_e32 v149, v149, v149
	v_fmac_f32_e32 v149, v147, v147
	s_waitcnt lgkmcnt(0)
	v_mfma_f32_16x16x32_bf16 v[134:137], v[98:101], v[210:213], v[134:137]
	v_add_f32_e32 v145, v149, v145
	v_mfma_f32_16x16x32_bf16 v[130:133], v[98:101], v[214:217], v[130:133]
	s_waitcnt vmcnt(23)
	v_and_b32_e32 v149, 0xffff0000, v94
	v_lshlrev_b32_e32 v147, 16, v94
	v_mul_f32_e32 v149, v149, v149
	v_fmac_f32_e32 v149, v147, v147
	v_add_f32_e32 v145, v149, v145
	v_and_b32_e32 v149, 0xffff0000, v95
	v_lshlrev_b32_e32 v147, 16, v95
	v_mul_f32_e32 v149, v149, v149
	v_fmac_f32_e32 v149, v147, v147
	v_add_f32_e32 v145, v149, v145
	v_and_b32_e32 v149, 0xffff0000, v96
	v_lshlrev_b32_e32 v147, 16, v96
	v_mul_f32_e32 v149, v149, v149
	v_fmac_f32_e32 v149, v147, v147
	v_add_f32_e32 v145, v149, v145
	v_and_b32_e32 v149, 0xffff0000, v97
	ds_read_b128 v[210:213], v174 offset:512
	ds_read_b128 v[214:217], v174 offset:33536
	ds_read_b128 v[218:221], v175 offset:512
	ds_read_b128 v[222:225], v175 offset:33536
	ds_read_b128 v[226:229], v174 offset:576
	v_lshlrev_b32_e32 v147, 16, v97
	v_mul_f32_e32 v149, v149, v149
	s_waitcnt lgkmcnt(4)
	v_mfma_f32_16x16x32_bf16 v[134:137], v[94:97], v[210:213], v[134:137]
	v_fmac_f32_e32 v149, v147, v147
	v_add_f32_e32 v145, v149, v145
	s_waitcnt vmcnt(22)
	v_and_b32_e32 v149, 0xffff0000, v90
	s_waitcnt lgkmcnt(3)
	v_mfma_f32_16x16x32_bf16 v[130:133], v[94:97], v[214:217], v[130:133]
	v_lshlrev_b32_e32 v147, 16, v90
	v_mul_f32_e32 v149, v149, v149
	v_fmac_f32_e32 v149, v147, v147
	s_waitcnt lgkmcnt(2)
	v_mfma_f32_16x16x32_bf16 v[134:137], v[94:97], v[218:221], v[134:137]
	ds_read_b128 v[218:221], v174 offset:33600
	ds_read_b128 v[214:217], v175 offset:33600
	v_add_f32_e32 v145, v149, v145
	v_and_b32_e32 v149, 0xffff0000, v91
	s_waitcnt lgkmcnt(3)
	v_mfma_f32_16x16x32_bf16 v[130:133], v[94:97], v[222:225], v[130:133]
	v_lshlrev_b32_e32 v147, 16, v91
	v_mul_f32_e32 v149, v149, v149
	v_fmac_f32_e32 v149, v147, v147
	v_add_f32_e32 v145, v149, v145
	v_and_b32_e32 v149, 0xffff0000, v92
	ds_read_b128 v[210:213], v175 offset:576
	v_lshlrev_b32_e32 v147, 16, v92
	v_mul_f32_e32 v149, v149, v149
	s_waitcnt lgkmcnt(3)
	v_mfma_f32_16x16x32_bf16 v[134:137], v[90:93], v[226:229], v[134:137]
	v_fmac_f32_e32 v149, v147, v147
	v_add_f32_e32 v145, v149, v145
	v_and_b32_e32 v149, 0xffff0000, v93
	s_waitcnt lgkmcnt(2)
	v_mfma_f32_16x16x32_bf16 v[130:133], v[90:93], v[218:221], v[130:133]
	v_lshlrev_b32_e32 v147, 16, v93
	v_mul_f32_e32 v149, v149, v149
	v_fmac_f32_e32 v149, v147, v147
	s_waitcnt lgkmcnt(0)
	v_mfma_f32_16x16x32_bf16 v[134:137], v[90:93], v[210:213], v[134:137]
	v_add_f32_e32 v145, v149, v145
	v_mfma_f32_16x16x32_bf16 v[130:133], v[90:93], v[214:217], v[130:133]
	s_waitcnt vmcnt(21)
	v_and_b32_e32 v149, 0xffff0000, v86
	v_lshlrev_b32_e32 v147, 16, v86
	v_mul_f32_e32 v149, v149, v149
	v_fmac_f32_e32 v149, v147, v147
	v_add_f32_e32 v145, v149, v145
	v_and_b32_e32 v149, 0xffff0000, v87
	v_lshlrev_b32_e32 v147, 16, v87
	v_mul_f32_e32 v149, v149, v149
	v_fmac_f32_e32 v149, v147, v147
	v_add_f32_e32 v145, v149, v145
	v_and_b32_e32 v149, 0xffff0000, v88
	v_lshlrev_b32_e32 v147, 16, v88
	v_mul_f32_e32 v149, v149, v149
	v_fmac_f32_e32 v149, v147, v147
	v_add_f32_e32 v145, v149, v145
	v_and_b32_e32 v149, 0xffff0000, v89
	ds_read_b128 v[210:213], v174 offset:640
	ds_read_b128 v[214:217], v174 offset:33664
	ds_read_b128 v[218:221], v175 offset:640
	ds_read_b128 v[222:225], v175 offset:33664
	ds_read_b128 v[226:229], v174 offset:704
	v_lshlrev_b32_e32 v147, 16, v89
	v_mul_f32_e32 v149, v149, v149
	s_waitcnt lgkmcnt(4)
	v_mfma_f32_16x16x32_bf16 v[134:137], v[86:89], v[210:213], v[134:137]
	v_fmac_f32_e32 v149, v147, v147
	v_add_f32_e32 v145, v149, v145
	s_waitcnt vmcnt(20)
	v_and_b32_e32 v149, 0xffff0000, v82
	s_waitcnt lgkmcnt(3)
	v_mfma_f32_16x16x32_bf16 v[130:133], v[86:89], v[214:217], v[130:133]
	v_lshlrev_b32_e32 v147, 16, v82
	v_mul_f32_e32 v149, v149, v149
	v_fmac_f32_e32 v149, v147, v147
	s_waitcnt lgkmcnt(2)
	v_mfma_f32_16x16x32_bf16 v[134:137], v[86:89], v[218:221], v[134:137]
	ds_read_b128 v[218:221], v174 offset:33728
	ds_read_b128 v[214:217], v175 offset:33728
	v_add_f32_e32 v145, v149, v145
	v_and_b32_e32 v149, 0xffff0000, v83
	s_waitcnt lgkmcnt(3)
	v_mfma_f32_16x16x32_bf16 v[130:133], v[86:89], v[222:225], v[130:133]
	v_lshlrev_b32_e32 v147, 16, v83
	v_mul_f32_e32 v149, v149, v149
	v_fmac_f32_e32 v149, v147, v147
	v_add_f32_e32 v145, v149, v145
	v_and_b32_e32 v149, 0xffff0000, v84
	ds_read_b128 v[210:213], v175 offset:704
	v_lshlrev_b32_e32 v147, 16, v84
	v_mul_f32_e32 v149, v149, v149
	s_waitcnt lgkmcnt(3)
	v_mfma_f32_16x16x32_bf16 v[134:137], v[82:85], v[226:229], v[134:137]
	v_fmac_f32_e32 v149, v147, v147
	v_add_f32_e32 v145, v149, v145
	v_and_b32_e32 v149, 0xffff0000, v85
	s_waitcnt lgkmcnt(2)
	v_mfma_f32_16x16x32_bf16 v[130:133], v[82:85], v[218:221], v[130:133]
	v_lshlrev_b32_e32 v147, 16, v85
	v_mul_f32_e32 v149, v149, v149
	v_fmac_f32_e32 v149, v147, v147
	s_waitcnt lgkmcnt(0)
	v_mfma_f32_16x16x32_bf16 v[134:137], v[82:85], v[210:213], v[134:137]
	v_add_f32_e32 v145, v149, v145
	v_mfma_f32_16x16x32_bf16 v[130:133], v[82:85], v[214:217], v[130:133]
	s_waitcnt vmcnt(19)
	v_and_b32_e32 v149, 0xffff0000, v78
	v_lshlrev_b32_e32 v147, 16, v78
	v_mul_f32_e32 v149, v149, v149
	v_fmac_f32_e32 v149, v147, v147
	v_add_f32_e32 v145, v149, v145
	v_and_b32_e32 v149, 0xffff0000, v79
	v_lshlrev_b32_e32 v147, 16, v79
	v_mul_f32_e32 v149, v149, v149
	v_fmac_f32_e32 v149, v147, v147
	v_add_f32_e32 v145, v149, v145
	v_and_b32_e32 v149, 0xffff0000, v80
	v_lshlrev_b32_e32 v147, 16, v80
	v_mul_f32_e32 v149, v149, v149
	v_fmac_f32_e32 v149, v147, v147
	v_add_f32_e32 v145, v149, v145
	v_and_b32_e32 v149, 0xffff0000, v81
	ds_read_b128 v[210:213], v174 offset:768
	ds_read_b128 v[214:217], v174 offset:33792
	ds_read_b128 v[218:221], v175 offset:768
	ds_read_b128 v[222:225], v175 offset:33792
	ds_read_b128 v[226:229], v174 offset:832
	v_lshlrev_b32_e32 v147, 16, v81
	v_mul_f32_e32 v149, v149, v149
	s_waitcnt lgkmcnt(4)
	v_mfma_f32_16x16x32_bf16 v[134:137], v[78:81], v[210:213], v[134:137]
	v_fmac_f32_e32 v149, v147, v147
	v_add_f32_e32 v145, v149, v145
	s_waitcnt vmcnt(18)
	v_and_b32_e32 v149, 0xffff0000, v74
	s_waitcnt lgkmcnt(3)
	v_mfma_f32_16x16x32_bf16 v[130:133], v[78:81], v[214:217], v[130:133]
	v_lshlrev_b32_e32 v147, 16, v74
	v_mul_f32_e32 v149, v149, v149
	v_fmac_f32_e32 v149, v147, v147
	s_waitcnt lgkmcnt(2)
	v_mfma_f32_16x16x32_bf16 v[134:137], v[78:81], v[218:221], v[134:137]
	ds_read_b128 v[218:221], v174 offset:33856
	ds_read_b128 v[214:217], v175 offset:33856
	v_add_f32_e32 v145, v149, v145
	v_and_b32_e32 v149, 0xffff0000, v75
	s_waitcnt lgkmcnt(3)
	v_mfma_f32_16x16x32_bf16 v[130:133], v[78:81], v[222:225], v[130:133]
	v_lshlrev_b32_e32 v147, 16, v75
	v_mul_f32_e32 v149, v149, v149
	v_fmac_f32_e32 v149, v147, v147
	v_add_f32_e32 v145, v149, v145
	v_and_b32_e32 v149, 0xffff0000, v76
	ds_read_b128 v[210:213], v175 offset:832
	v_lshlrev_b32_e32 v147, 16, v76
	v_mul_f32_e32 v149, v149, v149
	s_waitcnt lgkmcnt(3)
	v_mfma_f32_16x16x32_bf16 v[134:137], v[74:77], v[226:229], v[134:137]
	v_fmac_f32_e32 v149, v147, v147
	v_add_f32_e32 v145, v149, v145
	v_and_b32_e32 v149, 0xffff0000, v77
	s_waitcnt lgkmcnt(2)
	v_mfma_f32_16x16x32_bf16 v[130:133], v[74:77], v[218:221], v[130:133]
	v_lshlrev_b32_e32 v147, 16, v77
	v_mul_f32_e32 v149, v149, v149
	v_fmac_f32_e32 v149, v147, v147
	s_waitcnt lgkmcnt(0)
	v_mfma_f32_16x16x32_bf16 v[134:137], v[74:77], v[210:213], v[134:137]
	v_add_f32_e32 v145, v149, v145
	v_mfma_f32_16x16x32_bf16 v[130:133], v[74:77], v[214:217], v[130:133]
	s_waitcnt vmcnt(17)
	v_and_b32_e32 v149, 0xffff0000, v70
	v_lshlrev_b32_e32 v147, 16, v70
	v_mul_f32_e32 v149, v149, v149
	v_fmac_f32_e32 v149, v147, v147
	v_add_f32_e32 v145, v149, v145
	v_and_b32_e32 v149, 0xffff0000, v71
	v_lshlrev_b32_e32 v147, 16, v71
	v_mul_f32_e32 v149, v149, v149
	v_fmac_f32_e32 v149, v147, v147
	v_add_f32_e32 v145, v149, v145
	v_and_b32_e32 v149, 0xffff0000, v72
	v_lshlrev_b32_e32 v147, 16, v72
	v_mul_f32_e32 v149, v149, v149
	v_fmac_f32_e32 v149, v147, v147
	v_add_f32_e32 v145, v149, v145
	v_and_b32_e32 v149, 0xffff0000, v73
	ds_read_b128 v[210:213], v174 offset:896
	ds_read_b128 v[214:217], v174 offset:33920
	ds_read_b128 v[218:221], v175 offset:896
	ds_read_b128 v[222:225], v175 offset:33920
	ds_read_b128 v[226:229], v174 offset:960
	v_lshlrev_b32_e32 v147, 16, v73
	v_mul_f32_e32 v149, v149, v149
	s_waitcnt lgkmcnt(4)
	v_mfma_f32_16x16x32_bf16 v[134:137], v[70:73], v[210:213], v[134:137]
	v_fmac_f32_e32 v149, v147, v147
	v_add_f32_e32 v145, v149, v145
	s_waitcnt vmcnt(16)
	v_and_b32_e32 v149, 0xffff0000, v66
	s_waitcnt lgkmcnt(3)
	v_mfma_f32_16x16x32_bf16 v[130:133], v[70:73], v[214:217], v[130:133]
	v_lshlrev_b32_e32 v147, 16, v66
	v_mul_f32_e32 v149, v149, v149
	v_fmac_f32_e32 v149, v147, v147
	s_waitcnt lgkmcnt(2)
	v_mfma_f32_16x16x32_bf16 v[134:137], v[70:73], v[218:221], v[134:137]
	ds_read_b128 v[218:221], v174 offset:33984
	ds_read_b128 v[214:217], v175 offset:33984
	v_add_f32_e32 v145, v149, v145
	v_and_b32_e32 v149, 0xffff0000, v67
	s_waitcnt lgkmcnt(3)
	v_mfma_f32_16x16x32_bf16 v[130:133], v[70:73], v[222:225], v[130:133]
	v_lshlrev_b32_e32 v147, 16, v67
	v_mul_f32_e32 v149, v149, v149
	v_fmac_f32_e32 v149, v147, v147
	v_add_f32_e32 v145, v149, v145
	v_and_b32_e32 v149, 0xffff0000, v68
	ds_read_b128 v[210:213], v175 offset:960
	v_lshlrev_b32_e32 v147, 16, v68
	v_mul_f32_e32 v149, v149, v149
	s_waitcnt lgkmcnt(3)
	v_mfma_f32_16x16x32_bf16 v[134:137], v[66:69], v[226:229], v[134:137]
	v_fmac_f32_e32 v149, v147, v147
	v_add_f32_e32 v145, v149, v145
	v_and_b32_e32 v149, 0xffff0000, v69
	s_waitcnt lgkmcnt(2)
	v_mfma_f32_16x16x32_bf16 v[130:133], v[66:69], v[218:221], v[130:133]
	v_lshlrev_b32_e32 v147, 16, v69
	v_mul_f32_e32 v149, v149, v149
	v_fmac_f32_e32 v149, v147, v147
	s_waitcnt lgkmcnt(0)
	v_mfma_f32_16x16x32_bf16 v[134:137], v[66:69], v[210:213], v[134:137]
	v_add_f32_e32 v145, v149, v145
	v_mfma_f32_16x16x32_bf16 v[130:133], v[66:69], v[214:217], v[130:133]
	s_waitcnt vmcnt(15)
	v_and_b32_e32 v149, 0xffff0000, v62
	v_lshlrev_b32_e32 v147, 16, v62
	v_mul_f32_e32 v149, v149, v149
	v_fmac_f32_e32 v149, v147, v147
	v_add_f32_e32 v145, v149, v145
	v_and_b32_e32 v149, 0xffff0000, v63
	v_lshlrev_b32_e32 v147, 16, v63
	v_mul_f32_e32 v149, v149, v149
	v_fmac_f32_e32 v149, v147, v147
	v_add_f32_e32 v145, v149, v145
	v_and_b32_e32 v149, 0xffff0000, v64
	v_lshlrev_b32_e32 v147, 16, v64
	v_mul_f32_e32 v149, v149, v149
	v_fmac_f32_e32 v149, v147, v147
	v_add_f32_e32 v145, v149, v145
	v_and_b32_e32 v149, 0xffff0000, v65
	ds_read_b128 v[210:213], v174 offset:1024
	ds_read_b128 v[214:217], v174 offset:34048
	ds_read_b128 v[218:221], v175 offset:1024
	ds_read_b128 v[222:225], v175 offset:34048
	ds_read_b128 v[226:229], v174 offset:1088
	v_lshlrev_b32_e32 v147, 16, v65
	v_mul_f32_e32 v149, v149, v149
	s_waitcnt lgkmcnt(4)
	v_mfma_f32_16x16x32_bf16 v[134:137], v[62:65], v[210:213], v[134:137]
	v_fmac_f32_e32 v149, v147, v147
	v_add_f32_e32 v145, v149, v145
	s_waitcnt vmcnt(14)
	v_and_b32_e32 v149, 0xffff0000, v58
	s_waitcnt lgkmcnt(3)
	v_mfma_f32_16x16x32_bf16 v[130:133], v[62:65], v[214:217], v[130:133]
	v_lshlrev_b32_e32 v147, 16, v58
	v_mul_f32_e32 v149, v149, v149
	v_fmac_f32_e32 v149, v147, v147
	s_waitcnt lgkmcnt(2)
	v_mfma_f32_16x16x32_bf16 v[134:137], v[62:65], v[218:221], v[134:137]
	ds_read_b128 v[218:221], v174 offset:34112
	ds_read_b128 v[214:217], v175 offset:34112
	v_add_f32_e32 v145, v149, v145
	v_and_b32_e32 v149, 0xffff0000, v59
	s_waitcnt lgkmcnt(3)
	v_mfma_f32_16x16x32_bf16 v[130:133], v[62:65], v[222:225], v[130:133]
	v_lshlrev_b32_e32 v147, 16, v59
	v_mul_f32_e32 v149, v149, v149
	v_fmac_f32_e32 v149, v147, v147
	v_add_f32_e32 v145, v149, v145
	v_and_b32_e32 v149, 0xffff0000, v60
	ds_read_b128 v[210:213], v175 offset:1088
	v_lshlrev_b32_e32 v147, 16, v60
	v_mul_f32_e32 v149, v149, v149
	s_waitcnt lgkmcnt(3)
	v_mfma_f32_16x16x32_bf16 v[134:137], v[58:61], v[226:229], v[134:137]
	v_fmac_f32_e32 v149, v147, v147
	v_add_f32_e32 v145, v149, v145
	v_and_b32_e32 v149, 0xffff0000, v61
	s_waitcnt lgkmcnt(2)
	v_mfma_f32_16x16x32_bf16 v[130:133], v[58:61], v[218:221], v[130:133]
	v_lshlrev_b32_e32 v147, 16, v61
	v_mul_f32_e32 v149, v149, v149
	v_fmac_f32_e32 v149, v147, v147
	s_waitcnt lgkmcnt(0)
	v_mfma_f32_16x16x32_bf16 v[134:137], v[58:61], v[210:213], v[134:137]
	v_add_f32_e32 v145, v149, v145
	v_mfma_f32_16x16x32_bf16 v[130:133], v[58:61], v[214:217], v[130:133]
	s_waitcnt vmcnt(13)
	v_and_b32_e32 v149, 0xffff0000, v54
	v_lshlrev_b32_e32 v147, 16, v54
	v_mul_f32_e32 v149, v149, v149
	v_fmac_f32_e32 v149, v147, v147
	v_add_f32_e32 v145, v149, v145
	v_and_b32_e32 v149, 0xffff0000, v55
	v_lshlrev_b32_e32 v147, 16, v55
	v_mul_f32_e32 v149, v149, v149
	v_fmac_f32_e32 v149, v147, v147
	v_add_f32_e32 v145, v149, v145
	v_and_b32_e32 v149, 0xffff0000, v56
	v_lshlrev_b32_e32 v147, 16, v56
	v_mul_f32_e32 v149, v149, v149
	v_fmac_f32_e32 v149, v147, v147
	v_add_f32_e32 v145, v149, v145
	v_and_b32_e32 v149, 0xffff0000, v57
	ds_read_b128 v[210:213], v174 offset:1152
	ds_read_b128 v[214:217], v174 offset:34176
	ds_read_b128 v[218:221], v175 offset:1152
	ds_read_b128 v[222:225], v175 offset:34176
	ds_read_b128 v[226:229], v174 offset:1216
	v_lshlrev_b32_e32 v147, 16, v57
	v_mul_f32_e32 v149, v149, v149
	s_waitcnt lgkmcnt(4)
	v_mfma_f32_16x16x32_bf16 v[134:137], v[54:57], v[210:213], v[134:137]
	v_fmac_f32_e32 v149, v147, v147
	v_add_f32_e32 v145, v149, v145
	s_waitcnt vmcnt(12)
	v_and_b32_e32 v149, 0xffff0000, v50
	s_waitcnt lgkmcnt(3)
	v_mfma_f32_16x16x32_bf16 v[130:133], v[54:57], v[214:217], v[130:133]
	v_lshlrev_b32_e32 v147, 16, v50
	v_mul_f32_e32 v149, v149, v149
	v_fmac_f32_e32 v149, v147, v147
	s_waitcnt lgkmcnt(2)
	v_mfma_f32_16x16x32_bf16 v[134:137], v[54:57], v[218:221], v[134:137]
	ds_read_b128 v[218:221], v174 offset:34240
	ds_read_b128 v[214:217], v175 offset:34240
	v_add_f32_e32 v145, v149, v145
	v_and_b32_e32 v149, 0xffff0000, v51
	s_waitcnt lgkmcnt(3)
	v_mfma_f32_16x16x32_bf16 v[130:133], v[54:57], v[222:225], v[130:133]
	v_lshlrev_b32_e32 v147, 16, v51
	v_mul_f32_e32 v149, v149, v149
	v_fmac_f32_e32 v149, v147, v147
	v_add_f32_e32 v145, v149, v145
	v_and_b32_e32 v149, 0xffff0000, v52
	ds_read_b128 v[210:213], v175 offset:1216
	v_lshlrev_b32_e32 v147, 16, v52
	v_mul_f32_e32 v149, v149, v149
	s_waitcnt lgkmcnt(3)
	v_mfma_f32_16x16x32_bf16 v[134:137], v[50:53], v[226:229], v[134:137]
	v_fmac_f32_e32 v149, v147, v147
	v_add_f32_e32 v145, v149, v145
	v_and_b32_e32 v149, 0xffff0000, v53
	s_waitcnt lgkmcnt(2)
	v_mfma_f32_16x16x32_bf16 v[130:133], v[50:53], v[218:221], v[130:133]
	v_lshlrev_b32_e32 v147, 16, v53
	v_mul_f32_e32 v149, v149, v149
	v_fmac_f32_e32 v149, v147, v147
	s_waitcnt lgkmcnt(0)
	v_mfma_f32_16x16x32_bf16 v[134:137], v[50:53], v[210:213], v[134:137]
	v_add_f32_e32 v145, v149, v145
	v_mfma_f32_16x16x32_bf16 v[130:133], v[50:53], v[214:217], v[130:133]
	s_waitcnt vmcnt(11)
	v_and_b32_e32 v149, 0xffff0000, v46
	v_lshlrev_b32_e32 v147, 16, v46
	v_mul_f32_e32 v149, v149, v149
	v_fmac_f32_e32 v149, v147, v147
	v_add_f32_e32 v145, v149, v145
	v_and_b32_e32 v149, 0xffff0000, v47
	v_lshlrev_b32_e32 v147, 16, v47
	v_mul_f32_e32 v149, v149, v149
	v_fmac_f32_e32 v149, v147, v147
	v_add_f32_e32 v145, v149, v145
	v_and_b32_e32 v149, 0xffff0000, v48
	v_lshlrev_b32_e32 v147, 16, v48
	v_mul_f32_e32 v149, v149, v149
	v_fmac_f32_e32 v149, v147, v147
	v_add_f32_e32 v145, v149, v145
	v_and_b32_e32 v149, 0xffff0000, v49
	ds_read_b128 v[210:213], v174 offset:1280
	ds_read_b128 v[214:217], v174 offset:34304
	ds_read_b128 v[218:221], v175 offset:1280
	ds_read_b128 v[222:225], v175 offset:34304
	ds_read_b128 v[226:229], v174 offset:1344
	v_lshlrev_b32_e32 v147, 16, v49
	v_mul_f32_e32 v149, v149, v149
	s_waitcnt lgkmcnt(4)
	v_mfma_f32_16x16x32_bf16 v[134:137], v[46:49], v[210:213], v[134:137]
	v_fmac_f32_e32 v149, v147, v147
	v_add_f32_e32 v145, v149, v145
	s_waitcnt vmcnt(10)
	v_and_b32_e32 v149, 0xffff0000, v42
	s_waitcnt lgkmcnt(3)
	v_mfma_f32_16x16x32_bf16 v[130:133], v[46:49], v[214:217], v[130:133]
	v_lshlrev_b32_e32 v147, 16, v42
	v_mul_f32_e32 v149, v149, v149
	v_fmac_f32_e32 v149, v147, v147
	s_waitcnt lgkmcnt(2)
	v_mfma_f32_16x16x32_bf16 v[134:137], v[46:49], v[218:221], v[134:137]
	ds_read_b128 v[218:221], v174 offset:34368
	ds_read_b128 v[214:217], v175 offset:34368
	v_add_f32_e32 v145, v149, v145
	v_and_b32_e32 v149, 0xffff0000, v43
	s_waitcnt lgkmcnt(3)
	v_mfma_f32_16x16x32_bf16 v[130:133], v[46:49], v[222:225], v[130:133]
	v_lshlrev_b32_e32 v147, 16, v43
	v_mul_f32_e32 v149, v149, v149
	v_fmac_f32_e32 v149, v147, v147
	v_add_f32_e32 v145, v149, v145
	v_and_b32_e32 v149, 0xffff0000, v44
	ds_read_b128 v[210:213], v175 offset:1344
	v_lshlrev_b32_e32 v147, 16, v44
	v_mul_f32_e32 v149, v149, v149
	s_waitcnt lgkmcnt(3)
	v_mfma_f32_16x16x32_bf16 v[134:137], v[42:45], v[226:229], v[134:137]
	v_fmac_f32_e32 v149, v147, v147
	v_add_f32_e32 v145, v149, v145
	v_and_b32_e32 v149, 0xffff0000, v45
	s_waitcnt lgkmcnt(2)
	v_mfma_f32_16x16x32_bf16 v[130:133], v[42:45], v[218:221], v[130:133]
	v_lshlrev_b32_e32 v147, 16, v45
	v_mul_f32_e32 v149, v149, v149
	v_fmac_f32_e32 v149, v147, v147
	s_waitcnt lgkmcnt(0)
	v_mfma_f32_16x16x32_bf16 v[134:137], v[42:45], v[210:213], v[134:137]
	v_add_f32_e32 v145, v149, v145
	v_mfma_f32_16x16x32_bf16 v[130:133], v[42:45], v[214:217], v[130:133]
	s_waitcnt vmcnt(9)
	v_and_b32_e32 v149, 0xffff0000, v38
	v_lshlrev_b32_e32 v147, 16, v38
	v_mul_f32_e32 v149, v149, v149
	v_fmac_f32_e32 v149, v147, v147
	v_add_f32_e32 v145, v149, v145
	v_and_b32_e32 v149, 0xffff0000, v39
	v_lshlrev_b32_e32 v147, 16, v39
	v_mul_f32_e32 v149, v149, v149
	v_fmac_f32_e32 v149, v147, v147
	v_add_f32_e32 v145, v149, v145
	v_and_b32_e32 v149, 0xffff0000, v40
	v_lshlrev_b32_e32 v147, 16, v40
	v_mul_f32_e32 v149, v149, v149
	v_fmac_f32_e32 v149, v147, v147
	v_add_f32_e32 v145, v149, v145
	v_and_b32_e32 v149, 0xffff0000, v41
	ds_read_b128 v[210:213], v174 offset:1408
	ds_read_b128 v[214:217], v174 offset:34432
	ds_read_b128 v[218:221], v175 offset:1408
	ds_read_b128 v[222:225], v175 offset:34432
	ds_read_b128 v[226:229], v174 offset:1472
	v_lshlrev_b32_e32 v147, 16, v41
	v_mul_f32_e32 v149, v149, v149
	s_waitcnt lgkmcnt(4)
	v_mfma_f32_16x16x32_bf16 v[134:137], v[38:41], v[210:213], v[134:137]
	v_fmac_f32_e32 v149, v147, v147
	v_add_f32_e32 v145, v149, v145
	s_waitcnt vmcnt(8)
	v_and_b32_e32 v149, 0xffff0000, v34
	s_waitcnt lgkmcnt(3)
	v_mfma_f32_16x16x32_bf16 v[130:133], v[38:41], v[214:217], v[130:133]
	v_lshlrev_b32_e32 v147, 16, v34
	v_mul_f32_e32 v149, v149, v149
	v_fmac_f32_e32 v149, v147, v147
	s_waitcnt lgkmcnt(2)
	v_mfma_f32_16x16x32_bf16 v[134:137], v[38:41], v[218:221], v[134:137]
	ds_read_b128 v[218:221], v174 offset:34496
	ds_read_b128 v[214:217], v175 offset:34496
	v_add_f32_e32 v145, v149, v145
	v_and_b32_e32 v149, 0xffff0000, v35
	s_waitcnt lgkmcnt(3)
	v_mfma_f32_16x16x32_bf16 v[130:133], v[38:41], v[222:225], v[130:133]
	v_lshlrev_b32_e32 v147, 16, v35
	v_mul_f32_e32 v149, v149, v149
	v_fmac_f32_e32 v149, v147, v147
	v_add_f32_e32 v145, v149, v145
	v_and_b32_e32 v149, 0xffff0000, v36
	ds_read_b128 v[210:213], v175 offset:1472
	v_lshlrev_b32_e32 v147, 16, v36
	v_mul_f32_e32 v149, v149, v149
	s_waitcnt lgkmcnt(3)
	v_mfma_f32_16x16x32_bf16 v[134:137], v[34:37], v[226:229], v[134:137]
	v_fmac_f32_e32 v149, v147, v147
	v_add_f32_e32 v145, v149, v145
	v_and_b32_e32 v149, 0xffff0000, v37
	s_waitcnt lgkmcnt(2)
	v_mfma_f32_16x16x32_bf16 v[130:133], v[34:37], v[218:221], v[130:133]
	v_lshlrev_b32_e32 v147, 16, v37
	v_mul_f32_e32 v149, v149, v149
	v_fmac_f32_e32 v149, v147, v147
	s_waitcnt lgkmcnt(0)
	v_mfma_f32_16x16x32_bf16 v[134:137], v[34:37], v[210:213], v[134:137]
	v_add_f32_e32 v145, v149, v145
	v_mfma_f32_16x16x32_bf16 v[130:133], v[34:37], v[214:217], v[130:133]
	s_waitcnt vmcnt(7)
	v_and_b32_e32 v149, 0xffff0000, v30
	v_lshlrev_b32_e32 v147, 16, v30
	v_mul_f32_e32 v149, v149, v149
	v_fmac_f32_e32 v149, v147, v147
	v_add_f32_e32 v145, v149, v145
	v_and_b32_e32 v149, 0xffff0000, v31
	v_lshlrev_b32_e32 v147, 16, v31
	v_mul_f32_e32 v149, v149, v149
	v_fmac_f32_e32 v149, v147, v147
	v_add_f32_e32 v145, v149, v145
	v_and_b32_e32 v149, 0xffff0000, v32
	v_lshlrev_b32_e32 v147, 16, v32
	v_mul_f32_e32 v149, v149, v149
	v_fmac_f32_e32 v149, v147, v147
	v_add_f32_e32 v145, v149, v145
	v_and_b32_e32 v149, 0xffff0000, v33
	ds_read_b128 v[210:213], v174 offset:1536
	ds_read_b128 v[214:217], v174 offset:34560
	ds_read_b128 v[218:221], v175 offset:1536
	ds_read_b128 v[222:225], v175 offset:34560
	ds_read_b128 v[226:229], v174 offset:1600
	v_lshlrev_b32_e32 v147, 16, v33
	v_mul_f32_e32 v149, v149, v149
	s_waitcnt lgkmcnt(4)
	v_mfma_f32_16x16x32_bf16 v[134:137], v[30:33], v[210:213], v[134:137]
	v_fmac_f32_e32 v149, v147, v147
	v_add_f32_e32 v145, v149, v145
	s_waitcnt vmcnt(6)
	v_and_b32_e32 v149, 0xffff0000, v26
	s_waitcnt lgkmcnt(3)
	v_mfma_f32_16x16x32_bf16 v[130:133], v[30:33], v[214:217], v[130:133]
	v_lshlrev_b32_e32 v147, 16, v26
	v_mul_f32_e32 v149, v149, v149
	v_fmac_f32_e32 v149, v147, v147
	s_waitcnt lgkmcnt(2)
	v_mfma_f32_16x16x32_bf16 v[134:137], v[30:33], v[218:221], v[134:137]
	ds_read_b128 v[218:221], v174 offset:34624
	ds_read_b128 v[214:217], v175 offset:34624
	v_add_f32_e32 v145, v149, v145
	v_and_b32_e32 v149, 0xffff0000, v27
	s_waitcnt lgkmcnt(3)
	v_mfma_f32_16x16x32_bf16 v[130:133], v[30:33], v[222:225], v[130:133]
	v_lshlrev_b32_e32 v147, 16, v27
	v_mul_f32_e32 v149, v149, v149
	v_fmac_f32_e32 v149, v147, v147
	v_add_f32_e32 v145, v149, v145
	v_and_b32_e32 v149, 0xffff0000, v28
	ds_read_b128 v[210:213], v175 offset:1600
	v_lshlrev_b32_e32 v147, 16, v28
	v_mul_f32_e32 v149, v149, v149
	s_waitcnt lgkmcnt(3)
	v_mfma_f32_16x16x32_bf16 v[134:137], v[26:29], v[226:229], v[134:137]
	v_fmac_f32_e32 v149, v147, v147
	v_add_f32_e32 v145, v149, v145
	v_and_b32_e32 v149, 0xffff0000, v29
	s_waitcnt lgkmcnt(2)
	v_mfma_f32_16x16x32_bf16 v[130:133], v[26:29], v[218:221], v[130:133]
	v_lshlrev_b32_e32 v147, 16, v29
	v_mul_f32_e32 v149, v149, v149
	v_fmac_f32_e32 v149, v147, v147
	s_waitcnt lgkmcnt(0)
	v_mfma_f32_16x16x32_bf16 v[134:137], v[26:29], v[210:213], v[134:137]
	v_add_f32_e32 v145, v149, v145
	v_mfma_f32_16x16x32_bf16 v[130:133], v[26:29], v[214:217], v[130:133]
	s_waitcnt vmcnt(5)
	v_and_b32_e32 v149, 0xffff0000, v22
	v_lshlrev_b32_e32 v147, 16, v22
	v_mul_f32_e32 v149, v149, v149
	v_fmac_f32_e32 v149, v147, v147
	v_add_f32_e32 v145, v149, v145
	v_and_b32_e32 v149, 0xffff0000, v23
	v_lshlrev_b32_e32 v147, 16, v23
	v_mul_f32_e32 v149, v149, v149
	v_fmac_f32_e32 v149, v147, v147
	v_add_f32_e32 v145, v149, v145
	v_and_b32_e32 v149, 0xffff0000, v24
	v_lshlrev_b32_e32 v147, 16, v24
	v_mul_f32_e32 v149, v149, v149
	v_fmac_f32_e32 v149, v147, v147
	v_add_f32_e32 v145, v149, v145
	v_and_b32_e32 v149, 0xffff0000, v25
	ds_read_b128 v[210:213], v174 offset:1664
	ds_read_b128 v[214:217], v174 offset:34688
	ds_read_b128 v[218:221], v175 offset:1664
	ds_read_b128 v[222:225], v175 offset:34688
	ds_read_b128 v[226:229], v174 offset:1728
	v_lshlrev_b32_e32 v147, 16, v25
	v_mul_f32_e32 v149, v149, v149
	s_waitcnt lgkmcnt(4)
	v_mfma_f32_16x16x32_bf16 v[134:137], v[22:25], v[210:213], v[134:137]
	v_fmac_f32_e32 v149, v147, v147
	v_add_f32_e32 v145, v149, v145
	s_waitcnt vmcnt(4)
	v_and_b32_e32 v149, 0xffff0000, v18
	s_waitcnt lgkmcnt(3)
	v_mfma_f32_16x16x32_bf16 v[130:133], v[22:25], v[214:217], v[130:133]
	v_lshlrev_b32_e32 v147, 16, v18
	v_mul_f32_e32 v149, v149, v149
	v_fmac_f32_e32 v149, v147, v147
	s_waitcnt lgkmcnt(2)
	v_mfma_f32_16x16x32_bf16 v[134:137], v[22:25], v[218:221], v[134:137]
	ds_read_b128 v[218:221], v174 offset:34752
	ds_read_b128 v[214:217], v175 offset:34752
	v_add_f32_e32 v145, v149, v145
	v_and_b32_e32 v149, 0xffff0000, v19
	s_waitcnt lgkmcnt(3)
	v_mfma_f32_16x16x32_bf16 v[130:133], v[22:25], v[222:225], v[130:133]
	v_lshlrev_b32_e32 v147, 16, v19
	v_mul_f32_e32 v149, v149, v149
	v_fmac_f32_e32 v149, v147, v147
	v_add_f32_e32 v145, v149, v145
	v_and_b32_e32 v149, 0xffff0000, v20
	ds_read_b128 v[210:213], v175 offset:1728
	v_lshlrev_b32_e32 v147, 16, v20
	v_mul_f32_e32 v149, v149, v149
	s_waitcnt lgkmcnt(3)
	v_mfma_f32_16x16x32_bf16 v[134:137], v[18:21], v[226:229], v[134:137]
	v_fmac_f32_e32 v149, v147, v147
	v_add_f32_e32 v145, v149, v145
	v_and_b32_e32 v149, 0xffff0000, v21
	s_waitcnt lgkmcnt(2)
	v_mfma_f32_16x16x32_bf16 v[130:133], v[18:21], v[218:221], v[130:133]
	v_lshlrev_b32_e32 v147, 16, v21
	v_mul_f32_e32 v149, v149, v149
	v_fmac_f32_e32 v149, v147, v147
	s_waitcnt lgkmcnt(0)
	v_mfma_f32_16x16x32_bf16 v[134:137], v[18:21], v[210:213], v[134:137]
	v_add_f32_e32 v145, v149, v145
	v_mfma_f32_16x16x32_bf16 v[130:133], v[18:21], v[214:217], v[130:133]
	s_waitcnt vmcnt(3)
	v_and_b32_e32 v149, 0xffff0000, v14
	v_lshlrev_b32_e32 v147, 16, v14
	v_mul_f32_e32 v149, v149, v149
	v_fmac_f32_e32 v149, v147, v147
	v_add_f32_e32 v145, v149, v145
	v_and_b32_e32 v149, 0xffff0000, v15
	v_lshlrev_b32_e32 v147, 16, v15
	v_mul_f32_e32 v149, v149, v149
	v_fmac_f32_e32 v149, v147, v147
	v_add_f32_e32 v145, v149, v145
	v_and_b32_e32 v149, 0xffff0000, v16
	v_lshlrev_b32_e32 v147, 16, v16
	v_mul_f32_e32 v149, v149, v149
	v_fmac_f32_e32 v149, v147, v147
	v_add_f32_e32 v145, v149, v145
	v_and_b32_e32 v149, 0xffff0000, v17
	ds_read_b128 v[210:213], v174 offset:1792
	ds_read_b128 v[214:217], v174 offset:34816
	ds_read_b128 v[218:221], v175 offset:1792
	ds_read_b128 v[222:225], v175 offset:34816
	ds_read_b128 v[226:229], v174 offset:1856
	v_lshlrev_b32_e32 v147, 16, v17
	v_mul_f32_e32 v149, v149, v149
	s_waitcnt lgkmcnt(4)
	v_mfma_f32_16x16x32_bf16 v[134:137], v[14:17], v[210:213], v[134:137]
	v_fmac_f32_e32 v149, v147, v147
	v_add_f32_e32 v145, v149, v145
	s_waitcnt vmcnt(2)
	v_and_b32_e32 v149, 0xffff0000, v10
	s_waitcnt lgkmcnt(3)
	v_mfma_f32_16x16x32_bf16 v[130:133], v[14:17], v[214:217], v[130:133]
	v_lshlrev_b32_e32 v147, 16, v10
	v_mul_f32_e32 v149, v149, v149
	v_fmac_f32_e32 v149, v147, v147
	s_waitcnt lgkmcnt(2)
	v_mfma_f32_16x16x32_bf16 v[134:137], v[14:17], v[218:221], v[134:137]
	ds_read_b128 v[218:221], v174 offset:34880
	ds_read_b128 v[214:217], v175 offset:34880
	v_add_f32_e32 v145, v149, v145
	v_and_b32_e32 v149, 0xffff0000, v11
	s_waitcnt lgkmcnt(3)
	v_mfma_f32_16x16x32_bf16 v[130:133], v[14:17], v[222:225], v[130:133]
	v_lshlrev_b32_e32 v147, 16, v11
	v_mul_f32_e32 v149, v149, v149
	v_fmac_f32_e32 v149, v147, v147
	v_add_f32_e32 v145, v149, v145
	v_and_b32_e32 v149, 0xffff0000, v12
	ds_read_b128 v[210:213], v175 offset:1856
	v_lshlrev_b32_e32 v147, 16, v12
	v_mul_f32_e32 v149, v149, v149
	s_waitcnt lgkmcnt(3)
	v_mfma_f32_16x16x32_bf16 v[134:137], v[10:13], v[226:229], v[134:137]
	v_fmac_f32_e32 v149, v147, v147
	v_add_f32_e32 v145, v149, v145
	v_and_b32_e32 v149, 0xffff0000, v13
	s_waitcnt lgkmcnt(2)
	v_mfma_f32_16x16x32_bf16 v[130:133], v[10:13], v[218:221], v[130:133]
	v_lshlrev_b32_e32 v147, 16, v13
	v_mul_f32_e32 v149, v149, v149
	v_fmac_f32_e32 v149, v147, v147
	s_waitcnt lgkmcnt(0)
	v_mfma_f32_16x16x32_bf16 v[134:137], v[10:13], v[210:213], v[134:137]
	v_add_f32_e32 v145, v149, v145
	v_mfma_f32_16x16x32_bf16 v[130:133], v[10:13], v[214:217], v[130:133]
	s_waitcnt vmcnt(1)
	v_and_b32_e32 v149, 0xffff0000, v6
	ds_read_b128 v[210:213], v174 offset:1920
	ds_read_b128 v[214:217], v174 offset:34944
	ds_read_b128 v[218:221], v175 offset:1920
	ds_read_b128 v[222:225], v175 offset:34944
	ds_read_b128 v[226:229], v174 offset:1984
	v_lshlrev_b32_e32 v147, 16, v6
	v_mul_f32_e32 v149, v149, v149
	s_waitcnt lgkmcnt(4)
	v_mfma_f32_16x16x32_bf16 v[134:137], v[6:9], v[210:213], v[134:137]
	v_fmac_f32_e32 v149, v147, v147
	v_add_f32_e32 v145, v149, v145
	v_and_b32_e32 v149, 0xffff0000, v7
	v_lshlrev_b32_e32 v147, 16, v7
	v_mul_f32_e32 v149, v149, v149
	v_fmac_f32_e32 v149, v147, v147
	s_waitcnt lgkmcnt(2)
	v_mfma_f32_16x16x32_bf16 v[134:137], v[6:9], v[218:221], v[134:137]
	v_add_f32_e32 v145, v149, v145
	v_and_b32_e32 v149, 0xffff0000, v8
	v_lshlrev_b32_e32 v147, 16, v8
	v_mfma_f32_16x16x32_bf16 v[130:133], v[6:9], v[214:217], v[130:133]
	v_mul_f32_e32 v149, v149, v149
	v_fmac_f32_e32 v149, v147, v147
	v_add_f32_e32 v145, v149, v145
	v_and_b32_e32 v149, 0xffff0000, v9
	s_waitcnt lgkmcnt(1)
	v_mfma_f32_16x16x32_bf16 v[222:225], v[6:9], v[222:225], v[130:133]
	v_lshlrev_b32_e32 v147, 16, v9
	ds_read_b128 v[218:221], v174 offset:35008
	ds_read_b128 v[214:217], v175 offset:35008
	s_waitcnt vmcnt(0) lgkmcnt(2)
	v_mfma_f32_16x16x32_bf16 v[130:133], v[2:5], v[226:229], v[134:137]
	ds_read_b128 v[210:213], v175 offset:1984
	s_nop 1
	v_mul_f32_e32 v134, v149, v149
	v_and_b32_e32 v136, 0xffff0000, v2
	v_fmac_f32_e32 v134, v147, v147
	v_lshlrev_b32_e32 v135, 16, v2
	v_mul_f32_e32 v136, v136, v136
	v_add_f32_e32 v134, v134, v145
	v_fmac_f32_e32 v136, v135, v135
	v_add_f32_e32 v134, v136, v134
	v_and_b32_e32 v136, 0xffff0000, v3
	v_lshlrev_b32_e32 v135, 16, v3
	v_mul_f32_e32 v136, v136, v136
	v_fmac_f32_e32 v136, v135, v135
	v_add_f32_e32 v134, v136, v134
	v_and_b32_e32 v136, 0xffff0000, v4
	v_lshlrev_b32_e32 v135, 16, v4
	v_mul_f32_e32 v136, v136, v136
	v_fmac_f32_e32 v136, v135, v135
	v_add_f32_e32 v145, v136, v134
	s_waitcnt lgkmcnt(2)
	v_mfma_f32_16x16x32_bf16 v[134:137], v[2:5], v[218:221], v[222:225]
	v_and_b32_e32 v149, 0xffff0000, v5
	v_lshlrev_b32_e32 v147, 16, v5
	v_mul_f32_e32 v149, v149, v149
	v_fmac_f32_e32 v149, v147, v147
	s_waitcnt lgkmcnt(0)
	v_mfma_f32_16x16x32_bf16 v[130:133], v[2:5], v[210:213], v[130:133]
	v_add_f32_e32 v145, v149, v145
	v_mfma_f32_16x16x32_bf16 v[134:137], v[2:5], v[214:217], v[134:137]
	ds_bpermute_b32 v147, v192, v145
	v_lshlrev_b32_e32 v149, 16, v126
	v_and_b32_e32 v126, 0xffff0000, v126
	s_waitcnt lgkmcnt(0)
	v_add_f32_e32 v145, v145, v147
	ds_bpermute_b32 v147, v193, v145
	s_waitcnt lgkmcnt(0)
	v_add_f32_e32 v145, v145, v147
	v_fmamk_f32 v145, v145, 0x3a800000, v195
	v_mul_f32_e32 v147, 0x4f800000, v145
	v_cmp_gt_f32_e32 vcc, s25, v145
	s_nop 1
	v_cndmask_b32_e32 v145, v145, v147, vcc
	v_sqrt_f32_e32 v147, v145
	s_nop 0
	v_add_u32_e32 v151, -1, v147
	v_add_u32_e32 v153, 1, v147
	v_fma_f32 v155, -v151, v147, v145
	v_fma_f32 v157, -v153, v147, v145
	v_cmp_ge_f32_e64 s[8:9], 0, v155
	s_nop 1
	v_cndmask_b32_e64 v147, v147, v151, s[8:9]
	v_cmp_lt_f32_e64 s[8:9], 0, v157
	s_nop 1
	v_cndmask_b32_e64 v147, v147, v153, s[8:9]
	v_mul_f32_e32 v151, 0x37800000, v147
	v_cndmask_b32_e32 v147, v147, v151, vcc
	v_cmp_class_f32_e32 vcc, v145, v196
	s_nop 1
	v_cndmask_b32_e32 v145, v147, v145, vcc
	v_div_scale_f32 v147, s[8:9], v145, v145, 1.0
	v_rcp_f32_e32 v151, v147
	v_div_scale_f32 v153, vcc, 1.0, v145, 1.0
	v_fma_f32 v155, -v147, v151, 1.0
	v_fmac_f32_e32 v151, v155, v151
	v_mul_f32_e32 v155, v153, v151
	v_fma_f32 v157, -v147, v155, v153
	v_fmac_f32_e32 v155, v157, v151
	v_fma_f32 v147, -v147, v155, v153
	v_div_fmas_f32 v147, v147, v151, v155
	v_div_fixup_f32 v145, v147, v145, 1.0
	v_mul_f32_e32 v147, 0x41800000, v145
	v_mul_f32_e32 v149, v147, v149
	v_mul_f32_e32 v126, v147, v126
	v_cvt_pk_fp8_f32 v210, v149, v126
	v_lshlrev_b32_e32 v151, 16, v127
	v_and_b32_e32 v127, 0xffff0000, v127
	v_mul_f32_e32 v126, v147, v151
	v_mul_f32_e32 v127, v147, v127
	v_cvt_pk_fp8_f32 v210, v126, v127 op_sel:[0,0,1]
	v_lshlrev_b32_e32 v126, 16, v128
	v_and_b32_e32 v127, 0xffff0000, v128
	v_mul_f32_e32 v126, v147, v126
	v_mul_f32_e32 v127, v147, v127
	v_cvt_pk_fp8_f32 v211, v126, v127
	v_lshlrev_b32_e32 v128, 16, v129
	v_and_b32_e32 v127, 0xffff0000, v129
	v_mul_f32_e32 v126, v147, v128
	v_mul_f32_e32 v127, v147, v127
	v_cvt_pk_fp8_f32 v211, v126, v127 op_sel:[0,0,1]
	v_lshl_add_u64 v[126:127], v[142:143], 0, v[168:169]
	global_store_dwordx2 v[126:127], v[210:211], off
	s_nop 0
	v_lshlrev_b32_e32 v128, 16, v122
	v_and_b32_e32 v122, 0xffff0000, v122
	v_mul_f32_e32 v128, v147, v128
	v_mul_f32_e32 v129, v147, v122
	v_cvt_pk_fp8_f32 v122, v128, v129
	v_lshlrev_b32_e32 v149, 16, v123
	v_and_b32_e32 v123, 0xffff0000, v123
	v_mul_f32_e32 v128, v147, v149
	v_mul_f32_e32 v123, v147, v123
	v_cvt_pk_fp8_f32 v122, v128, v123 op_sel:[0,0,1]
	v_lshlrev_b32_e32 v123, 16, v124
	v_mul_f32_e32 v128, v147, v123
	v_and_b32_e32 v123, 0xffff0000, v124
	v_mul_f32_e32 v124, v147, v123
	v_cvt_pk_fp8_f32 v123, v128, v124
	v_lshlrev_b32_e32 v129, 16, v125
	v_and_b32_e32 v125, 0xffff0000, v125
	v_mul_f32_e32 v124, v147, v129
	v_mul_f32_e32 v125, v147, v125
	v_cvt_pk_fp8_f32 v123, v124, v125 op_sel:[0,0,1]
	global_store_dwordx2 v[126:127], v[122:123], off offset:32
	s_nop 0
	v_lshlrev_b32_e32 v122, 16, v118
	v_and_b32_e32 v118, 0xffff0000, v118
	v_mul_f32_e32 v122, v147, v122
	v_mul_f32_e32 v123, v147, v118
	v_cvt_pk_fp8_f32 v118, v122, v123
	v_lshlrev_b32_e32 v124, 16, v119
	v_and_b32_e32 v119, 0xffff0000, v119
	v_mul_f32_e32 v122, v147, v124
	v_mul_f32_e32 v119, v147, v119
	v_cvt_pk_fp8_f32 v118, v122, v119 op_sel:[0,0,1]
	v_lshlrev_b32_e32 v119, 16, v120
	v_mul_f32_e32 v122, v147, v119
	v_and_b32_e32 v119, 0xffff0000, v120
	v_mul_f32_e32 v120, v147, v119
	v_cvt_pk_fp8_f32 v119, v122, v120
	v_lshlrev_b32_e32 v123, 16, v121
	v_and_b32_e32 v121, 0xffff0000, v121
	v_mul_f32_e32 v120, v147, v123
	v_mul_f32_e32 v121, v147, v121
	v_cvt_pk_fp8_f32 v119, v120, v121 op_sel:[0,0,1]
	global_store_dwordx2 v[126:127], v[118:119], off offset:64
	s_nop 0
	v_lshlrev_b32_e32 v118, 16, v114
	v_and_b32_e32 v114, 0xffff0000, v114
	v_mul_f32_e32 v118, v147, v118
	v_mul_f32_e32 v119, v147, v114
	v_cvt_pk_fp8_f32 v114, v118, v119
	v_lshlrev_b32_e32 v120, 16, v115
	v_and_b32_e32 v115, 0xffff0000, v115
	v_mul_f32_e32 v118, v147, v120
	v_mul_f32_e32 v115, v147, v115
	v_cvt_pk_fp8_f32 v114, v118, v115 op_sel:[0,0,1]
	v_lshlrev_b32_e32 v115, 16, v116
	v_mul_f32_e32 v118, v147, v115
	v_and_b32_e32 v115, 0xffff0000, v116
	v_mul_f32_e32 v116, v147, v115
	v_cvt_pk_fp8_f32 v115, v118, v116
	v_lshlrev_b32_e32 v119, 16, v117
	v_and_b32_e32 v117, 0xffff0000, v117
	v_mul_f32_e32 v116, v147, v119
	v_mul_f32_e32 v117, v147, v117
	v_cvt_pk_fp8_f32 v115, v116, v117 op_sel:[0,0,1]
	global_store_dwordx2 v[126:127], v[114:115], off offset:96
	s_nop 0
	v_lshlrev_b32_e32 v114, 16, v110
	v_and_b32_e32 v110, 0xffff0000, v110
	v_mul_f32_e32 v114, v147, v114
	v_mul_f32_e32 v115, v147, v110
	v_cvt_pk_fp8_f32 v110, v114, v115
	v_lshlrev_b32_e32 v116, 16, v111
	v_and_b32_e32 v111, 0xffff0000, v111
	v_mul_f32_e32 v114, v147, v116
	v_mul_f32_e32 v111, v147, v111
	v_cvt_pk_fp8_f32 v110, v114, v111 op_sel:[0,0,1]
	v_lshlrev_b32_e32 v111, 16, v112
	v_mul_f32_e32 v114, v147, v111
	v_and_b32_e32 v111, 0xffff0000, v112
	v_mul_f32_e32 v112, v147, v111
	v_cvt_pk_fp8_f32 v111, v114, v112
	v_lshlrev_b32_e32 v115, 16, v113
	v_and_b32_e32 v113, 0xffff0000, v113
	v_mul_f32_e32 v112, v147, v115
	v_mul_f32_e32 v113, v147, v113
	v_cvt_pk_fp8_f32 v111, v112, v113 op_sel:[0,0,1]
	global_store_dwordx2 v[126:127], v[110:111], off offset:128
	s_nop 0
	v_lshlrev_b32_e32 v110, 16, v106
	v_and_b32_e32 v106, 0xffff0000, v106
	v_mul_f32_e32 v110, v147, v110
	v_mul_f32_e32 v111, v147, v106
	v_cvt_pk_fp8_f32 v106, v110, v111
	v_lshlrev_b32_e32 v112, 16, v107
	v_and_b32_e32 v107, 0xffff0000, v107
	v_mul_f32_e32 v110, v147, v112
	v_mul_f32_e32 v107, v147, v107
	v_cvt_pk_fp8_f32 v106, v110, v107 op_sel:[0,0,1]
	v_lshlrev_b32_e32 v107, 16, v108
	v_mul_f32_e32 v110, v147, v107
	v_and_b32_e32 v107, 0xffff0000, v108
	v_mul_f32_e32 v108, v147, v107
	v_cvt_pk_fp8_f32 v107, v110, v108
	v_lshlrev_b32_e32 v111, 16, v109
	v_and_b32_e32 v109, 0xffff0000, v109
	v_mul_f32_e32 v108, v147, v111
	v_mul_f32_e32 v109, v147, v109
	v_cvt_pk_fp8_f32 v107, v108, v109 op_sel:[0,0,1]
	global_store_dwordx2 v[126:127], v[106:107], off offset:160
	s_nop 0
	v_lshlrev_b32_e32 v106, 16, v102
	v_and_b32_e32 v102, 0xffff0000, v102
	v_mul_f32_e32 v106, v147, v106
	v_mul_f32_e32 v107, v147, v102
	v_cvt_pk_fp8_f32 v102, v106, v107
	v_lshlrev_b32_e32 v108, 16, v103
	v_and_b32_e32 v103, 0xffff0000, v103
	v_mul_f32_e32 v106, v147, v108
	v_mul_f32_e32 v103, v147, v103
	v_cvt_pk_fp8_f32 v102, v106, v103 op_sel:[0,0,1]
	v_lshlrev_b32_e32 v103, 16, v104
	v_mul_f32_e32 v106, v147, v103
	v_and_b32_e32 v103, 0xffff0000, v104
	v_mul_f32_e32 v104, v147, v103
	v_cvt_pk_fp8_f32 v103, v106, v104
	v_lshlrev_b32_e32 v107, 16, v105
	v_and_b32_e32 v105, 0xffff0000, v105
	v_mul_f32_e32 v104, v147, v107
	v_mul_f32_e32 v105, v147, v105
	v_cvt_pk_fp8_f32 v103, v104, v105 op_sel:[0,0,1]
	global_store_dwordx2 v[126:127], v[102:103], off offset:192
	s_nop 0
	v_lshlrev_b32_e32 v102, 16, v98
	v_and_b32_e32 v98, 0xffff0000, v98
	v_mul_f32_e32 v102, v147, v102
	v_mul_f32_e32 v103, v147, v98
	v_cvt_pk_fp8_f32 v98, v102, v103
	v_lshlrev_b32_e32 v104, 16, v99
	v_and_b32_e32 v99, 0xffff0000, v99
	v_mul_f32_e32 v102, v147, v104
	v_mul_f32_e32 v99, v147, v99
	v_cvt_pk_fp8_f32 v98, v102, v99 op_sel:[0,0,1]
	v_lshlrev_b32_e32 v99, 16, v100
	v_mul_f32_e32 v102, v147, v99
	v_and_b32_e32 v99, 0xffff0000, v100
	v_mul_f32_e32 v100, v147, v99
	v_cvt_pk_fp8_f32 v99, v102, v100
	v_lshlrev_b32_e32 v103, 16, v101
	v_and_b32_e32 v101, 0xffff0000, v101
	v_mul_f32_e32 v100, v147, v103
	v_mul_f32_e32 v101, v147, v101
	v_cvt_pk_fp8_f32 v99, v100, v101 op_sel:[0,0,1]
	global_store_dwordx2 v[126:127], v[98:99], off offset:224
	s_nop 0
	v_lshlrev_b32_e32 v98, 16, v94
	v_and_b32_e32 v94, 0xffff0000, v94
	v_mul_f32_e32 v98, v147, v98
	v_mul_f32_e32 v99, v147, v94
	v_cvt_pk_fp8_f32 v94, v98, v99
	v_lshlrev_b32_e32 v100, 16, v95
	v_and_b32_e32 v95, 0xffff0000, v95
	v_mul_f32_e32 v98, v147, v100
	v_mul_f32_e32 v95, v147, v95
	v_cvt_pk_fp8_f32 v94, v98, v95 op_sel:[0,0,1]
	v_lshlrev_b32_e32 v95, 16, v96
	v_mul_f32_e32 v98, v147, v95
	v_and_b32_e32 v95, 0xffff0000, v96
	v_mul_f32_e32 v96, v147, v95
	v_cvt_pk_fp8_f32 v95, v98, v96
	v_lshlrev_b32_e32 v99, 16, v97
	v_and_b32_e32 v97, 0xffff0000, v97
	v_mul_f32_e32 v96, v147, v99
	v_mul_f32_e32 v97, v147, v97
	v_cvt_pk_fp8_f32 v95, v96, v97 op_sel:[0,0,1]
	global_store_dwordx2 v[126:127], v[94:95], off offset:256
	s_nop 0
	v_lshlrev_b32_e32 v94, 16, v90
	v_and_b32_e32 v90, 0xffff0000, v90
	v_mul_f32_e32 v94, v147, v94
	v_mul_f32_e32 v95, v147, v90
	v_cvt_pk_fp8_f32 v90, v94, v95
	v_lshlrev_b32_e32 v96, 16, v91
	v_and_b32_e32 v91, 0xffff0000, v91
	v_mul_f32_e32 v94, v147, v96
	v_mul_f32_e32 v91, v147, v91
	v_cvt_pk_fp8_f32 v90, v94, v91 op_sel:[0,0,1]
	v_lshlrev_b32_e32 v91, 16, v92
	v_mul_f32_e32 v94, v147, v91
	v_and_b32_e32 v91, 0xffff0000, v92
	v_mul_f32_e32 v92, v147, v91
	v_cvt_pk_fp8_f32 v91, v94, v92
	v_lshlrev_b32_e32 v95, 16, v93
	v_and_b32_e32 v93, 0xffff0000, v93
	v_mul_f32_e32 v92, v147, v95
	v_mul_f32_e32 v93, v147, v93
	v_cvt_pk_fp8_f32 v91, v92, v93 op_sel:[0,0,1]
	global_store_dwordx2 v[126:127], v[90:91], off offset:288
	s_nop 0
	v_lshlrev_b32_e32 v90, 16, v86
	v_and_b32_e32 v86, 0xffff0000, v86
	v_mul_f32_e32 v90, v147, v90
	v_mul_f32_e32 v91, v147, v86
	v_cvt_pk_fp8_f32 v86, v90, v91
	v_lshlrev_b32_e32 v92, 16, v87
	v_and_b32_e32 v87, 0xffff0000, v87
	v_mul_f32_e32 v90, v147, v92
	v_mul_f32_e32 v87, v147, v87
	v_cvt_pk_fp8_f32 v86, v90, v87 op_sel:[0,0,1]
	v_lshlrev_b32_e32 v87, 16, v88
	v_mul_f32_e32 v90, v147, v87
	v_and_b32_e32 v87, 0xffff0000, v88
	v_mul_f32_e32 v88, v147, v87
	v_cvt_pk_fp8_f32 v87, v90, v88
	v_lshlrev_b32_e32 v91, 16, v89
	v_and_b32_e32 v89, 0xffff0000, v89
	v_mul_f32_e32 v88, v147, v91
	v_mul_f32_e32 v89, v147, v89
	v_cvt_pk_fp8_f32 v87, v88, v89 op_sel:[0,0,1]
	global_store_dwordx2 v[126:127], v[86:87], off offset:320
	s_nop 0
	v_lshlrev_b32_e32 v86, 16, v82
	v_and_b32_e32 v82, 0xffff0000, v82
	v_mul_f32_e32 v86, v147, v86
	v_mul_f32_e32 v87, v147, v82
	v_cvt_pk_fp8_f32 v82, v86, v87
	v_lshlrev_b32_e32 v88, 16, v83
	v_and_b32_e32 v83, 0xffff0000, v83
	v_mul_f32_e32 v86, v147, v88
	v_mul_f32_e32 v83, v147, v83
	v_cvt_pk_fp8_f32 v82, v86, v83 op_sel:[0,0,1]
	v_lshlrev_b32_e32 v83, 16, v84
	v_mul_f32_e32 v86, v147, v83
	v_and_b32_e32 v83, 0xffff0000, v84
	v_mul_f32_e32 v84, v147, v83
	v_cvt_pk_fp8_f32 v83, v86, v84
	v_lshlrev_b32_e32 v87, 16, v85
	v_and_b32_e32 v85, 0xffff0000, v85
	v_mul_f32_e32 v84, v147, v87
	v_mul_f32_e32 v85, v147, v85
	v_cvt_pk_fp8_f32 v83, v84, v85 op_sel:[0,0,1]
	global_store_dwordx2 v[126:127], v[82:83], off offset:352
	s_nop 0
	v_lshlrev_b32_e32 v82, 16, v78
	v_and_b32_e32 v78, 0xffff0000, v78
	v_mul_f32_e32 v82, v147, v82
	v_mul_f32_e32 v83, v147, v78
	v_cvt_pk_fp8_f32 v78, v82, v83
	v_lshlrev_b32_e32 v84, 16, v79
	v_and_b32_e32 v79, 0xffff0000, v79
	v_mul_f32_e32 v82, v147, v84
	v_mul_f32_e32 v79, v147, v79
	v_cvt_pk_fp8_f32 v78, v82, v79 op_sel:[0,0,1]
	v_lshlrev_b32_e32 v79, 16, v80
	v_mul_f32_e32 v82, v147, v79
	v_and_b32_e32 v79, 0xffff0000, v80
	v_mul_f32_e32 v80, v147, v79
	v_cvt_pk_fp8_f32 v79, v82, v80
	v_lshlrev_b32_e32 v83, 16, v81
	v_and_b32_e32 v81, 0xffff0000, v81
	v_mul_f32_e32 v80, v147, v83
	v_mul_f32_e32 v81, v147, v81
	v_cvt_pk_fp8_f32 v79, v80, v81 op_sel:[0,0,1]
	global_store_dwordx2 v[126:127], v[78:79], off offset:384
	s_nop 0
	v_lshlrev_b32_e32 v78, 16, v74
	v_and_b32_e32 v74, 0xffff0000, v74
	v_mul_f32_e32 v78, v147, v78
	v_mul_f32_e32 v79, v147, v74
	v_cvt_pk_fp8_f32 v74, v78, v79
	v_lshlrev_b32_e32 v80, 16, v75
	v_and_b32_e32 v75, 0xffff0000, v75
	v_mul_f32_e32 v78, v147, v80
	v_mul_f32_e32 v75, v147, v75
	v_cvt_pk_fp8_f32 v74, v78, v75 op_sel:[0,0,1]
	v_lshlrev_b32_e32 v75, 16, v76
	v_mul_f32_e32 v78, v147, v75
	v_and_b32_e32 v75, 0xffff0000, v76
	v_mul_f32_e32 v76, v147, v75
	v_cvt_pk_fp8_f32 v75, v78, v76
	v_lshlrev_b32_e32 v79, 16, v77
	v_and_b32_e32 v77, 0xffff0000, v77
	v_mul_f32_e32 v76, v147, v79
	v_mul_f32_e32 v77, v147, v77
	v_cvt_pk_fp8_f32 v75, v76, v77 op_sel:[0,0,1]
	global_store_dwordx2 v[126:127], v[74:75], off offset:416
	s_nop 0
	v_lshlrev_b32_e32 v74, 16, v70
	v_and_b32_e32 v70, 0xffff0000, v70
	v_mul_f32_e32 v74, v147, v74
	v_mul_f32_e32 v75, v147, v70
	v_cvt_pk_fp8_f32 v70, v74, v75
	v_lshlrev_b32_e32 v76, 16, v71
	v_and_b32_e32 v71, 0xffff0000, v71
	v_mul_f32_e32 v74, v147, v76
	v_mul_f32_e32 v71, v147, v71
	v_cvt_pk_fp8_f32 v70, v74, v71 op_sel:[0,0,1]
	v_lshlrev_b32_e32 v71, 16, v72
	v_mul_f32_e32 v74, v147, v71
	v_and_b32_e32 v71, 0xffff0000, v72
	v_mul_f32_e32 v72, v147, v71
	v_cvt_pk_fp8_f32 v71, v74, v72
	v_lshlrev_b32_e32 v75, 16, v73
	v_and_b32_e32 v73, 0xffff0000, v73
	v_mul_f32_e32 v72, v147, v75
	v_mul_f32_e32 v73, v147, v73
	v_cvt_pk_fp8_f32 v71, v72, v73 op_sel:[0,0,1]
	global_store_dwordx2 v[126:127], v[70:71], off offset:448
	s_nop 0
	v_lshlrev_b32_e32 v70, 16, v66
	v_and_b32_e32 v66, 0xffff0000, v66
	v_mul_f32_e32 v70, v147, v70
	v_mul_f32_e32 v71, v147, v66
	v_cvt_pk_fp8_f32 v66, v70, v71
	v_lshlrev_b32_e32 v72, 16, v67
	v_and_b32_e32 v67, 0xffff0000, v67
	v_mul_f32_e32 v70, v147, v72
	v_mul_f32_e32 v67, v147, v67
	v_cvt_pk_fp8_f32 v66, v70, v67 op_sel:[0,0,1]
	v_lshlrev_b32_e32 v67, 16, v68
	v_mul_f32_e32 v70, v147, v67
	v_and_b32_e32 v67, 0xffff0000, v68
	v_mul_f32_e32 v68, v147, v67
	v_cvt_pk_fp8_f32 v67, v70, v68
	v_lshlrev_b32_e32 v71, 16, v69
	v_and_b32_e32 v69, 0xffff0000, v69
	v_mul_f32_e32 v68, v147, v71
	v_mul_f32_e32 v69, v147, v69
	v_cvt_pk_fp8_f32 v67, v68, v69 op_sel:[0,0,1]
	global_store_dwordx2 v[126:127], v[66:67], off offset:480
	s_nop 0
	v_lshlrev_b32_e32 v66, 16, v62
	v_and_b32_e32 v62, 0xffff0000, v62
	v_mul_f32_e32 v66, v147, v66
	v_mul_f32_e32 v67, v147, v62
	v_cvt_pk_fp8_f32 v62, v66, v67
	v_lshlrev_b32_e32 v68, 16, v63
	v_and_b32_e32 v63, 0xffff0000, v63
	v_mul_f32_e32 v66, v147, v68
	v_mul_f32_e32 v63, v147, v63
	v_cvt_pk_fp8_f32 v62, v66, v63 op_sel:[0,0,1]
	v_lshlrev_b32_e32 v63, 16, v64
	v_mul_f32_e32 v66, v147, v63
	v_and_b32_e32 v63, 0xffff0000, v64
	v_mul_f32_e32 v64, v147, v63
	v_cvt_pk_fp8_f32 v63, v66, v64
	v_lshlrev_b32_e32 v67, 16, v65
	v_and_b32_e32 v65, 0xffff0000, v65
	v_mul_f32_e32 v64, v147, v67
	v_mul_f32_e32 v65, v147, v65
	v_cvt_pk_fp8_f32 v63, v64, v65 op_sel:[0,0,1]
	global_store_dwordx2 v[126:127], v[62:63], off offset:512
	s_nop 0
	v_lshlrev_b32_e32 v62, 16, v58
	v_and_b32_e32 v58, 0xffff0000, v58
	v_mul_f32_e32 v62, v147, v62
	v_mul_f32_e32 v63, v147, v58
	v_cvt_pk_fp8_f32 v58, v62, v63
	v_lshlrev_b32_e32 v64, 16, v59
	v_and_b32_e32 v59, 0xffff0000, v59
	v_mul_f32_e32 v62, v147, v64
	v_mul_f32_e32 v59, v147, v59
	v_cvt_pk_fp8_f32 v58, v62, v59 op_sel:[0,0,1]
	v_lshlrev_b32_e32 v59, 16, v60
	v_mul_f32_e32 v62, v147, v59
	v_and_b32_e32 v59, 0xffff0000, v60
	v_mul_f32_e32 v60, v147, v59
	v_cvt_pk_fp8_f32 v59, v62, v60
	v_lshlrev_b32_e32 v63, 16, v61
	v_and_b32_e32 v61, 0xffff0000, v61
	v_mul_f32_e32 v60, v147, v63
	v_mul_f32_e32 v61, v147, v61
	v_cvt_pk_fp8_f32 v59, v60, v61 op_sel:[0,0,1]
	global_store_dwordx2 v[126:127], v[58:59], off offset:544
	s_nop 0
	v_lshlrev_b32_e32 v58, 16, v54
	v_and_b32_e32 v54, 0xffff0000, v54
	v_mul_f32_e32 v58, v147, v58
	v_mul_f32_e32 v59, v147, v54
	v_cvt_pk_fp8_f32 v54, v58, v59
	v_lshlrev_b32_e32 v60, 16, v55
	v_and_b32_e32 v55, 0xffff0000, v55
	v_mul_f32_e32 v58, v147, v60
	v_mul_f32_e32 v55, v147, v55
	v_cvt_pk_fp8_f32 v54, v58, v55 op_sel:[0,0,1]
	v_lshlrev_b32_e32 v55, 16, v56
	v_mul_f32_e32 v58, v147, v55
	v_and_b32_e32 v55, 0xffff0000, v56
	v_mul_f32_e32 v56, v147, v55
	v_cvt_pk_fp8_f32 v55, v58, v56
	v_lshlrev_b32_e32 v59, 16, v57
	v_and_b32_e32 v57, 0xffff0000, v57
	v_mul_f32_e32 v56, v147, v59
	v_mul_f32_e32 v57, v147, v57
	v_cvt_pk_fp8_f32 v55, v56, v57 op_sel:[0,0,1]
	global_store_dwordx2 v[126:127], v[54:55], off offset:576
	s_nop 0
	v_lshlrev_b32_e32 v54, 16, v50
	v_and_b32_e32 v50, 0xffff0000, v50
	v_mul_f32_e32 v54, v147, v54
	v_mul_f32_e32 v55, v147, v50
	v_cvt_pk_fp8_f32 v50, v54, v55
	v_lshlrev_b32_e32 v56, 16, v51
	v_and_b32_e32 v51, 0xffff0000, v51
	v_mul_f32_e32 v54, v147, v56
	v_mul_f32_e32 v51, v147, v51
	v_cvt_pk_fp8_f32 v50, v54, v51 op_sel:[0,0,1]
	v_lshlrev_b32_e32 v51, 16, v52
	v_mul_f32_e32 v54, v147, v51
	v_and_b32_e32 v51, 0xffff0000, v52
	v_mul_f32_e32 v52, v147, v51
	v_cvt_pk_fp8_f32 v51, v54, v52
	v_lshlrev_b32_e32 v55, 16, v53
	v_and_b32_e32 v53, 0xffff0000, v53
	v_mul_f32_e32 v52, v147, v55
	v_mul_f32_e32 v53, v147, v53
	v_cvt_pk_fp8_f32 v51, v52, v53 op_sel:[0,0,1]
	global_store_dwordx2 v[126:127], v[50:51], off offset:608
	s_nop 0
	v_lshlrev_b32_e32 v50, 16, v46
	v_and_b32_e32 v46, 0xffff0000, v46
	v_mul_f32_e32 v50, v147, v50
	v_mul_f32_e32 v51, v147, v46
	v_cvt_pk_fp8_f32 v46, v50, v51
	v_lshlrev_b32_e32 v52, 16, v47
	v_and_b32_e32 v47, 0xffff0000, v47
	v_mul_f32_e32 v50, v147, v52
	v_mul_f32_e32 v47, v147, v47
	v_cvt_pk_fp8_f32 v46, v50, v47 op_sel:[0,0,1]
	v_lshlrev_b32_e32 v47, 16, v48
	v_mul_f32_e32 v50, v147, v47
	v_and_b32_e32 v47, 0xffff0000, v48
	v_mul_f32_e32 v48, v147, v47
	v_cvt_pk_fp8_f32 v47, v50, v48
	v_lshlrev_b32_e32 v51, 16, v49
	v_and_b32_e32 v49, 0xffff0000, v49
	v_mul_f32_e32 v48, v147, v51
	v_mul_f32_e32 v49, v147, v49
	v_cvt_pk_fp8_f32 v47, v48, v49 op_sel:[0,0,1]
	global_store_dwordx2 v[126:127], v[46:47], off offset:640
	s_nop 0
	v_lshlrev_b32_e32 v46, 16, v42
	v_and_b32_e32 v42, 0xffff0000, v42
	v_mul_f32_e32 v46, v147, v46
	v_mul_f32_e32 v47, v147, v42
	v_cvt_pk_fp8_f32 v42, v46, v47
	v_lshlrev_b32_e32 v48, 16, v43
	v_and_b32_e32 v43, 0xffff0000, v43
	v_mul_f32_e32 v46, v147, v48
	v_mul_f32_e32 v43, v147, v43
	v_cvt_pk_fp8_f32 v42, v46, v43 op_sel:[0,0,1]
	v_lshlrev_b32_e32 v43, 16, v44
	v_mul_f32_e32 v46, v147, v43
	v_and_b32_e32 v43, 0xffff0000, v44
	v_mul_f32_e32 v44, v147, v43
	v_cvt_pk_fp8_f32 v43, v46, v44
	v_lshlrev_b32_e32 v47, 16, v45
	v_and_b32_e32 v45, 0xffff0000, v45
	v_mul_f32_e32 v44, v147, v47
	v_mul_f32_e32 v45, v147, v45
	v_cvt_pk_fp8_f32 v43, v44, v45 op_sel:[0,0,1]
	global_store_dwordx2 v[126:127], v[42:43], off offset:672
	s_nop 0
	v_lshlrev_b32_e32 v42, 16, v38
	v_and_b32_e32 v38, 0xffff0000, v38
	v_mul_f32_e32 v42, v147, v42
	v_mul_f32_e32 v43, v147, v38
	v_cvt_pk_fp8_f32 v38, v42, v43
	v_lshlrev_b32_e32 v44, 16, v39
	v_and_b32_e32 v39, 0xffff0000, v39
	v_mul_f32_e32 v42, v147, v44
	v_mul_f32_e32 v39, v147, v39
	v_cvt_pk_fp8_f32 v38, v42, v39 op_sel:[0,0,1]
	v_lshlrev_b32_e32 v39, 16, v40
	v_mul_f32_e32 v42, v147, v39
	v_and_b32_e32 v39, 0xffff0000, v40
	v_mul_f32_e32 v40, v147, v39
	v_cvt_pk_fp8_f32 v39, v42, v40
	v_lshlrev_b32_e32 v43, 16, v41
	v_and_b32_e32 v41, 0xffff0000, v41
	v_mul_f32_e32 v40, v147, v43
	v_mul_f32_e32 v41, v147, v41
	v_cvt_pk_fp8_f32 v39, v40, v41 op_sel:[0,0,1]
	global_store_dwordx2 v[126:127], v[38:39], off offset:704
	s_nop 0
	v_lshlrev_b32_e32 v38, 16, v34
	v_and_b32_e32 v34, 0xffff0000, v34
	v_mul_f32_e32 v38, v147, v38
	v_mul_f32_e32 v39, v147, v34
	v_cvt_pk_fp8_f32 v34, v38, v39
	v_lshlrev_b32_e32 v40, 16, v35
	v_and_b32_e32 v35, 0xffff0000, v35
	v_mul_f32_e32 v38, v147, v40
	v_mul_f32_e32 v35, v147, v35
	v_cvt_pk_fp8_f32 v34, v38, v35 op_sel:[0,0,1]
	v_lshlrev_b32_e32 v35, 16, v36
	v_mul_f32_e32 v38, v147, v35
	v_and_b32_e32 v35, 0xffff0000, v36
	v_mul_f32_e32 v36, v147, v35
	v_cvt_pk_fp8_f32 v35, v38, v36
	v_lshlrev_b32_e32 v39, 16, v37
	v_and_b32_e32 v37, 0xffff0000, v37
	v_mul_f32_e32 v36, v147, v39
	v_mul_f32_e32 v37, v147, v37
	v_cvt_pk_fp8_f32 v35, v36, v37 op_sel:[0,0,1]
	global_store_dwordx2 v[126:127], v[34:35], off offset:736
	s_nop 0
	v_lshlrev_b32_e32 v34, 16, v30
	v_and_b32_e32 v30, 0xffff0000, v30
	v_mul_f32_e32 v34, v147, v34
	v_mul_f32_e32 v35, v147, v30
	v_cvt_pk_fp8_f32 v30, v34, v35
	v_lshlrev_b32_e32 v36, 16, v31
	v_and_b32_e32 v31, 0xffff0000, v31
	v_mul_f32_e32 v34, v147, v36
	v_mul_f32_e32 v31, v147, v31
	v_cvt_pk_fp8_f32 v30, v34, v31 op_sel:[0,0,1]
	v_lshlrev_b32_e32 v31, 16, v32
	v_mul_f32_e32 v34, v147, v31
	v_and_b32_e32 v31, 0xffff0000, v32
	v_mul_f32_e32 v32, v147, v31
	v_cvt_pk_fp8_f32 v31, v34, v32
	v_lshlrev_b32_e32 v35, 16, v33
	v_and_b32_e32 v33, 0xffff0000, v33
	v_mul_f32_e32 v32, v147, v35
	v_mul_f32_e32 v33, v147, v33
	v_cvt_pk_fp8_f32 v31, v32, v33 op_sel:[0,0,1]
	global_store_dwordx2 v[126:127], v[30:31], off offset:768
	s_nop 0
	v_lshlrev_b32_e32 v30, 16, v26
	v_and_b32_e32 v26, 0xffff0000, v26
	v_mul_f32_e32 v30, v147, v30
	v_mul_f32_e32 v31, v147, v26
	v_cvt_pk_fp8_f32 v26, v30, v31
	v_lshlrev_b32_e32 v32, 16, v27
	v_and_b32_e32 v27, 0xffff0000, v27
	v_mul_f32_e32 v30, v147, v32
	v_mul_f32_e32 v27, v147, v27
	v_cvt_pk_fp8_f32 v26, v30, v27 op_sel:[0,0,1]
	v_lshlrev_b32_e32 v27, 16, v28
	v_mul_f32_e32 v30, v147, v27
	v_and_b32_e32 v27, 0xffff0000, v28
	v_mul_f32_e32 v28, v147, v27
	v_cvt_pk_fp8_f32 v27, v30, v28
	v_lshlrev_b32_e32 v31, 16, v29
	v_and_b32_e32 v29, 0xffff0000, v29
	v_mul_f32_e32 v28, v147, v31
	v_mul_f32_e32 v29, v147, v29
	v_cvt_pk_fp8_f32 v27, v28, v29 op_sel:[0,0,1]
	global_store_dwordx2 v[126:127], v[26:27], off offset:800
	s_nop 0
	v_lshlrev_b32_e32 v26, 16, v22
	v_and_b32_e32 v22, 0xffff0000, v22
	v_mul_f32_e32 v26, v147, v26
	v_mul_f32_e32 v27, v147, v22
	v_cvt_pk_fp8_f32 v22, v26, v27
	v_lshlrev_b32_e32 v28, 16, v23
	v_and_b32_e32 v23, 0xffff0000, v23
	v_mul_f32_e32 v26, v147, v28
	v_mul_f32_e32 v23, v147, v23
	v_cvt_pk_fp8_f32 v22, v26, v23 op_sel:[0,0,1]
	v_lshlrev_b32_e32 v23, 16, v24
	v_mul_f32_e32 v26, v147, v23
	v_and_b32_e32 v23, 0xffff0000, v24
	v_mul_f32_e32 v24, v147, v23
	v_cvt_pk_fp8_f32 v23, v26, v24
	v_lshlrev_b32_e32 v27, 16, v25
	v_and_b32_e32 v25, 0xffff0000, v25
	v_mul_f32_e32 v24, v147, v27
	v_mul_f32_e32 v25, v147, v25
	v_cvt_pk_fp8_f32 v23, v24, v25 op_sel:[0,0,1]
	global_store_dwordx2 v[126:127], v[22:23], off offset:832
	s_nop 0
	v_lshlrev_b32_e32 v22, 16, v18
	v_and_b32_e32 v18, 0xffff0000, v18
	v_mul_f32_e32 v22, v147, v22
	v_mul_f32_e32 v23, v147, v18
	v_cvt_pk_fp8_f32 v18, v22, v23
	v_lshlrev_b32_e32 v24, 16, v19
	v_and_b32_e32 v19, 0xffff0000, v19
	v_mul_f32_e32 v22, v147, v24
	v_mul_f32_e32 v19, v147, v19
	v_cvt_pk_fp8_f32 v18, v22, v19 op_sel:[0,0,1]
	v_lshlrev_b32_e32 v19, 16, v20
	v_mul_f32_e32 v22, v147, v19
	v_and_b32_e32 v19, 0xffff0000, v20
	v_mul_f32_e32 v20, v147, v19
	v_cvt_pk_fp8_f32 v19, v22, v20
	v_lshlrev_b32_e32 v23, 16, v21
	v_and_b32_e32 v21, 0xffff0000, v21
	v_mul_f32_e32 v20, v147, v23
	v_mul_f32_e32 v21, v147, v21
	v_cvt_pk_fp8_f32 v19, v20, v21 op_sel:[0,0,1]
	global_store_dwordx2 v[126:127], v[18:19], off offset:864
	s_nop 0
	v_lshlrev_b32_e32 v18, 16, v14
	v_and_b32_e32 v14, 0xffff0000, v14
	v_mul_f32_e32 v18, v147, v18
	v_mul_f32_e32 v19, v147, v14
	v_cvt_pk_fp8_f32 v14, v18, v19
	v_lshlrev_b32_e32 v20, 16, v15
	v_and_b32_e32 v15, 0xffff0000, v15
	v_mul_f32_e32 v18, v147, v20
	v_mul_f32_e32 v15, v147, v15
	v_cvt_pk_fp8_f32 v14, v18, v15 op_sel:[0,0,1]
	v_lshlrev_b32_e32 v15, 16, v16
	v_mul_f32_e32 v18, v147, v15
	v_and_b32_e32 v15, 0xffff0000, v16
	v_mul_f32_e32 v16, v147, v15
	v_cvt_pk_fp8_f32 v15, v18, v16
	v_lshlrev_b32_e32 v19, 16, v17
	v_and_b32_e32 v17, 0xffff0000, v17
	v_mul_f32_e32 v16, v147, v19
	v_mul_f32_e32 v17, v147, v17
	v_cvt_pk_fp8_f32 v15, v16, v17 op_sel:[0,0,1]
	global_store_dwordx2 v[126:127], v[14:15], off offset:896
	s_nop 0
	v_lshlrev_b32_e32 v14, 16, v10
	v_and_b32_e32 v10, 0xffff0000, v10
	v_mul_f32_e32 v14, v147, v14
	v_mul_f32_e32 v15, v147, v10
	v_cvt_pk_fp8_f32 v10, v14, v15
	v_lshlrev_b32_e32 v16, 16, v11
	v_and_b32_e32 v11, 0xffff0000, v11
	v_mul_f32_e32 v14, v147, v16
	v_mul_f32_e32 v11, v147, v11
	v_cvt_pk_fp8_f32 v10, v14, v11 op_sel:[0,0,1]
	v_lshlrev_b32_e32 v11, 16, v12
	v_mul_f32_e32 v14, v147, v11
	v_and_b32_e32 v11, 0xffff0000, v12
	v_mul_f32_e32 v12, v147, v11
	v_cvt_pk_fp8_f32 v11, v14, v12
	v_lshlrev_b32_e32 v15, 16, v13
	v_and_b32_e32 v13, 0xffff0000, v13
	v_mul_f32_e32 v12, v147, v15
	v_mul_f32_e32 v13, v147, v13
	v_cvt_pk_fp8_f32 v11, v12, v13 op_sel:[0,0,1]
	global_store_dwordx2 v[126:127], v[10:11], off offset:928
	s_nop 0
	v_lshlrev_b32_e32 v10, 16, v6
	v_and_b32_e32 v6, 0xffff0000, v6
	v_mul_f32_e32 v10, v147, v10
	v_mul_f32_e32 v11, v147, v6
	v_cvt_pk_fp8_f32 v6, v10, v11
	v_lshlrev_b32_e32 v12, 16, v7
	v_and_b32_e32 v7, 0xffff0000, v7
	v_mul_f32_e32 v10, v147, v12
	v_mul_f32_e32 v7, v147, v7
	v_cvt_pk_fp8_f32 v6, v10, v7 op_sel:[0,0,1]
	v_lshlrev_b32_e32 v7, 16, v8
	v_mul_f32_e32 v10, v147, v7
	v_and_b32_e32 v7, 0xffff0000, v8
	v_mul_f32_e32 v8, v147, v7
	v_cvt_pk_fp8_f32 v7, v10, v8
	v_lshlrev_b32_e32 v11, 16, v9
	v_and_b32_e32 v9, 0xffff0000, v9
	v_mul_f32_e32 v8, v147, v11
	v_mul_f32_e32 v9, v147, v9
	v_cvt_pk_fp8_f32 v7, v8, v9 op_sel:[0,0,1]
	global_store_dwordx2 v[126:127], v[6:7], off offset:960
	s_nop 0
	v_lshlrev_b32_e32 v6, 16, v2
	v_and_b32_e32 v2, 0xffff0000, v2
	v_mul_f32_e32 v6, v147, v6
	v_mul_f32_e32 v7, v147, v2
	v_cvt_pk_fp8_f32 v2, v6, v7
	v_lshlrev_b32_e32 v8, 16, v3
	v_and_b32_e32 v3, 0xffff0000, v3
	v_mul_f32_e32 v6, v147, v8
	v_mul_f32_e32 v3, v147, v3
	v_cvt_pk_fp8_f32 v2, v6, v3 op_sel:[0,0,1]
	v_lshlrev_b32_e32 v3, 16, v4
	v_mul_f32_e32 v6, v147, v3
	v_and_b32_e32 v3, 0xffff0000, v4
	v_mul_f32_e32 v4, v147, v3
	v_cvt_pk_fp8_f32 v3, v6, v4
	v_lshlrev_b32_e32 v7, 16, v5
	v_and_b32_e32 v5, 0xffff0000, v5
	v_mul_f32_e32 v4, v147, v7
	v_mul_f32_e32 v5, v147, v5
	v_cvt_pk_fp8_f32 v3, v4, v5 op_sel:[0,0,1]
	ds_bpermute_b32 v4, v179, v145
	ds_bpermute_b32 v5, v185, v145
	global_store_dwordx2 v[126:127], v[2:3], off offset:992
	ds_bpermute_b32 v2, v181, v145
	s_waitcnt lgkmcnt(2)
	v_fma_f32 v3, v130, v4, v172
	v_fma_f32 v4, v134, v4, v173
	s_waitcnt lgkmcnt(0)
	ds_write2_b32 v180, v3, v4 offset1:16
	ds_bpermute_b32 v3, v183, v145
	s_waitcnt lgkmcnt(2)
	v_fma_f32 v4, v131, v2, v172
	v_fma_f32 v2, v135, v2, v173
	ds_write2_b32 v182, v4, v2 offset1:16
	s_waitcnt lgkmcnt(1)
	v_fma_f32 v2, v132, v3, v172
	v_fma_f32 v3, v136, v3, v173
	ds_write2_b32 v184, v2, v3 offset1:16
	v_fma_f32 v2, v133, v5, v172
	v_fma_f32 v3, v137, v5, v173
	ds_write2_b32 v186, v2, v3 offset1:16
	s_waitcnt lgkmcnt(0)
	s_and_saveexec_b64 s[20:21], s[6:7]
	s_cbranch_execz .LBB0_437
	v_add_u32_e32 v2, s0, v176
	ds_read2_b32 v[32:33], v2 offset1:1
	ds_read2_b32 v[30:31], v2 offset0:2 offset1:3
	ds_read2_b32 v[28:29], v2 offset0:4 offset1:5
	ds_read2_b32 v[26:27], v2 offset0:6 offset1:7
	ds_read2_b32 v[24:25], v2 offset0:8 offset1:9
	ds_read2_b32 v[22:23], v2 offset0:10 offset1:11
	ds_read2_b32 v[20:21], v2 offset0:12 offset1:13
	ds_read2_b32 v[18:19], v2 offset0:14 offset1:15
	ds_read2_b32 v[16:17], v2 offset0:16 offset1:17
	ds_read2_b32 v[14:15], v2 offset0:18 offset1:19
	ds_read2_b32 v[12:13], v2 offset0:20 offset1:21
	ds_read2_b32 v[10:11], v2 offset0:22 offset1:23
	ds_read2_b32 v[8:9], v2 offset0:24 offset1:25
	ds_read2_b32 v[6:7], v2 offset0:26 offset1:27
	ds_read2_b32 v[4:5], v2 offset0:28 offset1:29
	ds_read2_b32 v[2:3], v2 offset0:30 offset1:31
	s_waitcnt lgkmcnt(14)
	v_cmp_gt_f32_e32 vcc, v33, v32
	s_nop 1
	v_cndmask_b32_e32 v35, v32, v33, vcc
	v_cndmask_b32_e64 v34, 0, 1, vcc
	v_cmp_gt_f32_e32 vcc, v30, v35
	s_nop 1
	v_cndmask_b32_e32 v35, v35, v30, vcc
	v_cndmask_b32_e64 v34, v34, 2, vcc
	v_cmp_gt_f32_e32 vcc, v31, v35
	s_nop 1
	v_cndmask_b32_e32 v35, v35, v31, vcc
	v_cndmask_b32_e64 v34, v34, 3, vcc
	s_waitcnt lgkmcnt(13)
	v_cmp_gt_f32_e32 vcc, v28, v35
	s_nop 1
	v_cndmask_b32_e32 v35, v35, v28, vcc
	v_cndmask_b32_e64 v34, v34, 4, vcc
	v_cmp_gt_f32_e32 vcc, v29, v35
	s_nop 1
	v_cndmask_b32_e32 v35, v35, v29, vcc
	v_cndmask_b32_e64 v34, v34, 5, vcc
	s_waitcnt lgkmcnt(12)
	v_cmp_gt_f32_e32 vcc, v26, v35
	s_nop 1
	v_cndmask_b32_e32 v35, v35, v26, vcc
	v_cndmask_b32_e64 v34, v34, 6, vcc
	v_cmp_gt_f32_e32 vcc, v27, v35
	s_nop 1
	v_cndmask_b32_e32 v35, v35, v27, vcc
	v_cndmask_b32_e64 v34, v34, 7, vcc
	s_waitcnt lgkmcnt(11)
	v_cmp_gt_f32_e32 vcc, v24, v35
	s_nop 1
	v_cndmask_b32_e32 v35, v35, v24, vcc
	v_cndmask_b32_e64 v34, v34, 8, vcc
	v_cmp_gt_f32_e32 vcc, v25, v35
	s_nop 1
	v_cndmask_b32_e32 v35, v35, v25, vcc
	v_cndmask_b32_e64 v34, v34, 9, vcc
	s_waitcnt lgkmcnt(10)
	v_cmp_gt_f32_e32 vcc, v22, v35
	s_nop 1
	v_cndmask_b32_e32 v35, v35, v22, vcc
	v_cndmask_b32_e64 v34, v34, 10, vcc
	v_cmp_gt_f32_e32 vcc, v23, v35
	s_nop 1
	v_cndmask_b32_e32 v35, v35, v23, vcc
	v_cndmask_b32_e64 v34, v34, 11, vcc
	s_waitcnt lgkmcnt(9)
	v_cmp_gt_f32_e32 vcc, v20, v35
	s_nop 1
	v_cndmask_b32_e32 v35, v35, v20, vcc
	v_cndmask_b32_e64 v34, v34, 12, vcc
	v_cmp_gt_f32_e32 vcc, v21, v35
	s_nop 1
	v_cndmask_b32_e32 v35, v35, v21, vcc
	v_cndmask_b32_e64 v34, v34, 13, vcc
	s_waitcnt lgkmcnt(8)
	v_cmp_gt_f32_e32 vcc, v18, v35
	s_nop 1
	v_cndmask_b32_e32 v35, v35, v18, vcc
	v_cndmask_b32_e64 v34, v34, 14, vcc
	v_cmp_gt_f32_e32 vcc, v19, v35
	s_nop 1
	v_cndmask_b32_e32 v35, v35, v19, vcc
	v_cndmask_b32_e64 v34, v34, 15, vcc
	s_waitcnt lgkmcnt(7)
	v_cmp_gt_f32_e32 vcc, v16, v35
	s_nop 1
	v_cndmask_b32_e32 v35, v35, v16, vcc
	v_cndmask_b32_e64 v34, v34, 16, vcc
	v_cmp_gt_f32_e32 vcc, v17, v35
	s_nop 1
	v_cndmask_b32_e32 v35, v35, v17, vcc
	v_cndmask_b32_e64 v34, v34, 17, vcc
	s_waitcnt lgkmcnt(6)
	v_cmp_gt_f32_e32 vcc, v14, v35
	s_nop 1
	v_cndmask_b32_e32 v35, v35, v14, vcc
	v_cndmask_b32_e64 v34, v34, 18, vcc
	v_cmp_gt_f32_e32 vcc, v15, v35
	s_nop 1
	v_cndmask_b32_e32 v35, v35, v15, vcc
	v_cndmask_b32_e64 v34, v34, 19, vcc
	s_waitcnt lgkmcnt(5)
	v_cmp_gt_f32_e32 vcc, v12, v35
	s_nop 1
	v_cndmask_b32_e32 v35, v35, v12, vcc
	v_cndmask_b32_e64 v34, v34, 20, vcc
	v_cmp_gt_f32_e32 vcc, v13, v35
	s_nop 1
	v_cndmask_b32_e32 v35, v35, v13, vcc
	v_cndmask_b32_e64 v34, v34, 21, vcc
	s_waitcnt lgkmcnt(4)
	v_cmp_gt_f32_e32 vcc, v10, v35
	s_nop 1
	v_cndmask_b32_e32 v35, v35, v10, vcc
	v_cndmask_b32_e64 v34, v34, 22, vcc
	v_cmp_gt_f32_e32 vcc, v11, v35
	s_nop 1
	v_cndmask_b32_e32 v35, v35, v11, vcc
	v_cndmask_b32_e64 v34, v34, 23, vcc
	s_waitcnt lgkmcnt(3)
	v_cmp_gt_f32_e32 vcc, v8, v35
	s_nop 1
	v_cndmask_b32_e32 v35, v35, v8, vcc
	v_cndmask_b32_e64 v34, v34, 24, vcc
	v_cmp_gt_f32_e32 vcc, v9, v35
	s_nop 1
	v_cndmask_b32_e32 v35, v35, v9, vcc
	v_cndmask_b32_e64 v34, v34, 25, vcc
	s_waitcnt lgkmcnt(2)
	v_cmp_gt_f32_e32 vcc, v6, v35
	s_nop 1
	v_cndmask_b32_e32 v35, v35, v6, vcc
	v_cndmask_b32_e64 v34, v34, 26, vcc
	v_cmp_gt_f32_e32 vcc, v7, v35
	s_nop 1
	v_cndmask_b32_e32 v35, v35, v7, vcc
	v_cndmask_b32_e64 v34, v34, 27, vcc
	s_waitcnt lgkmcnt(1)
	v_cmp_gt_f32_e32 vcc, v4, v35
	s_nop 1
	v_cndmask_b32_e32 v35, v35, v4, vcc
	v_cndmask_b32_e64 v34, v34, 28, vcc
	v_cmp_gt_f32_e32 vcc, v5, v35
	s_nop 1
	v_cndmask_b32_e32 v35, v35, v5, vcc
	v_cndmask_b32_e64 v34, v34, 29, vcc
	s_waitcnt lgkmcnt(0)
	v_cmp_gt_f32_e32 vcc, v2, v35
	s_nop 1
	v_cndmask_b32_e32 v35, v35, v2, vcc
	v_cndmask_b32_e64 v34, v34, 30, vcc
	v_cmp_gt_f32_e32 vcc, v3, v35
	s_nop 1
	v_cndmask_b32_e64 v146, v34, 31, vcc
	v_cndmask_b32_e32 v34, v35, v3, vcc
	v_cmp_eq_u32_e32 vcc, 0, v146
	v_lshlrev_b32_e64 v36, v146, 1
	v_and_b32_e32 v38, 2, v36
	v_cndmask_b32_e32 v37, v32, v198, vcc
	v_cmp_gt_f32_e64 s[8:9], v33, v37
	v_cndmask_b32_e64 v35, 0, -1, vcc
	s_or_b64 vcc, vcc, s[8:9]
	v_cndmask_b32_e64 v39, 0, 1, vcc
	v_cndmask_b32_e32 v40, v32, v33, vcc
	v_cmp_eq_u32_e32 vcc, 0, v38
	v_and_b32_e32 v38, 4, v36
	s_nop 0
	v_cndmask_b32_e32 v37, v37, v40, vcc
	v_cndmask_b32_e32 v35, v35, v39, vcc
	v_cmp_eq_u32_e32 vcc, 0, v38
	v_cmp_gt_f32_e64 s[8:9], v30, v37
	s_and_b64 vcc, vcc, s[8:9]
	v_cndmask_b32_e64 v35, v35, 2, vcc
	v_cndmask_b32_e32 v37, v37, v30, vcc
	v_and_b32_e32 v38, 8, v36
	v_cmp_gt_i32_e64 s[8:9], 0, v35
	v_cmp_gt_f32_e64 s[10:11], v31, v37
	v_cmp_eq_u32_e32 vcc, 0, v38
	s_or_b64 s[8:9], s[8:9], s[10:11]
	s_and_b64 vcc, vcc, s[8:9]
	v_cndmask_b32_e64 v35, v35, 3, vcc
	v_cndmask_b32_e32 v37, v37, v31, vcc
	v_and_b32_e32 v38, 16, v36
	v_cmp_gt_i32_e64 s[8:9], 0, v35
	v_cmp_gt_f32_e64 s[10:11], v28, v37
	v_cmp_eq_u32_e32 vcc, 0, v38
	s_or_b64 s[8:9], s[8:9], s[10:11]
	s_and_b64 vcc, vcc, s[8:9]
	v_cndmask_b32_e64 v35, v35, 4, vcc
	v_cndmask_b32_e32 v37, v37, v28, vcc
	v_and_b32_e32 v38, 32, v36
	v_cmp_gt_i32_e64 s[8:9], 0, v35
	v_cmp_gt_f32_e64 s[10:11], v29, v37
	v_cmp_eq_u32_e32 vcc, 0, v38
	s_or_b64 s[8:9], s[8:9], s[10:11]
	s_and_b64 vcc, vcc, s[8:9]
	v_cndmask_b32_e64 v35, v35, 5, vcc
	v_cndmask_b32_e32 v37, v37, v29, vcc
	v_and_b32_e32 v38, 64, v36
	v_cmp_gt_i32_e64 s[8:9], 0, v35
	v_cmp_gt_f32_e64 s[10:11], v26, v37
	v_cmp_eq_u32_e32 vcc, 0, v38
	s_or_b64 s[8:9], s[8:9], s[10:11]
	s_and_b64 vcc, vcc, s[8:9]
	v_cndmask_b32_e64 v35, v35, 6, vcc
	v_cndmask_b32_e32 v37, v37, v26, vcc
	v_and_b32_e32 v38, 0x80, v36
	v_cmp_gt_i32_e64 s[8:9], 0, v35
	v_cmp_gt_f32_e64 s[10:11], v27, v37
	v_cmp_eq_u32_e32 vcc, 0, v38
	s_or_b64 s[8:9], s[8:9], s[10:11]
	s_and_b64 vcc, vcc, s[8:9]
	v_cndmask_b32_e64 v35, v35, 7, vcc
	v_cndmask_b32_e32 v37, v37, v27, vcc
	v_and_b32_e32 v38, 0x100, v36
	v_cmp_gt_i32_e64 s[8:9], 0, v35
	v_cmp_gt_f32_e64 s[10:11], v24, v37
	v_cmp_eq_u32_e32 vcc, 0, v38
	s_or_b64 s[8:9], s[8:9], s[10:11]
	s_and_b64 vcc, vcc, s[8:9]
	v_cndmask_b32_e64 v35, v35, 8, vcc
	v_cndmask_b32_e32 v37, v37, v24, vcc
	v_and_b32_e32 v38, 0x200, v36
	v_cmp_gt_i32_e64 s[8:9], 0, v35
	v_cmp_gt_f32_e64 s[10:11], v25, v37
	v_cmp_eq_u32_e32 vcc, 0, v38
	s_or_b64 s[8:9], s[8:9], s[10:11]
	s_and_b64 vcc, vcc, s[8:9]
	v_cndmask_b32_e64 v35, v35, 9, vcc
	v_cndmask_b32_e32 v37, v37, v25, vcc
	v_and_b32_e32 v38, 0x400, v36
	v_cmp_gt_i32_e64 s[8:9], 0, v35
	v_cmp_gt_f32_e64 s[10:11], v22, v37
	v_cmp_eq_u32_e32 vcc, 0, v38
	s_or_b64 s[8:9], s[8:9], s[10:11]
	s_and_b64 vcc, vcc, s[8:9]
	v_cndmask_b32_e64 v35, v35, 10, vcc
	v_cndmask_b32_e32 v37, v37, v22, vcc
	v_and_b32_e32 v38, 0x800, v36
	v_cmp_gt_i32_e64 s[8:9], 0, v35
	v_cmp_gt_f32_e64 s[10:11], v23, v37
	v_cmp_eq_u32_e32 vcc, 0, v38
	s_or_b64 s[8:9], s[8:9], s[10:11]
	s_and_b64 vcc, vcc, s[8:9]
	v_cndmask_b32_e64 v35, v35, 11, vcc
	v_cndmask_b32_e32 v37, v37, v23, vcc
	v_and_b32_e32 v38, 0x1000, v36
	v_cmp_gt_i32_e64 s[8:9], 0, v35
	v_cmp_gt_f32_e64 s[10:11], v20, v37
	v_cmp_eq_u32_e32 vcc, 0, v38
	s_or_b64 s[8:9], s[8:9], s[10:11]
	s_and_b64 vcc, vcc, s[8:9]
	v_cndmask_b32_e64 v35, v35, 12, vcc
	v_cndmask_b32_e32 v37, v37, v20, vcc
	v_and_b32_e32 v38, 0x2000, v36
	v_cmp_gt_i32_e64 s[8:9], 0, v35
	v_cmp_gt_f32_e64 s[10:11], v21, v37
	v_cmp_eq_u32_e32 vcc, 0, v38
	s_or_b64 s[8:9], s[8:9], s[10:11]
	s_and_b64 vcc, vcc, s[8:9]
	v_cndmask_b32_e64 v35, v35, 13, vcc
	v_cndmask_b32_e32 v37, v37, v21, vcc
	v_and_b32_e32 v38, 0x4000, v36
	v_cmp_gt_i32_e64 s[8:9], 0, v35
	v_cmp_gt_f32_e64 s[10:11], v18, v37
	v_cmp_eq_u32_e32 vcc, 0, v38
	s_or_b64 s[8:9], s[8:9], s[10:11]
	s_and_b64 vcc, vcc, s[8:9]
	v_cndmask_b32_e64 v35, v35, 14, vcc
	v_cndmask_b32_e32 v37, v37, v18, vcc
	v_and_b32_e32 v38, 0x8000, v36
	v_cmp_gt_i32_e64 s[8:9], 0, v35
	v_cmp_gt_f32_e64 s[10:11], v19, v37
	v_cmp_eq_u32_e32 vcc, 0, v38
	s_or_b64 s[8:9], s[8:9], s[10:11]
	s_and_b64 vcc, vcc, s[8:9]
	v_cndmask_b32_e64 v35, v35, 15, vcc
	v_cndmask_b32_e32 v37, v37, v19, vcc
	v_and_b32_e32 v38, 0x10000, v36
	v_cmp_gt_i32_e64 s[8:9], 0, v35
	v_cmp_gt_f32_e64 s[10:11], v16, v37
	v_cmp_eq_u32_e32 vcc, 0, v38
	s_or_b64 s[8:9], s[8:9], s[10:11]
	s_and_b64 vcc, vcc, s[8:9]
	v_cndmask_b32_e64 v35, v35, 16, vcc
	v_cndmask_b32_e32 v37, v37, v16, vcc
	v_and_b32_e32 v38, 0x20000, v36
	v_cmp_gt_i32_e64 s[8:9], 0, v35
	v_cmp_gt_f32_e64 s[10:11], v17, v37
	v_cmp_eq_u32_e32 vcc, 0, v38
	s_or_b64 s[8:9], s[8:9], s[10:11]
	s_and_b64 vcc, vcc, s[8:9]
	v_cndmask_b32_e64 v35, v35, 17, vcc
	v_cndmask_b32_e32 v37, v37, v17, vcc
	v_and_b32_e32 v38, 0x40000, v36
	v_cmp_gt_i32_e64 s[8:9], 0, v35
	v_cmp_gt_f32_e64 s[10:11], v14, v37
	v_cmp_eq_u32_e32 vcc, 0, v38
	s_or_b64 s[8:9], s[8:9], s[10:11]
	s_and_b64 vcc, vcc, s[8:9]
	v_cndmask_b32_e64 v35, v35, 18, vcc
	v_cndmask_b32_e32 v37, v37, v14, vcc
	v_and_b32_e32 v38, 0x80000, v36
	v_cmp_gt_i32_e64 s[8:9], 0, v35
	v_cmp_gt_f32_e64 s[10:11], v15, v37
	v_cmp_eq_u32_e32 vcc, 0, v38
	s_or_b64 s[8:9], s[8:9], s[10:11]
	s_and_b64 vcc, vcc, s[8:9]
	v_cndmask_b32_e64 v35, v35, 19, vcc
	v_cndmask_b32_e32 v37, v37, v15, vcc
	v_and_b32_e32 v38, 0x100000, v36
	v_cmp_gt_i32_e64 s[8:9], 0, v35
	v_cmp_gt_f32_e64 s[10:11], v12, v37
	v_cmp_eq_u32_e32 vcc, 0, v38
	s_or_b64 s[8:9], s[8:9], s[10:11]
	s_and_b64 vcc, vcc, s[8:9]
	v_cndmask_b32_e64 v35, v35, 20, vcc
	v_cndmask_b32_e32 v37, v37, v12, vcc
	v_and_b32_e32 v38, 0x200000, v36
	v_cmp_gt_i32_e64 s[8:9], 0, v35
	v_cmp_gt_f32_e64 s[10:11], v13, v37
	v_cmp_eq_u32_e32 vcc, 0, v38
	s_or_b64 s[8:9], s[8:9], s[10:11]
	s_and_b64 vcc, vcc, s[8:9]
	v_cndmask_b32_e64 v35, v35, 21, vcc
	v_cndmask_b32_e32 v37, v37, v13, vcc
	v_and_b32_e32 v38, 0x400000, v36
	v_cmp_gt_i32_e64 s[8:9], 0, v35
	v_cmp_gt_f32_e64 s[10:11], v10, v37
	v_cmp_eq_u32_e32 vcc, 0, v38
	s_or_b64 s[8:9], s[8:9], s[10:11]
	s_and_b64 vcc, vcc, s[8:9]
	v_cndmask_b32_e64 v35, v35, 22, vcc
	v_cndmask_b32_e32 v37, v37, v10, vcc
	v_and_b32_e32 v38, 0x800000, v36
	v_cmp_gt_i32_e64 s[8:9], 0, v35
	v_cmp_gt_f32_e64 s[10:11], v11, v37
	v_cmp_eq_u32_e32 vcc, 0, v38
	s_or_b64 s[8:9], s[8:9], s[10:11]
	s_and_b64 vcc, vcc, s[8:9]
	v_cndmask_b32_e64 v35, v35, 23, vcc
	v_cndmask_b32_e32 v37, v37, v11, vcc
	v_and_b32_e32 v38, 0x1000000, v36
	v_cmp_gt_i32_e64 s[8:9], 0, v35
	v_cmp_gt_f32_e64 s[10:11], v8, v37
	v_cmp_eq_u32_e32 vcc, 0, v38
	s_or_b64 s[8:9], s[8:9], s[10:11]
	s_and_b64 vcc, vcc, s[8:9]
	v_cndmask_b32_e64 v35, v35, 24, vcc
	v_cndmask_b32_e32 v37, v37, v8, vcc
	v_and_b32_e32 v38, 0x2000000, v36
	v_cmp_gt_i32_e64 s[8:9], 0, v35
	v_cmp_gt_f32_e64 s[10:11], v9, v37
	v_cmp_eq_u32_e32 vcc, 0, v38
	s_or_b64 s[8:9], s[8:9], s[10:11]
	s_and_b64 vcc, vcc, s[8:9]
	v_cndmask_b32_e64 v35, v35, 25, vcc
	v_cndmask_b32_e32 v37, v37, v9, vcc
	v_and_b32_e32 v38, 0x4000000, v36
	v_cmp_gt_i32_e64 s[8:9], 0, v35
	v_cmp_gt_f32_e64 s[10:11], v6, v37
	v_cmp_eq_u32_e32 vcc, 0, v38
	s_or_b64 s[8:9], s[8:9], s[10:11]
	s_and_b64 vcc, vcc, s[8:9]
	v_cndmask_b32_e64 v35, v35, 26, vcc
	v_cndmask_b32_e32 v37, v37, v6, vcc
	v_and_b32_e32 v38, 0x8000000, v36
	v_cmp_gt_i32_e64 s[8:9], 0, v35
	v_cmp_gt_f32_e64 s[10:11], v7, v37
	v_cmp_eq_u32_e32 vcc, 0, v38
	s_or_b64 s[8:9], s[8:9], s[10:11]
	s_and_b64 vcc, vcc, s[8:9]
	v_cndmask_b32_e64 v35, v35, 27, vcc
	v_cndmask_b32_e32 v37, v37, v7, vcc
	v_and_b32_e32 v38, 0x10000000, v36
	v_cmp_gt_i32_e64 s[8:9], 0, v35
	v_cmp_gt_f32_e64 s[10:11], v4, v37
	v_cmp_eq_u32_e32 vcc, 0, v38
	s_or_b64 s[8:9], s[8:9], s[10:11]
	s_and_b64 vcc, vcc, s[8:9]
	v_cndmask_b32_e64 v35, v35, 28, vcc
	v_cndmask_b32_e32 v37, v37, v4, vcc
	v_and_b32_e32 v38, 0x20000000, v36
	v_cmp_gt_i32_e64 s[8:9], 0, v35
	v_cmp_gt_f32_e64 s[10:11], v5, v37
	v_cmp_eq_u32_e32 vcc, 0, v38
	s_or_b64 s[8:9], s[8:9], s[10:11]
	s_and_b64 vcc, vcc, s[8:9]
	v_cndmask_b32_e64 v35, v35, 29, vcc
	v_cndmask_b32_e32 v37, v37, v5, vcc
	v_and_b32_e32 v38, 2.0, v36
	v_cmp_gt_i32_e64 s[8:9], 0, v35
	v_cmp_gt_f32_e64 s[10:11], v2, v37
	v_cmp_eq_u32_e32 vcc, 0, v38
	s_or_b64 s[8:9], s[8:9], s[10:11]
	s_and_b64 vcc, vcc, s[8:9]
	v_cndmask_b32_e64 v35, v35, 30, vcc
	v_cndmask_b32_e32 v37, v37, v2, vcc
	v_cmp_gt_i32_e32 vcc, 0, v35
	v_cmp_gt_f32_e64 s[8:9], v3, v37
	s_or_b64 vcc, vcc, s[8:9]
	v_cndmask_b32_e64 v38, v35, 31, vcc
	v_cndmask_b32_e32 v39, v37, v3, vcc
	v_cmp_eq_u32_e32 vcc, 31, v146
	s_nop 1
	v_cndmask_b32_e32 v150, v38, v35, vcc
	v_lshl_or_b32 v36, 1, v150, v36
	v_cndmask_b32_e32 v35, v39, v37, vcc
	v_and_b32_e32 v37, 1, v36
	v_cmp_eq_u32_e32 vcc, 1, v37
	v_and_b32_e32 v39, 2, v36
	v_bfe_i32 v38, v36, 0, 1
	v_cndmask_b32_e32 v37, v32, v198, vcc
	v_cmp_gt_f32_e64 s[8:9], v33, v37
	s_or_b64 vcc, vcc, s[8:9]
	v_cndmask_b32_e64 v40, 0, 1, vcc
	v_cndmask_b32_e32 v41, v32, v33, vcc
	v_cmp_eq_u32_e32 vcc, 0, v39
	v_and_b32_e32 v39, 4, v36
	s_nop 0
	v_cndmask_b32_e32 v38, v38, v40, vcc
	v_cndmask_b32_e32 v37, v37, v41, vcc
	v_cmp_eq_u32_e32 vcc, 0, v39
	v_and_b32_e32 v39, 3, v36
	v_cmp_eq_u32_e64 s[8:9], 3, v39
	v_cmp_gt_f32_e64 s[10:11], v30, v37
	s_or_b64 s[8:9], s[8:9], s[10:11]
	s_and_b64 vcc, vcc, s[8:9]
	v_cndmask_b32_e64 v38, v38, 2, vcc
	v_cndmask_b32_e32 v37, v37, v30, vcc
	v_and_b32_e32 v39, 8, v36
	v_cmp_gt_i32_e64 s[8:9], 0, v38
	v_cmp_gt_f32_e64 s[10:11], v31, v37
	v_cmp_eq_u32_e32 vcc, 0, v39
	s_or_b64 s[8:9], s[8:9], s[10:11]
	s_and_b64 vcc, vcc, s[8:9]
	v_cndmask_b32_e64 v38, v38, 3, vcc
	v_cndmask_b32_e32 v37, v37, v31, vcc
	v_and_b32_e32 v39, 16, v36
	v_cmp_gt_i32_e64 s[8:9], 0, v38
	v_cmp_gt_f32_e64 s[10:11], v28, v37
	v_cmp_eq_u32_e32 vcc, 0, v39
	s_or_b64 s[8:9], s[8:9], s[10:11]
	s_and_b64 vcc, vcc, s[8:9]
	v_cndmask_b32_e64 v38, v38, 4, vcc
	v_cndmask_b32_e32 v37, v37, v28, vcc
	v_and_b32_e32 v39, 32, v36
	v_cmp_gt_i32_e64 s[8:9], 0, v38
	v_cmp_gt_f32_e64 s[10:11], v29, v37
	v_cmp_eq_u32_e32 vcc, 0, v39
	s_or_b64 s[8:9], s[8:9], s[10:11]
	s_and_b64 vcc, vcc, s[8:9]
	v_cndmask_b32_e64 v38, v38, 5, vcc
	v_cndmask_b32_e32 v37, v37, v29, vcc
	v_and_b32_e32 v39, 64, v36
	v_cmp_gt_i32_e64 s[8:9], 0, v38
	v_cmp_gt_f32_e64 s[10:11], v26, v37
	v_cmp_eq_u32_e32 vcc, 0, v39
	s_or_b64 s[8:9], s[8:9], s[10:11]
	s_and_b64 vcc, vcc, s[8:9]
	v_cndmask_b32_e64 v38, v38, 6, vcc
	v_cndmask_b32_e32 v37, v37, v26, vcc
	v_and_b32_e32 v39, 0x80, v36
	v_cmp_gt_i32_e64 s[8:9], 0, v38
	v_cmp_gt_f32_e64 s[10:11], v27, v37
	v_cmp_eq_u32_e32 vcc, 0, v39
	s_or_b64 s[8:9], s[8:9], s[10:11]
	s_and_b64 vcc, vcc, s[8:9]
	v_cndmask_b32_e64 v38, v38, 7, vcc
	v_cndmask_b32_e32 v37, v37, v27, vcc
	v_and_b32_e32 v39, 0x100, v36
	v_cmp_gt_i32_e64 s[8:9], 0, v38
	v_cmp_gt_f32_e64 s[10:11], v24, v37
	v_cmp_eq_u32_e32 vcc, 0, v39
	s_or_b64 s[8:9], s[8:9], s[10:11]
	s_and_b64 vcc, vcc, s[8:9]
	v_cndmask_b32_e64 v38, v38, 8, vcc
	v_cndmask_b32_e32 v37, v37, v24, vcc
	v_and_b32_e32 v39, 0x200, v36
	v_cmp_gt_i32_e64 s[8:9], 0, v38
	v_cmp_gt_f32_e64 s[10:11], v25, v37
	v_cmp_eq_u32_e32 vcc, 0, v39
	s_or_b64 s[8:9], s[8:9], s[10:11]
	s_and_b64 vcc, vcc, s[8:9]
	v_cndmask_b32_e64 v38, v38, 9, vcc
	v_cndmask_b32_e32 v37, v37, v25, vcc
	v_and_b32_e32 v39, 0x400, v36
	v_cmp_gt_i32_e64 s[8:9], 0, v38
	v_cmp_gt_f32_e64 s[10:11], v22, v37
	v_cmp_eq_u32_e32 vcc, 0, v39
	s_or_b64 s[8:9], s[8:9], s[10:11]
	s_and_b64 vcc, vcc, s[8:9]
	v_cndmask_b32_e64 v38, v38, 10, vcc
	v_cndmask_b32_e32 v37, v37, v22, vcc
	v_and_b32_e32 v39, 0x800, v36
	v_cmp_gt_i32_e64 s[8:9], 0, v38
	v_cmp_gt_f32_e64 s[10:11], v23, v37
	v_cmp_eq_u32_e32 vcc, 0, v39
	s_or_b64 s[8:9], s[8:9], s[10:11]
	s_and_b64 vcc, vcc, s[8:9]
	v_cndmask_b32_e64 v38, v38, 11, vcc
	v_cndmask_b32_e32 v37, v37, v23, vcc
	v_and_b32_e32 v39, 0x1000, v36
	v_cmp_gt_i32_e64 s[8:9], 0, v38
	v_cmp_gt_f32_e64 s[10:11], v20, v37
	v_cmp_eq_u32_e32 vcc, 0, v39
	s_or_b64 s[8:9], s[8:9], s[10:11]
	s_and_b64 vcc, vcc, s[8:9]
	v_cndmask_b32_e64 v38, v38, 12, vcc
	v_cndmask_b32_e32 v37, v37, v20, vcc
	v_and_b32_e32 v39, 0x2000, v36
	v_cmp_gt_i32_e64 s[8:9], 0, v38
	v_cmp_gt_f32_e64 s[10:11], v21, v37
	v_cmp_eq_u32_e32 vcc, 0, v39
	s_or_b64 s[8:9], s[8:9], s[10:11]
	s_and_b64 vcc, vcc, s[8:9]
	v_cndmask_b32_e64 v38, v38, 13, vcc
	v_cndmask_b32_e32 v37, v37, v21, vcc
	v_and_b32_e32 v39, 0x4000, v36
	v_cmp_gt_i32_e64 s[8:9], 0, v38
	v_cmp_gt_f32_e64 s[10:11], v18, v37
	v_cmp_eq_u32_e32 vcc, 0, v39
	s_or_b64 s[8:9], s[8:9], s[10:11]
	s_and_b64 vcc, vcc, s[8:9]
	v_cndmask_b32_e64 v38, v38, 14, vcc
	v_cndmask_b32_e32 v37, v37, v18, vcc
	v_and_b32_e32 v39, 0x8000, v36
	v_cmp_gt_i32_e64 s[8:9], 0, v38
	v_cmp_gt_f32_e64 s[10:11], v19, v37
	v_cmp_eq_u32_e32 vcc, 0, v39
	s_or_b64 s[8:9], s[8:9], s[10:11]
	s_and_b64 vcc, vcc, s[8:9]
	v_cndmask_b32_e64 v38, v38, 15, vcc
	v_cndmask_b32_e32 v37, v37, v19, vcc
	v_and_b32_e32 v39, 0x10000, v36
	v_cmp_gt_i32_e64 s[8:9], 0, v38
	v_cmp_gt_f32_e64 s[10:11], v16, v37
	v_cmp_eq_u32_e32 vcc, 0, v39
	s_or_b64 s[8:9], s[8:9], s[10:11]
	s_and_b64 vcc, vcc, s[8:9]
	v_cndmask_b32_e64 v38, v38, 16, vcc
	v_cndmask_b32_e32 v37, v37, v16, vcc
	v_and_b32_e32 v39, 0x20000, v36
	v_cmp_gt_i32_e64 s[8:9], 0, v38
	v_cmp_gt_f32_e64 s[10:11], v17, v37
	v_cmp_eq_u32_e32 vcc, 0, v39
	s_or_b64 s[8:9], s[8:9], s[10:11]
	s_and_b64 vcc, vcc, s[8:9]
	v_cndmask_b32_e64 v38, v38, 17, vcc
	v_cndmask_b32_e32 v37, v37, v17, vcc
	v_and_b32_e32 v39, 0x40000, v36
	v_cmp_gt_i32_e64 s[8:9], 0, v38
	v_cmp_gt_f32_e64 s[10:11], v14, v37
	v_cmp_eq_u32_e32 vcc, 0, v39
	s_or_b64 s[8:9], s[8:9], s[10:11]
	s_and_b64 vcc, vcc, s[8:9]
	v_cndmask_b32_e64 v38, v38, 18, vcc
	v_cndmask_b32_e32 v37, v37, v14, vcc
	v_and_b32_e32 v39, 0x80000, v36
	v_cmp_gt_i32_e64 s[8:9], 0, v38
	v_cmp_gt_f32_e64 s[10:11], v15, v37
	v_cmp_eq_u32_e32 vcc, 0, v39
	s_or_b64 s[8:9], s[8:9], s[10:11]
	s_and_b64 vcc, vcc, s[8:9]
	v_cndmask_b32_e64 v38, v38, 19, vcc
	v_cndmask_b32_e32 v37, v37, v15, vcc
	v_and_b32_e32 v39, 0x100000, v36
	v_cmp_gt_i32_e64 s[8:9], 0, v38
	v_cmp_gt_f32_e64 s[10:11], v12, v37
	v_cmp_eq_u32_e32 vcc, 0, v39
	s_or_b64 s[8:9], s[8:9], s[10:11]
	s_and_b64 vcc, vcc, s[8:9]
	v_cndmask_b32_e64 v38, v38, 20, vcc
	v_cndmask_b32_e32 v37, v37, v12, vcc
	v_and_b32_e32 v39, 0x200000, v36
	v_cmp_gt_i32_e64 s[8:9], 0, v38
	v_cmp_gt_f32_e64 s[10:11], v13, v37
	v_cmp_eq_u32_e32 vcc, 0, v39
	s_or_b64 s[8:9], s[8:9], s[10:11]
	s_and_b64 vcc, vcc, s[8:9]
	v_cndmask_b32_e64 v38, v38, 21, vcc
	v_cndmask_b32_e32 v37, v37, v13, vcc
	v_and_b32_e32 v39, 0x400000, v36
	v_cmp_gt_i32_e64 s[8:9], 0, v38
	v_cmp_gt_f32_e64 s[10:11], v10, v37
	v_cmp_eq_u32_e32 vcc, 0, v39
	s_or_b64 s[8:9], s[8:9], s[10:11]
	s_and_b64 vcc, vcc, s[8:9]
	v_cndmask_b32_e64 v38, v38, 22, vcc
	v_cndmask_b32_e32 v37, v37, v10, vcc
	v_and_b32_e32 v39, 0x800000, v36
	v_cmp_gt_i32_e64 s[8:9], 0, v38
	v_cmp_gt_f32_e64 s[10:11], v11, v37
	v_cmp_eq_u32_e32 vcc, 0, v39
	s_or_b64 s[8:9], s[8:9], s[10:11]
	s_and_b64 vcc, vcc, s[8:9]
	v_cndmask_b32_e64 v38, v38, 23, vcc
	v_cndmask_b32_e32 v37, v37, v11, vcc
	v_and_b32_e32 v39, 0x1000000, v36
	v_cmp_gt_i32_e64 s[8:9], 0, v38
	v_cmp_gt_f32_e64 s[10:11], v8, v37
	v_cmp_eq_u32_e32 vcc, 0, v39
	s_or_b64 s[8:9], s[8:9], s[10:11]
	s_and_b64 vcc, vcc, s[8:9]
	v_cndmask_b32_e64 v38, v38, 24, vcc
	v_cndmask_b32_e32 v37, v37, v8, vcc
	v_and_b32_e32 v39, 0x2000000, v36
	v_cmp_gt_i32_e64 s[8:9], 0, v38
	v_cmp_gt_f32_e64 s[10:11], v9, v37
	v_cmp_eq_u32_e32 vcc, 0, v39
	s_or_b64 s[8:9], s[8:9], s[10:11]
	s_and_b64 vcc, vcc, s[8:9]
	v_cndmask_b32_e64 v38, v38, 25, vcc
	v_cndmask_b32_e32 v37, v37, v9, vcc
	v_and_b32_e32 v39, 0x4000000, v36
	v_cmp_gt_i32_e64 s[8:9], 0, v38
	v_cmp_gt_f32_e64 s[10:11], v6, v37
	v_cmp_eq_u32_e32 vcc, 0, v39
	s_or_b64 s[8:9], s[8:9], s[10:11]
	s_and_b64 vcc, vcc, s[8:9]
	v_cndmask_b32_e64 v38, v38, 26, vcc
	v_cndmask_b32_e32 v37, v37, v6, vcc
	v_and_b32_e32 v39, 0x8000000, v36
	v_cmp_gt_i32_e64 s[8:9], 0, v38
	v_cmp_gt_f32_e64 s[10:11], v7, v37
	v_cmp_eq_u32_e32 vcc, 0, v39
	s_or_b64 s[8:9], s[8:9], s[10:11]
	s_and_b64 vcc, vcc, s[8:9]
	v_cndmask_b32_e64 v38, v38, 27, vcc
	v_cndmask_b32_e32 v37, v37, v7, vcc
	v_and_b32_e32 v39, 0x10000000, v36
	v_cmp_gt_i32_e64 s[8:9], 0, v38
	v_cmp_gt_f32_e64 s[10:11], v4, v37
	v_cmp_eq_u32_e32 vcc, 0, v39
	s_or_b64 s[8:9], s[8:9], s[10:11]
	s_and_b64 vcc, vcc, s[8:9]
	v_cndmask_b32_e64 v38, v38, 28, vcc
	v_cndmask_b32_e32 v37, v37, v4, vcc
	v_and_b32_e32 v39, 0x20000000, v36
	v_cmp_gt_i32_e64 s[8:9], 0, v38
	v_cmp_gt_f32_e64 s[10:11], v5, v37
	v_cmp_eq_u32_e32 vcc, 0, v39
	s_or_b64 s[8:9], s[8:9], s[10:11]
	s_and_b64 vcc, vcc, s[8:9]
	v_cndmask_b32_e64 v38, v38, 29, vcc
	v_cndmask_b32_e32 v37, v37, v5, vcc
	v_and_b32_e32 v39, 2.0, v36
	v_cmp_gt_i32_e64 s[8:9], 0, v38
	v_cmp_gt_f32_e64 s[10:11], v2, v37
	v_cmp_eq_u32_e32 vcc, 0, v39
	s_or_b64 s[8:9], s[8:9], s[10:11]
	s_and_b64 vcc, vcc, s[8:9]
	v_cndmask_b32_e64 v38, v38, 30, vcc
	v_cndmask_b32_e32 v37, v37, v2, vcc
	v_cmp_gt_i32_e64 s[8:9], 0, v38
	v_cmp_gt_f32_e64 s[10:11], v3, v37
	v_cmp_lt_i32_e32 vcc, -1, v36
	s_or_b64 s[8:9], s[8:9], s[10:11]
	s_and_b64 vcc, vcc, s[8:9]
	v_cndmask_b32_e64 v154, v38, 31, vcc
	v_lshlrev_b32_e64 v38, v154, 1
	v_or_b32_e32 v39, v38, v36
	v_and_b32_e32 v40, 1, v39
	v_cndmask_b32_e32 v37, v37, v3, vcc
	v_cmp_eq_u32_e32 vcc, 1, v40
	v_bitop3_b32 v42, v38, 2, v36 bitop3:0xc8
	v_bfe_i32 v41, v39, 0, 1
	v_cndmask_b32_e32 v40, v32, v198, vcc
	v_cmp_gt_f32_e64 s[8:9], v33, v40
	s_or_b64 vcc, vcc, s[8:9]
	v_cndmask_b32_e64 v43, 0, 1, vcc
	v_cndmask_b32_e32 v32, v32, v33, vcc
	v_cmp_eq_u32_e32 vcc, 0, v42
	s_nop 1
	v_cndmask_b32_e32 v32, v40, v32, vcc
	v_bitop3_b32 v40, v38, 4, v36 bitop3:0xc8
	v_cndmask_b32_e32 v33, v41, v43, vcc
	v_cmp_eq_u32_e32 vcc, 0, v40
	v_bitop3_b32 v40, v38, 3, v36 bitop3:0xc8
	v_cmp_eq_u32_e64 s[8:9], 3, v40
	v_cmp_gt_f32_e64 s[10:11], v30, v32
	s_or_b64 s[8:9], s[8:9], s[10:11]
	s_and_b64 vcc, vcc, s[8:9]
	v_cndmask_b32_e64 v33, v33, 2, vcc
	v_cndmask_b32_e32 v30, v32, v30, vcc
	v_bitop3_b32 v32, v38, 8, v36 bitop3:0xc8
	v_cmp_gt_i32_e64 s[8:9], 0, v33
	v_cmp_gt_f32_e64 s[10:11], v31, v30
	v_cmp_eq_u32_e32 vcc, 0, v32
	s_or_b64 s[8:9], s[8:9], s[10:11]
	s_and_b64 vcc, vcc, s[8:9]
	v_cndmask_b32_e64 v32, v33, 3, vcc
	v_cndmask_b32_e32 v30, v30, v31, vcc
	v_bitop3_b32 v31, v38, 16, v36 bitop3:0xc8
	v_cmp_gt_i32_e64 s[8:9], 0, v32
	v_cmp_gt_f32_e64 s[10:11], v28, v30
	v_cmp_eq_u32_e32 vcc, 0, v31
	s_or_b64 s[8:9], s[8:9], s[10:11]
	s_and_b64 vcc, vcc, s[8:9]
	v_cndmask_b32_e64 v31, v32, 4, vcc
	v_cndmask_b32_e32 v28, v30, v28, vcc
	v_bitop3_b32 v30, v38, 32, v36 bitop3:0xc8
	v_cmp_gt_i32_e64 s[8:9], 0, v31
	v_cmp_gt_f32_e64 s[10:11], v29, v28
	v_cmp_eq_u32_e32 vcc, 0, v30
	s_or_b64 s[8:9], s[8:9], s[10:11]
	s_and_b64 vcc, vcc, s[8:9]
	v_cndmask_b32_e64 v30, v31, 5, vcc
	v_cndmask_b32_e32 v28, v28, v29, vcc
	v_bitop3_b32 v29, v38, 64, v36 bitop3:0xc8
	v_cmp_gt_i32_e64 s[8:9], 0, v30
	v_cmp_gt_f32_e64 s[10:11], v26, v28
	v_cmp_eq_u32_e32 vcc, 0, v29
	s_or_b64 s[8:9], s[8:9], s[10:11]
	s_and_b64 vcc, vcc, s[8:9]
	v_cndmask_b32_e64 v29, v30, 6, vcc
	v_cndmask_b32_e32 v26, v28, v26, vcc
	v_bitop3_b32 v28, v38, s26, v36 bitop3:0xc8
	v_cmp_gt_i32_e64 s[8:9], 0, v29
	v_cmp_gt_f32_e64 s[10:11], v27, v26
	v_cmp_eq_u32_e32 vcc, 0, v28
	s_or_b64 s[8:9], s[8:9], s[10:11]
	s_and_b64 vcc, vcc, s[8:9]
	v_cndmask_b32_e64 v28, v29, 7, vcc
	v_cndmask_b32_e32 v26, v26, v27, vcc
	v_bitop3_b32 v27, v38, s27, v36 bitop3:0xc8
	v_cmp_gt_i32_e64 s[8:9], 0, v28
	v_cmp_gt_f32_e64 s[10:11], v24, v26
	v_cmp_eq_u32_e32 vcc, 0, v27
	s_or_b64 s[8:9], s[8:9], s[10:11]
	s_and_b64 vcc, vcc, s[8:9]
	v_cndmask_b32_e64 v27, v28, 8, vcc
	v_cndmask_b32_e32 v24, v26, v24, vcc
	v_bitop3_b32 v26, v38, s28, v36 bitop3:0xc8
	v_cmp_gt_i32_e64 s[8:9], 0, v27
	v_cmp_gt_f32_e64 s[10:11], v25, v24
	v_cmp_eq_u32_e32 vcc, 0, v26
	s_or_b64 s[8:9], s[8:9], s[10:11]
	s_and_b64 vcc, vcc, s[8:9]
	v_cndmask_b32_e64 v26, v27, 9, vcc
	v_cndmask_b32_e32 v24, v24, v25, vcc
	v_bitop3_b32 v25, v38, s29, v36 bitop3:0xc8
	v_cmp_gt_i32_e64 s[8:9], 0, v26
	v_cmp_gt_f32_e64 s[10:11], v22, v24
	v_cmp_eq_u32_e32 vcc, 0, v25
	s_or_b64 s[8:9], s[8:9], s[10:11]
	s_and_b64 vcc, vcc, s[8:9]
	v_cndmask_b32_e64 v25, v26, 10, vcc
	v_cndmask_b32_e32 v22, v24, v22, vcc
	v_bitop3_b32 v24, v38, s30, v36 bitop3:0xc8
	v_cmp_gt_i32_e64 s[8:9], 0, v25
	v_cmp_gt_f32_e64 s[10:11], v23, v22
	v_cmp_eq_u32_e32 vcc, 0, v24
	s_or_b64 s[8:9], s[8:9], s[10:11]
	s_and_b64 vcc, vcc, s[8:9]
	v_cndmask_b32_e64 v24, v25, 11, vcc
	v_cndmask_b32_e32 v22, v22, v23, vcc
	v_bitop3_b32 v23, v38, s31, v36 bitop3:0xc8
	v_cmp_gt_i32_e64 s[8:9], 0, v24
	v_cmp_gt_f32_e64 s[10:11], v20, v22
	v_cmp_eq_u32_e32 vcc, 0, v23
	s_or_b64 s[8:9], s[8:9], s[10:11]
	s_and_b64 vcc, vcc, s[8:9]
	v_cndmask_b32_e64 v23, v24, 12, vcc
	v_cndmask_b32_e32 v20, v22, v20, vcc
	v_bitop3_b32 v22, v38, s33, v36 bitop3:0xc8
	v_cmp_gt_i32_e64 s[8:9], 0, v23
	v_cmp_gt_f32_e64 s[10:11], v21, v20
	v_cmp_eq_u32_e32 vcc, 0, v22
	s_or_b64 s[8:9], s[8:9], s[10:11]
	s_and_b64 vcc, vcc, s[8:9]
	v_cndmask_b32_e64 v22, v23, 13, vcc
	v_cndmask_b32_e32 v20, v20, v21, vcc
	v_bitop3_b32 v21, v38, s34, v36 bitop3:0xc8
	v_cmp_gt_i32_e64 s[8:9], 0, v22
	v_cmp_gt_f32_e64 s[10:11], v18, v20
	v_cmp_eq_u32_e32 vcc, 0, v21
	s_or_b64 s[8:9], s[8:9], s[10:11]
	s_and_b64 vcc, vcc, s[8:9]
	v_cndmask_b32_e64 v21, v22, 14, vcc
	v_cndmask_b32_e32 v18, v20, v18, vcc
	v_bitop3_b32 v20, v38, s35, v36 bitop3:0xc8
	v_cmp_gt_i32_e64 s[8:9], 0, v21
	v_cmp_gt_f32_e64 s[10:11], v19, v18
	v_cmp_eq_u32_e32 vcc, 0, v20
	s_or_b64 s[8:9], s[8:9], s[10:11]
	s_and_b64 vcc, vcc, s[8:9]
	v_cndmask_b32_e64 v20, v21, 15, vcc
	v_cndmask_b32_e32 v18, v18, v19, vcc
	v_bitop3_b32 v19, v38, s36, v36 bitop3:0xc8
	v_cmp_gt_i32_e64 s[8:9], 0, v20
	v_cmp_gt_f32_e64 s[10:11], v16, v18
	v_cmp_eq_u32_e32 vcc, 0, v19
	s_or_b64 s[8:9], s[8:9], s[10:11]
	s_and_b64 vcc, vcc, s[8:9]
	v_cndmask_b32_e64 v19, v20, 16, vcc
	v_cndmask_b32_e32 v16, v18, v16, vcc
	v_bitop3_b32 v18, v38, s37, v36 bitop3:0xc8
	v_cmp_gt_i32_e64 s[8:9], 0, v19
	v_cmp_gt_f32_e64 s[10:11], v17, v16
	v_cmp_eq_u32_e32 vcc, 0, v18
	s_or_b64 s[8:9], s[8:9], s[10:11]
	s_and_b64 vcc, vcc, s[8:9]
	v_cndmask_b32_e64 v18, v19, 17, vcc
	v_cndmask_b32_e32 v16, v16, v17, vcc
	v_bitop3_b32 v17, v38, s38, v36 bitop3:0xc8
	v_cmp_gt_i32_e64 s[8:9], 0, v18
	v_cmp_gt_f32_e64 s[10:11], v14, v16
	v_cmp_eq_u32_e32 vcc, 0, v17
	s_or_b64 s[8:9], s[8:9], s[10:11]
	s_and_b64 vcc, vcc, s[8:9]
	v_cndmask_b32_e64 v17, v18, 18, vcc
	v_cndmask_b32_e32 v14, v16, v14, vcc
	v_bitop3_b32 v16, v38, s39, v36 bitop3:0xc8
	v_cmp_gt_i32_e64 s[8:9], 0, v17
	v_cmp_gt_f32_e64 s[10:11], v15, v14
	v_cmp_eq_u32_e32 vcc, 0, v16
	s_or_b64 s[8:9], s[8:9], s[10:11]
	s_and_b64 vcc, vcc, s[8:9]
	v_cndmask_b32_e64 v16, v17, 19, vcc
	v_cndmask_b32_e32 v14, v14, v15, vcc
	v_bitop3_b32 v15, v38, s40, v36 bitop3:0xc8
	v_cmp_gt_i32_e64 s[8:9], 0, v16
	v_cmp_gt_f32_e64 s[10:11], v12, v14
	v_cmp_eq_u32_e32 vcc, 0, v15
	s_or_b64 s[8:9], s[8:9], s[10:11]
	s_and_b64 vcc, vcc, s[8:9]
	v_cndmask_b32_e64 v15, v16, 20, vcc
	v_cndmask_b32_e32 v12, v14, v12, vcc
	v_bitop3_b32 v14, v38, s41, v36 bitop3:0xc8
	v_cmp_gt_i32_e64 s[8:9], 0, v15
	v_cmp_gt_f32_e64 s[10:11], v13, v12
	v_cmp_eq_u32_e32 vcc, 0, v14
	s_or_b64 s[8:9], s[8:9], s[10:11]
	s_and_b64 vcc, vcc, s[8:9]
	v_cndmask_b32_e64 v14, v15, 21, vcc
	v_cndmask_b32_e32 v12, v12, v13, vcc
	v_bitop3_b32 v13, v38, s42, v36 bitop3:0xc8
	v_cmp_gt_i32_e64 s[8:9], 0, v14
	v_cmp_gt_f32_e64 s[10:11], v10, v12
	v_cmp_eq_u32_e32 vcc, 0, v13
	s_or_b64 s[8:9], s[8:9], s[10:11]
	s_and_b64 vcc, vcc, s[8:9]
	v_cndmask_b32_e64 v13, v14, 22, vcc
	v_cndmask_b32_e32 v10, v12, v10, vcc
	v_bitop3_b32 v12, v38, s43, v36 bitop3:0xc8
	v_cmp_gt_i32_e64 s[8:9], 0, v13
	v_cmp_gt_f32_e64 s[10:11], v11, v10
	v_cmp_eq_u32_e32 vcc, 0, v12
	s_or_b64 s[8:9], s[8:9], s[10:11]
	s_and_b64 vcc, vcc, s[8:9]
	v_cndmask_b32_e64 v12, v13, 23, vcc
	v_cndmask_b32_e32 v10, v10, v11, vcc
	v_bitop3_b32 v11, v38, s44, v36 bitop3:0xc8
	v_cmp_gt_i32_e64 s[8:9], 0, v12
	v_cmp_gt_f32_e64 s[10:11], v8, v10
	v_cmp_eq_u32_e32 vcc, 0, v11
	s_or_b64 s[8:9], s[8:9], s[10:11]
	s_and_b64 vcc, vcc, s[8:9]
	v_cndmask_b32_e64 v11, v12, 24, vcc
	v_cndmask_b32_e32 v8, v10, v8, vcc
	v_bitop3_b32 v10, v38, s45, v36 bitop3:0xc8
	v_cmp_gt_i32_e64 s[8:9], 0, v11
	v_cmp_gt_f32_e64 s[10:11], v9, v8
	v_cmp_eq_u32_e32 vcc, 0, v10
	s_or_b64 s[8:9], s[8:9], s[10:11]
	s_and_b64 vcc, vcc, s[8:9]
	v_cndmask_b32_e64 v10, v11, 25, vcc
	v_cndmask_b32_e32 v8, v8, v9, vcc
	v_bitop3_b32 v9, v38, s46, v36 bitop3:0xc8
	v_cmp_gt_i32_e64 s[8:9], 0, v10
	v_cmp_gt_f32_e64 s[10:11], v6, v8
	v_cmp_eq_u32_e32 vcc, 0, v9
	s_or_b64 s[8:9], s[8:9], s[10:11]
	s_and_b64 vcc, vcc, s[8:9]
	v_cndmask_b32_e64 v9, v10, 26, vcc
	v_cndmask_b32_e32 v6, v8, v6, vcc
	v_bitop3_b32 v8, v38, s47, v36 bitop3:0xc8
	v_cmp_gt_i32_e64 s[8:9], 0, v9
	v_cmp_gt_f32_e64 s[10:11], v7, v6
	v_cmp_eq_u32_e32 vcc, 0, v8
	s_or_b64 s[8:9], s[8:9], s[10:11]
	s_and_b64 vcc, vcc, s[8:9]
	v_cndmask_b32_e64 v8, v9, 27, vcc
	v_cndmask_b32_e32 v6, v6, v7, vcc
	v_bitop3_b32 v7, v38, s48, v36 bitop3:0xc8
	v_cmp_gt_i32_e64 s[8:9], 0, v8
	v_cmp_gt_f32_e64 s[10:11], v4, v6
	v_cmp_eq_u32_e32 vcc, 0, v7
	s_or_b64 s[8:9], s[8:9], s[10:11]
	s_and_b64 vcc, vcc, s[8:9]
	v_cndmask_b32_e64 v7, v8, 28, vcc
	v_cndmask_b32_e32 v4, v6, v4, vcc
	v_bitop3_b32 v6, v38, s49, v36 bitop3:0xc8
	v_cmp_gt_i32_e64 s[8:9], 0, v7
	v_cmp_gt_f32_e64 s[10:11], v5, v4
	v_cmp_eq_u32_e32 vcc, 0, v6
	s_or_b64 s[8:9], s[8:9], s[10:11]
	s_and_b64 vcc, vcc, s[8:9]
	v_cndmask_b32_e64 v6, v7, 29, vcc
	v_cndmask_b32_e32 v4, v4, v5, vcc
	v_bitop3_b32 v5, v38, 2.0, v36 bitop3:0xc8
	v_cmp_gt_i32_e64 s[8:9], 0, v6
	v_cmp_gt_f32_e64 s[10:11], v2, v4
	v_cmp_eq_u32_e32 vcc, 0, v5
	s_or_b64 s[8:9], s[8:9], s[10:11]
	s_and_b64 vcc, vcc, s[8:9]
	v_cndmask_b32_e32 v2, v4, v2, vcc
	v_sub_f32_e32 v4, v35, v34
	v_cndmask_b32_e64 v5, v6, 30, vcc
	v_mul_f32_e32 v6, 0x3fb8aa3b, v4
	v_fma_f32 v7, v4, s50, -v6
	v_rndne_f32_e32 v8, v6
	v_fmac_f32_e32 v7, 0x32a5705f, v4
	v_sub_f32_e32 v6, v6, v8
	v_add_f32_e32 v6, v6, v7
	v_cmp_gt_i32_e64 s[8:9], 0, v5
	v_cmp_gt_f32_e64 s[10:11], v3, v2
	v_exp_f32_e32 v6, v6
	v_cvt_i32_f32_e32 v7, v8
	v_cmp_lt_i32_e32 vcc, -1, v39
	s_or_b64 s[8:9], s[8:9], s[10:11]
	s_and_b64 vcc, vcc, s[8:9]
	v_cndmask_b32_e64 v158, v5, 31, vcc
	v_sub_f32_e32 v5, v37, v34
	v_cndmask_b32_e32 v2, v2, v3, vcc
	v_ldexp_f32 v3, v6, v7
	v_mul_f32_e32 v6, 0x3fb8aa3b, v5
	v_fma_f32 v7, v5, s50, -v6
	v_rndne_f32_e32 v8, v6
	v_fmac_f32_e32 v7, 0x32a5705f, v5
	v_sub_f32_e32 v6, v6, v8
	v_add_f32_e32 v6, v6, v7
	v_exp_f32_e32 v6, v6
	v_cvt_i32_f32_e32 v7, v8
	v_cmp_ngt_f32_e32 vcc, s51, v4
	v_sub_f32_e32 v2, v2, v34
	s_nop 0
	v_cndmask_b32_e32 v3, 0, v3, vcc
	v_cmp_nlt_f32_e32 vcc, s52, v4
	s_nop 1
	v_cndmask_b32_e32 v4, v199, v3, vcc
	v_ldexp_f32 v3, v6, v7
	v_mul_f32_e32 v6, 0x3fb8aa3b, v2
	v_fma_f32 v7, v2, s50, -v6
	v_rndne_f32_e32 v8, v6
	v_fmac_f32_e32 v7, 0x32a5705f, v2
	v_sub_f32_e32 v6, v6, v8
	v_add_f32_e32 v6, v6, v7
	v_exp_f32_e32 v6, v6
	v_cvt_i32_f32_e32 v7, v8
	v_cmp_ngt_f32_e32 vcc, s51, v5
	s_nop 1
	v_cndmask_b32_e32 v3, 0, v3, vcc
	v_cmp_nlt_f32_e32 vcc, s52, v5
	v_ldexp_f32 v5, v6, v7
	s_nop 0
	v_cndmask_b32_e32 v3, v199, v3, vcc
	v_cmp_ngt_f32_e32 vcc, s51, v2
	s_nop 1
	v_cndmask_b32_e32 v5, 0, v5, vcc
	v_cmp_nlt_f32_e32 vcc, s52, v2
	s_nop 1
	v_cndmask_b32_e32 v2, v199, v5, vcc
	v_add_f32_e32 v5, 1.0, v4
	v_add_f32_e32 v5, v5, v3
	v_add_f32_e32 v5, v5, v2
	v_div_scale_f32 v6, s[8:9], v5, v5, 1.0
	v_rcp_f32_e32 v7, v6
	s_nop 0
	v_fma_f32 v8, -v6, v7, 1.0
	v_fmac_f32_e32 v7, v8, v7
	v_div_scale_f32 v8, vcc, 1.0, v5, 1.0
	v_mul_f32_e32 v9, v8, v7
	v_fma_f32 v10, -v6, v9, v8
	v_fmac_f32_e32 v9, v10, v7
	v_fma_f32 v6, -v6, v9, v8
	v_lshl_add_u32 v8, v146, 2, s1
	ds_add_rtn_u32 v205, v8, v197
	v_lshl_add_u32 v8, v150, 2, s1
	ds_add_rtn_u32 v207, v8, v197
	v_lshl_add_u32 v8, v154, 2, s1
	ds_add_rtn_u32 v208, v8, v197
	v_lshl_add_u32 v8, v158, 2, s1
	ds_add_rtn_u32 v209, v8, v197
	v_div_fmas_f32 v6, v6, v7, v9
	v_div_fixup_f32 v160, v6, v5, 1.0
	v_mul_f32_e32 v206, v4, v160
	v_pk_mul_f32 v[164:165], v[2:3], v[160:161] op_sel_hi:[1,0]
.LBB0_437:
	s_or_b64 exec, exec, s[20:21]
	s_waitcnt lgkmcnt(0)
	v_add_u32_e32 v166, 16, v166
	v_ashrrev_i32_e32 v167, 31, v166
	v_lshlrev_b64 v[2:3], 11, v[166:167]
	v_lshl_add_u64 v[2:3], v[140:141], 0, v[2:3]
	global_load_dwordx4 v[126:129], v[2:3], off nt
	global_load_dwordx4 v[122:125], v[2:3], off offset:64 nt
	global_load_dwordx4 v[118:121], v[2:3], off offset:128 nt
	global_load_dwordx4 v[114:117], v[2:3], off offset:192 nt
	global_load_dwordx4 v[110:113], v[2:3], off offset:256 nt
	global_load_dwordx4 v[106:109], v[2:3], off offset:320 nt
	global_load_dwordx4 v[102:105], v[2:3], off offset:384 nt
	global_load_dwordx4 v[98:101], v[2:3], off offset:448 nt
	global_load_dwordx4 v[94:97], v[2:3], off offset:512 nt
	global_load_dwordx4 v[90:93], v[2:3], off offset:576 nt
	global_load_dwordx4 v[86:89], v[2:3], off offset:640 nt
	global_load_dwordx4 v[82:85], v[2:3], off offset:704 nt
	global_load_dwordx4 v[78:81], v[2:3], off offset:768 nt
	global_load_dwordx4 v[74:77], v[2:3], off offset:832 nt
	global_load_dwordx4 v[70:73], v[2:3], off offset:896 nt
	global_load_dwordx4 v[66:69], v[2:3], off offset:960 nt
	global_load_dwordx4 v[62:65], v[2:3], off offset:1024 nt
	global_load_dwordx4 v[58:61], v[2:3], off offset:1088 nt
	global_load_dwordx4 v[54:57], v[2:3], off offset:1152 nt
	global_load_dwordx4 v[50:53], v[2:3], off offset:1216 nt
	global_load_dwordx4 v[46:49], v[2:3], off offset:1280 nt
	global_load_dwordx4 v[42:45], v[2:3], off offset:1344 nt
	global_load_dwordx4 v[38:41], v[2:3], off offset:1408 nt
	global_load_dwordx4 v[34:37], v[2:3], off offset:1472 nt
	global_load_dwordx4 v[30:33], v[2:3], off offset:1536 nt
	global_load_dwordx4 v[26:29], v[2:3], off offset:1600 nt
	global_load_dwordx4 v[22:25], v[2:3], off offset:1664 nt
	global_load_dwordx4 v[18:21], v[2:3], off offset:1728 nt
	global_load_dwordx4 v[14:17], v[2:3], off offset:1792 nt
	global_load_dwordx4 v[10:13], v[2:3], off offset:1856 nt
	global_load_dwordx4 v[6:9], v[2:3], off offset:1920 nt
	s_nop 0
	global_load_dwordx4 v[2:5], v[2:3], off offset:1984 nt
	ds_read_b128 v[130:133], v175 offset:33024
	ds_read_b128 v[134:137], v175 offset:33088
	ds_read_b128 v[210:213], v175
	ds_read_b128 v[214:217], v175 offset:64
	ds_read_b128 v[218:221], v174 offset:33024
	ds_read_b128 v[222:225], v174 offset:33088
	ds_read_b128 v[226:229], v174
	ds_read_b128 v[230:233], v174 offset:64
	v_lshlrev_b64 v[166:167], 10, v[166:167]
	s_waitcnt vmcnt(31) lgkmcnt(1)
	v_mfma_f32_16x16x32_bf16 v[226:229], v[126:129], v[226:229], 0
	v_and_b32_e32 v147, 0xffff0000, v126
	v_and_b32_e32 v151, 0xffff0000, v127
	v_lshlrev_b32_e32 v145, 16, v126
	v_mfma_f32_16x16x32_bf16 v[218:221], v[126:129], v[218:221], 0
	v_lshlrev_b32_e32 v149, 16, v127
	v_and_b32_e32 v155, 0xffff0000, v128
	v_mul_f32_e32 v147, v147, v147
	v_mul_f32_e32 v151, v151, v151
	v_mfma_f32_16x16x32_bf16 v[210:213], v[126:129], v[210:213], v[226:229]
	v_lshlrev_b32_e32 v153, 16, v128
	v_and_b32_e32 v159, 0xffff0000, v129
	v_mul_f32_e32 v155, v155, v155
	v_mfma_f32_16x16x32_bf16 v[130:133], v[126:129], v[130:133], v[218:221]
	v_fmac_f32_e32 v147, v145, v145
	v_fmac_f32_e32 v151, v149, v149
	v_lshlrev_b32_e32 v157, 16, v129
	s_waitcnt vmcnt(30)
	v_and_b32_e32 v169, 0xffff0000, v122
	v_mul_f32_e32 v159, v159, v159
	v_fmac_f32_e32 v155, v153, v153
	v_add_f32_e32 v145, v147, v151
	v_lshlrev_b32_e32 v168, 16, v122
	v_and_b32_e32 v235, 0xffff0000, v123
	v_mul_f32_e32 v169, v169, v169
	v_fmac_f32_e32 v159, v157, v157
	v_add_f32_e32 v145, v155, v145
	v_lshlrev_b32_e32 v234, 16, v123
	v_and_b32_e32 v237, 0xffff0000, v124
	v_mul_f32_e32 v235, v235, v235
	v_fmac_f32_e32 v169, v168, v168
	s_waitcnt lgkmcnt(0)
	v_mfma_f32_16x16x32_bf16 v[210:213], v[122:125], v[230:233], v[210:213]
	v_add_f32_e32 v145, v159, v145
	v_lshlrev_b32_e32 v236, 16, v124
	v_and_b32_e32 v239, 0xffff0000, v125
	v_mfma_f32_16x16x32_bf16 v[130:133], v[122:125], v[222:225], v[130:133]
	v_mul_f32_e32 v237, v237, v237
	v_fmac_f32_e32 v235, v234, v234
	v_add_f32_e32 v145, v169, v145
	v_lshlrev_b32_e32 v238, 16, v125
	v_mul_f32_e32 v239, v239, v239
	v_fmac_f32_e32 v237, v236, v236
	v_add_f32_e32 v145, v235, v145
	v_fmac_f32_e32 v239, v238, v238
	v_add_f32_e32 v145, v237, v145
	v_mfma_f32_16x16x32_bf16 v[210:213], v[122:125], v[214:217], v[210:213]
	v_add_f32_e32 v145, v239, v145
	v_mfma_f32_16x16x32_bf16 v[130:133], v[122:125], v[134:137], v[130:133]
	s_waitcnt vmcnt(29)
	v_and_b32_e32 v149, 0xffff0000, v118
	v_lshlrev_b32_e32 v147, 16, v118
	v_mul_f32_e32 v149, v149, v149
	v_fmac_f32_e32 v149, v147, v147
	v_add_f32_e32 v145, v149, v145
	v_and_b32_e32 v149, 0xffff0000, v119
	v_lshlrev_b32_e32 v147, 16, v119
	v_mul_f32_e32 v149, v149, v149
	v_fmac_f32_e32 v149, v147, v147
	v_add_f32_e32 v145, v149, v145
	v_and_b32_e32 v149, 0xffff0000, v120
	v_lshlrev_b32_e32 v147, 16, v120
	v_mul_f32_e32 v149, v149, v149
	v_fmac_f32_e32 v149, v147, v147
	v_add_f32_e32 v145, v149, v145
	v_and_b32_e32 v149, 0xffff0000, v121
	ds_read_b128 v[134:137], v174 offset:128
	ds_read_b128 v[214:217], v174 offset:33152
	ds_read_b128 v[218:221], v175 offset:128
	ds_read_b128 v[222:225], v175 offset:33152
	ds_read_b128 v[226:229], v174 offset:192
	v_lshlrev_b32_e32 v147, 16, v121
	v_mul_f32_e32 v149, v149, v149
	s_waitcnt lgkmcnt(4)
	v_mfma_f32_16x16x32_bf16 v[134:137], v[118:121], v[134:137], v[210:213]
	v_fmac_f32_e32 v149, v147, v147
	v_add_f32_e32 v145, v149, v145
	s_waitcnt vmcnt(28)
	v_and_b32_e32 v149, 0xffff0000, v114
	s_waitcnt lgkmcnt(3)
	v_mfma_f32_16x16x32_bf16 v[130:133], v[118:121], v[214:217], v[130:133]
	v_lshlrev_b32_e32 v147, 16, v114
	v_mul_f32_e32 v149, v149, v149
	v_fmac_f32_e32 v149, v147, v147
	s_waitcnt lgkmcnt(2)
	v_mfma_f32_16x16x32_bf16 v[134:137], v[118:121], v[218:221], v[134:137]
	ds_read_b128 v[218:221], v174 offset:33216
	ds_read_b128 v[214:217], v175 offset:33216
	v_add_f32_e32 v145, v149, v145
	v_and_b32_e32 v149, 0xffff0000, v115
	s_waitcnt lgkmcnt(3)
	v_mfma_f32_16x16x32_bf16 v[130:133], v[118:121], v[222:225], v[130:133]
	v_lshlrev_b32_e32 v147, 16, v115
	v_mul_f32_e32 v149, v149, v149
	v_fmac_f32_e32 v149, v147, v147
	v_add_f32_e32 v145, v149, v145
	v_and_b32_e32 v149, 0xffff0000, v116
	ds_read_b128 v[210:213], v175 offset:192
	v_lshlrev_b32_e32 v147, 16, v116
	v_mul_f32_e32 v149, v149, v149
	s_waitcnt lgkmcnt(3)
	v_mfma_f32_16x16x32_bf16 v[134:137], v[114:117], v[226:229], v[134:137]
	v_fmac_f32_e32 v149, v147, v147
	v_add_f32_e32 v145, v149, v145
	v_and_b32_e32 v149, 0xffff0000, v117
	s_waitcnt lgkmcnt(2)
	v_mfma_f32_16x16x32_bf16 v[130:133], v[114:117], v[218:221], v[130:133]
	v_lshlrev_b32_e32 v147, 16, v117
	v_mul_f32_e32 v149, v149, v149
	v_fmac_f32_e32 v149, v147, v147
	s_waitcnt lgkmcnt(0)
	v_mfma_f32_16x16x32_bf16 v[134:137], v[114:117], v[210:213], v[134:137]
	v_add_f32_e32 v145, v149, v145
	v_mfma_f32_16x16x32_bf16 v[130:133], v[114:117], v[214:217], v[130:133]
	s_waitcnt vmcnt(27)
	v_and_b32_e32 v149, 0xffff0000, v110
	v_lshlrev_b32_e32 v147, 16, v110
	v_mul_f32_e32 v149, v149, v149
	v_fmac_f32_e32 v149, v147, v147
	v_add_f32_e32 v145, v149, v145
	v_and_b32_e32 v149, 0xffff0000, v111
	v_lshlrev_b32_e32 v147, 16, v111
	v_mul_f32_e32 v149, v149, v149
	v_fmac_f32_e32 v149, v147, v147
	v_add_f32_e32 v145, v149, v145
	v_and_b32_e32 v149, 0xffff0000, v112
	v_lshlrev_b32_e32 v147, 16, v112
	v_mul_f32_e32 v149, v149, v149
	v_fmac_f32_e32 v149, v147, v147
	v_add_f32_e32 v145, v149, v145
	v_and_b32_e32 v149, 0xffff0000, v113
	ds_read_b128 v[210:213], v174 offset:256
	ds_read_b128 v[214:217], v174 offset:33280
	ds_read_b128 v[218:221], v175 offset:256
	ds_read_b128 v[222:225], v175 offset:33280
	ds_read_b128 v[226:229], v174 offset:320
	v_lshlrev_b32_e32 v147, 16, v113
	v_mul_f32_e32 v149, v149, v149
	s_waitcnt lgkmcnt(4)
	v_mfma_f32_16x16x32_bf16 v[134:137], v[110:113], v[210:213], v[134:137]
	v_fmac_f32_e32 v149, v147, v147
	v_add_f32_e32 v145, v149, v145
	s_waitcnt vmcnt(26)
	v_and_b32_e32 v149, 0xffff0000, v106
	s_waitcnt lgkmcnt(3)
	v_mfma_f32_16x16x32_bf16 v[130:133], v[110:113], v[214:217], v[130:133]
	v_lshlrev_b32_e32 v147, 16, v106
	v_mul_f32_e32 v149, v149, v149
	v_fmac_f32_e32 v149, v147, v147
	s_waitcnt lgkmcnt(2)
	v_mfma_f32_16x16x32_bf16 v[134:137], v[110:113], v[218:221], v[134:137]
	ds_read_b128 v[218:221], v174 offset:33344
	ds_read_b128 v[214:217], v175 offset:33344
	v_add_f32_e32 v145, v149, v145
	v_and_b32_e32 v149, 0xffff0000, v107
	s_waitcnt lgkmcnt(3)
	v_mfma_f32_16x16x32_bf16 v[130:133], v[110:113], v[222:225], v[130:133]
	v_lshlrev_b32_e32 v147, 16, v107
	v_mul_f32_e32 v149, v149, v149
	v_fmac_f32_e32 v149, v147, v147
	v_add_f32_e32 v145, v149, v145
	v_and_b32_e32 v149, 0xffff0000, v108
	ds_read_b128 v[210:213], v175 offset:320
	v_lshlrev_b32_e32 v147, 16, v108
	v_mul_f32_e32 v149, v149, v149
	s_waitcnt lgkmcnt(3)
	v_mfma_f32_16x16x32_bf16 v[134:137], v[106:109], v[226:229], v[134:137]
	v_fmac_f32_e32 v149, v147, v147
	v_add_f32_e32 v145, v149, v145
	v_and_b32_e32 v149, 0xffff0000, v109
	s_waitcnt lgkmcnt(2)
	v_mfma_f32_16x16x32_bf16 v[130:133], v[106:109], v[218:221], v[130:133]
	v_lshlrev_b32_e32 v147, 16, v109
	v_mul_f32_e32 v149, v149, v149
	v_fmac_f32_e32 v149, v147, v147
	s_waitcnt lgkmcnt(0)
	v_mfma_f32_16x16x32_bf16 v[134:137], v[106:109], v[210:213], v[134:137]
	v_add_f32_e32 v145, v149, v145
	v_mfma_f32_16x16x32_bf16 v[130:133], v[106:109], v[214:217], v[130:133]
	s_waitcnt vmcnt(25)
	v_and_b32_e32 v149, 0xffff0000, v102
	v_lshlrev_b32_e32 v147, 16, v102
	v_mul_f32_e32 v149, v149, v149
	v_fmac_f32_e32 v149, v147, v147
	v_add_f32_e32 v145, v149, v145
	v_and_b32_e32 v149, 0xffff0000, v103
	v_lshlrev_b32_e32 v147, 16, v103
	v_mul_f32_e32 v149, v149, v149
	v_fmac_f32_e32 v149, v147, v147
	v_add_f32_e32 v145, v149, v145
	v_and_b32_e32 v149, 0xffff0000, v104
	v_lshlrev_b32_e32 v147, 16, v104
	v_mul_f32_e32 v149, v149, v149
	v_fmac_f32_e32 v149, v147, v147
	v_add_f32_e32 v145, v149, v145
	v_and_b32_e32 v149, 0xffff0000, v105
	ds_read_b128 v[210:213], v174 offset:384
	ds_read_b128 v[214:217], v174 offset:33408
	ds_read_b128 v[218:221], v175 offset:384
	ds_read_b128 v[222:225], v175 offset:33408
	ds_read_b128 v[226:229], v174 offset:448
	v_lshlrev_b32_e32 v147, 16, v105
	v_mul_f32_e32 v149, v149, v149
	s_waitcnt lgkmcnt(4)
	v_mfma_f32_16x16x32_bf16 v[134:137], v[102:105], v[210:213], v[134:137]
	v_fmac_f32_e32 v149, v147, v147
	v_add_f32_e32 v145, v149, v145
	s_waitcnt vmcnt(24)
	v_and_b32_e32 v149, 0xffff0000, v98
	s_waitcnt lgkmcnt(3)
	v_mfma_f32_16x16x32_bf16 v[130:133], v[102:105], v[214:217], v[130:133]
	v_lshlrev_b32_e32 v147, 16, v98
	v_mul_f32_e32 v149, v149, v149
	v_fmac_f32_e32 v149, v147, v147
	s_waitcnt lgkmcnt(2)
	v_mfma_f32_16x16x32_bf16 v[134:137], v[102:105], v[218:221], v[134:137]
	ds_read_b128 v[218:221], v174 offset:33472
	ds_read_b128 v[214:217], v175 offset:33472
	v_add_f32_e32 v145, v149, v145
	v_and_b32_e32 v149, 0xffff0000, v99
	s_waitcnt lgkmcnt(3)
	v_mfma_f32_16x16x32_bf16 v[130:133], v[102:105], v[222:225], v[130:133]
	v_lshlrev_b32_e32 v147, 16, v99
	v_mul_f32_e32 v149, v149, v149
	v_fmac_f32_e32 v149, v147, v147
	v_add_f32_e32 v145, v149, v145
	v_and_b32_e32 v149, 0xffff0000, v100
	ds_read_b128 v[210:213], v175 offset:448
	v_lshlrev_b32_e32 v147, 16, v100
	v_mul_f32_e32 v149, v149, v149
	s_waitcnt lgkmcnt(3)
	v_mfma_f32_16x16x32_bf16 v[134:137], v[98:101], v[226:229], v[134:137]
	v_fmac_f32_e32 v149, v147, v147
	v_add_f32_e32 v145, v149, v145
	v_and_b32_e32 v149, 0xffff0000, v101
	s_waitcnt lgkmcnt(2)
	v_mfma_f32_16x16x32_bf16 v[130:133], v[98:101], v[218:221], v[130:133]
	v_lshlrev_b32_e32 v147, 16, v101
	v_mul_f32_e32 v149, v149, v149
	v_fmac_f32_e32 v149, v147, v147
	s_waitcnt lgkmcnt(0)
	v_mfma_f32_16x16x32_bf16 v[134:137], v[98:101], v[210:213], v[134:137]
	v_add_f32_e32 v145, v149, v145
	v_mfma_f32_16x16x32_bf16 v[130:133], v[98:101], v[214:217], v[130:133]
	s_waitcnt vmcnt(23)
	v_and_b32_e32 v149, 0xffff0000, v94
	v_lshlrev_b32_e32 v147, 16, v94
	v_mul_f32_e32 v149, v149, v149
	v_fmac_f32_e32 v149, v147, v147
	v_add_f32_e32 v145, v149, v145
	v_and_b32_e32 v149, 0xffff0000, v95
	v_lshlrev_b32_e32 v147, 16, v95
	v_mul_f32_e32 v149, v149, v149
	v_fmac_f32_e32 v149, v147, v147
	v_add_f32_e32 v145, v149, v145
	v_and_b32_e32 v149, 0xffff0000, v96
	v_lshlrev_b32_e32 v147, 16, v96
	v_mul_f32_e32 v149, v149, v149
	v_fmac_f32_e32 v149, v147, v147
	v_add_f32_e32 v145, v149, v145
	v_and_b32_e32 v149, 0xffff0000, v97
	ds_read_b128 v[210:213], v174 offset:512
	ds_read_b128 v[214:217], v174 offset:33536
	ds_read_b128 v[218:221], v175 offset:512
	ds_read_b128 v[222:225], v175 offset:33536
	ds_read_b128 v[226:229], v174 offset:576
	v_lshlrev_b32_e32 v147, 16, v97
	v_mul_f32_e32 v149, v149, v149
	s_waitcnt lgkmcnt(4)
	v_mfma_f32_16x16x32_bf16 v[134:137], v[94:97], v[210:213], v[134:137]
	v_fmac_f32_e32 v149, v147, v147
	v_add_f32_e32 v145, v149, v145
	s_waitcnt vmcnt(22)
	v_and_b32_e32 v149, 0xffff0000, v90
	s_waitcnt lgkmcnt(3)
	v_mfma_f32_16x16x32_bf16 v[130:133], v[94:97], v[214:217], v[130:133]
	v_lshlrev_b32_e32 v147, 16, v90
	v_mul_f32_e32 v149, v149, v149
	v_fmac_f32_e32 v149, v147, v147
	s_waitcnt lgkmcnt(2)
	v_mfma_f32_16x16x32_bf16 v[134:137], v[94:97], v[218:221], v[134:137]
	ds_read_b128 v[218:221], v174 offset:33600
	ds_read_b128 v[214:217], v175 offset:33600
	v_add_f32_e32 v145, v149, v145
	v_and_b32_e32 v149, 0xffff0000, v91
	s_waitcnt lgkmcnt(3)
	v_mfma_f32_16x16x32_bf16 v[130:133], v[94:97], v[222:225], v[130:133]
	v_lshlrev_b32_e32 v147, 16, v91
	v_mul_f32_e32 v149, v149, v149
	v_fmac_f32_e32 v149, v147, v147
	v_add_f32_e32 v145, v149, v145
	v_and_b32_e32 v149, 0xffff0000, v92
	ds_read_b128 v[210:213], v175 offset:576
	v_lshlrev_b32_e32 v147, 16, v92
	v_mul_f32_e32 v149, v149, v149
	s_waitcnt lgkmcnt(3)
	v_mfma_f32_16x16x32_bf16 v[134:137], v[90:93], v[226:229], v[134:137]
	v_fmac_f32_e32 v149, v147, v147
	v_add_f32_e32 v145, v149, v145
	v_and_b32_e32 v149, 0xffff0000, v93
	s_waitcnt lgkmcnt(2)
	v_mfma_f32_16x16x32_bf16 v[130:133], v[90:93], v[218:221], v[130:133]
	v_lshlrev_b32_e32 v147, 16, v93
	v_mul_f32_e32 v149, v149, v149
	v_fmac_f32_e32 v149, v147, v147
	s_waitcnt lgkmcnt(0)
	v_mfma_f32_16x16x32_bf16 v[134:137], v[90:93], v[210:213], v[134:137]
	v_add_f32_e32 v145, v149, v145
	v_mfma_f32_16x16x32_bf16 v[130:133], v[90:93], v[214:217], v[130:133]
	s_waitcnt vmcnt(21)
	v_and_b32_e32 v149, 0xffff0000, v86
	v_lshlrev_b32_e32 v147, 16, v86
	v_mul_f32_e32 v149, v149, v149
	v_fmac_f32_e32 v149, v147, v147
	v_add_f32_e32 v145, v149, v145
	v_and_b32_e32 v149, 0xffff0000, v87
	v_lshlrev_b32_e32 v147, 16, v87
	v_mul_f32_e32 v149, v149, v149
	v_fmac_f32_e32 v149, v147, v147
	v_add_f32_e32 v145, v149, v145
	v_and_b32_e32 v149, 0xffff0000, v88
	v_lshlrev_b32_e32 v147, 16, v88
	v_mul_f32_e32 v149, v149, v149
	v_fmac_f32_e32 v149, v147, v147
	v_add_f32_e32 v145, v149, v145
	v_and_b32_e32 v149, 0xffff0000, v89
	ds_read_b128 v[210:213], v174 offset:640
	ds_read_b128 v[214:217], v174 offset:33664
	ds_read_b128 v[218:221], v175 offset:640
	ds_read_b128 v[222:225], v175 offset:33664
	ds_read_b128 v[226:229], v174 offset:704
	v_lshlrev_b32_e32 v147, 16, v89
	v_mul_f32_e32 v149, v149, v149
	s_waitcnt lgkmcnt(4)
	v_mfma_f32_16x16x32_bf16 v[134:137], v[86:89], v[210:213], v[134:137]
	v_fmac_f32_e32 v149, v147, v147
	v_add_f32_e32 v145, v149, v145
	s_waitcnt vmcnt(20)
	v_and_b32_e32 v149, 0xffff0000, v82
	s_waitcnt lgkmcnt(3)
	v_mfma_f32_16x16x32_bf16 v[130:133], v[86:89], v[214:217], v[130:133]
	v_lshlrev_b32_e32 v147, 16, v82
	v_mul_f32_e32 v149, v149, v149
	v_fmac_f32_e32 v149, v147, v147
	s_waitcnt lgkmcnt(2)
	v_mfma_f32_16x16x32_bf16 v[134:137], v[86:89], v[218:221], v[134:137]
	ds_read_b128 v[218:221], v174 offset:33728
	ds_read_b128 v[214:217], v175 offset:33728
	v_add_f32_e32 v145, v149, v145
	v_and_b32_e32 v149, 0xffff0000, v83
	s_waitcnt lgkmcnt(3)
	v_mfma_f32_16x16x32_bf16 v[130:133], v[86:89], v[222:225], v[130:133]
	v_lshlrev_b32_e32 v147, 16, v83
	v_mul_f32_e32 v149, v149, v149
	v_fmac_f32_e32 v149, v147, v147
	v_add_f32_e32 v145, v149, v145
	v_and_b32_e32 v149, 0xffff0000, v84
	ds_read_b128 v[210:213], v175 offset:704
	v_lshlrev_b32_e32 v147, 16, v84
	v_mul_f32_e32 v149, v149, v149
	s_waitcnt lgkmcnt(3)
	v_mfma_f32_16x16x32_bf16 v[134:137], v[82:85], v[226:229], v[134:137]
	v_fmac_f32_e32 v149, v147, v147
	v_add_f32_e32 v145, v149, v145
	v_and_b32_e32 v149, 0xffff0000, v85
	s_waitcnt lgkmcnt(2)
	v_mfma_f32_16x16x32_bf16 v[130:133], v[82:85], v[218:221], v[130:133]
	v_lshlrev_b32_e32 v147, 16, v85
	v_mul_f32_e32 v149, v149, v149
	v_fmac_f32_e32 v149, v147, v147
	s_waitcnt lgkmcnt(0)
	v_mfma_f32_16x16x32_bf16 v[134:137], v[82:85], v[210:213], v[134:137]
	v_add_f32_e32 v145, v149, v145
	v_mfma_f32_16x16x32_bf16 v[130:133], v[82:85], v[214:217], v[130:133]
	s_waitcnt vmcnt(19)
	v_and_b32_e32 v149, 0xffff0000, v78
	v_lshlrev_b32_e32 v147, 16, v78
	v_mul_f32_e32 v149, v149, v149
	v_fmac_f32_e32 v149, v147, v147
	v_add_f32_e32 v145, v149, v145
	v_and_b32_e32 v149, 0xffff0000, v79
	v_lshlrev_b32_e32 v147, 16, v79
	v_mul_f32_e32 v149, v149, v149
	v_fmac_f32_e32 v149, v147, v147
	v_add_f32_e32 v145, v149, v145
	v_and_b32_e32 v149, 0xffff0000, v80
	v_lshlrev_b32_e32 v147, 16, v80
	v_mul_f32_e32 v149, v149, v149
	v_fmac_f32_e32 v149, v147, v147
	v_add_f32_e32 v145, v149, v145
	v_and_b32_e32 v149, 0xffff0000, v81
	ds_read_b128 v[210:213], v174 offset:768
	ds_read_b128 v[214:217], v174 offset:33792
	ds_read_b128 v[218:221], v175 offset:768
	ds_read_b128 v[222:225], v175 offset:33792
	ds_read_b128 v[226:229], v174 offset:832
	v_lshlrev_b32_e32 v147, 16, v81
	v_mul_f32_e32 v149, v149, v149
	s_waitcnt lgkmcnt(4)
	v_mfma_f32_16x16x32_bf16 v[134:137], v[78:81], v[210:213], v[134:137]
	v_fmac_f32_e32 v149, v147, v147
	v_add_f32_e32 v145, v149, v145
	s_waitcnt vmcnt(18)
	v_and_b32_e32 v149, 0xffff0000, v74
	s_waitcnt lgkmcnt(3)
	v_mfma_f32_16x16x32_bf16 v[130:133], v[78:81], v[214:217], v[130:133]
	v_lshlrev_b32_e32 v147, 16, v74
	v_mul_f32_e32 v149, v149, v149
	v_fmac_f32_e32 v149, v147, v147
	s_waitcnt lgkmcnt(2)
	v_mfma_f32_16x16x32_bf16 v[134:137], v[78:81], v[218:221], v[134:137]
	ds_read_b128 v[218:221], v174 offset:33856
	ds_read_b128 v[214:217], v175 offset:33856
	v_add_f32_e32 v145, v149, v145
	v_and_b32_e32 v149, 0xffff0000, v75
	s_waitcnt lgkmcnt(3)
	v_mfma_f32_16x16x32_bf16 v[130:133], v[78:81], v[222:225], v[130:133]
	v_lshlrev_b32_e32 v147, 16, v75
	v_mul_f32_e32 v149, v149, v149
	v_fmac_f32_e32 v149, v147, v147
	v_add_f32_e32 v145, v149, v145
	v_and_b32_e32 v149, 0xffff0000, v76
	ds_read_b128 v[210:213], v175 offset:832
	v_lshlrev_b32_e32 v147, 16, v76
	v_mul_f32_e32 v149, v149, v149
	s_waitcnt lgkmcnt(3)
	v_mfma_f32_16x16x32_bf16 v[134:137], v[74:77], v[226:229], v[134:137]
	v_fmac_f32_e32 v149, v147, v147
	v_add_f32_e32 v145, v149, v145
	v_and_b32_e32 v149, 0xffff0000, v77
	s_waitcnt lgkmcnt(2)
	v_mfma_f32_16x16x32_bf16 v[130:133], v[74:77], v[218:221], v[130:133]
	v_lshlrev_b32_e32 v147, 16, v77
	v_mul_f32_e32 v149, v149, v149
	v_fmac_f32_e32 v149, v147, v147
	s_waitcnt lgkmcnt(0)
	v_mfma_f32_16x16x32_bf16 v[134:137], v[74:77], v[210:213], v[134:137]
	v_add_f32_e32 v145, v149, v145
	v_mfma_f32_16x16x32_bf16 v[130:133], v[74:77], v[214:217], v[130:133]
	s_waitcnt vmcnt(17)
	v_and_b32_e32 v149, 0xffff0000, v70
	v_lshlrev_b32_e32 v147, 16, v70
	v_mul_f32_e32 v149, v149, v149
	v_fmac_f32_e32 v149, v147, v147
	v_add_f32_e32 v145, v149, v145
	v_and_b32_e32 v149, 0xffff0000, v71
	v_lshlrev_b32_e32 v147, 16, v71
	v_mul_f32_e32 v149, v149, v149
	v_fmac_f32_e32 v149, v147, v147
	v_add_f32_e32 v145, v149, v145
	v_and_b32_e32 v149, 0xffff0000, v72
	v_lshlrev_b32_e32 v147, 16, v72
	v_mul_f32_e32 v149, v149, v149
	v_fmac_f32_e32 v149, v147, v147
	v_add_f32_e32 v145, v149, v145
	v_and_b32_e32 v149, 0xffff0000, v73
	ds_read_b128 v[210:213], v174 offset:896
	ds_read_b128 v[214:217], v174 offset:33920
	ds_read_b128 v[218:221], v175 offset:896
	ds_read_b128 v[222:225], v175 offset:33920
	ds_read_b128 v[226:229], v174 offset:960
	v_lshlrev_b32_e32 v147, 16, v73
	v_mul_f32_e32 v149, v149, v149
	s_waitcnt lgkmcnt(4)
	v_mfma_f32_16x16x32_bf16 v[134:137], v[70:73], v[210:213], v[134:137]
	v_fmac_f32_e32 v149, v147, v147
	v_add_f32_e32 v145, v149, v145
	s_waitcnt vmcnt(16)
	v_and_b32_e32 v149, 0xffff0000, v66
	s_waitcnt lgkmcnt(3)
	v_mfma_f32_16x16x32_bf16 v[130:133], v[70:73], v[214:217], v[130:133]
	v_lshlrev_b32_e32 v147, 16, v66
	v_mul_f32_e32 v149, v149, v149
	v_fmac_f32_e32 v149, v147, v147
	s_waitcnt lgkmcnt(2)
	v_mfma_f32_16x16x32_bf16 v[134:137], v[70:73], v[218:221], v[134:137]
	ds_read_b128 v[218:221], v174 offset:33984
	ds_read_b128 v[214:217], v175 offset:33984
	v_add_f32_e32 v145, v149, v145
	v_and_b32_e32 v149, 0xffff0000, v67
	s_waitcnt lgkmcnt(3)
	v_mfma_f32_16x16x32_bf16 v[130:133], v[70:73], v[222:225], v[130:133]
	v_lshlrev_b32_e32 v147, 16, v67
	v_mul_f32_e32 v149, v149, v149
	v_fmac_f32_e32 v149, v147, v147
	v_add_f32_e32 v145, v149, v145
	v_and_b32_e32 v149, 0xffff0000, v68
	ds_read_b128 v[210:213], v175 offset:960
	v_lshlrev_b32_e32 v147, 16, v68
	v_mul_f32_e32 v149, v149, v149
	s_waitcnt lgkmcnt(3)
	v_mfma_f32_16x16x32_bf16 v[134:137], v[66:69], v[226:229], v[134:137]
	v_fmac_f32_e32 v149, v147, v147
	v_add_f32_e32 v145, v149, v145
	v_and_b32_e32 v149, 0xffff0000, v69
	s_waitcnt lgkmcnt(2)
	v_mfma_f32_16x16x32_bf16 v[130:133], v[66:69], v[218:221], v[130:133]
	v_lshlrev_b32_e32 v147, 16, v69
	v_mul_f32_e32 v149, v149, v149
	v_fmac_f32_e32 v149, v147, v147
	s_waitcnt lgkmcnt(0)
	v_mfma_f32_16x16x32_bf16 v[134:137], v[66:69], v[210:213], v[134:137]
	v_add_f32_e32 v145, v149, v145
	v_mfma_f32_16x16x32_bf16 v[130:133], v[66:69], v[214:217], v[130:133]
	s_waitcnt vmcnt(15)
	v_and_b32_e32 v149, 0xffff0000, v62
	v_lshlrev_b32_e32 v147, 16, v62
	v_mul_f32_e32 v149, v149, v149
	v_fmac_f32_e32 v149, v147, v147
	v_add_f32_e32 v145, v149, v145
	v_and_b32_e32 v149, 0xffff0000, v63
	v_lshlrev_b32_e32 v147, 16, v63
	v_mul_f32_e32 v149, v149, v149
	v_fmac_f32_e32 v149, v147, v147
	v_add_f32_e32 v145, v149, v145
	v_and_b32_e32 v149, 0xffff0000, v64
	v_lshlrev_b32_e32 v147, 16, v64
	v_mul_f32_e32 v149, v149, v149
	v_fmac_f32_e32 v149, v147, v147
	v_add_f32_e32 v145, v149, v145
	v_and_b32_e32 v149, 0xffff0000, v65
	ds_read_b128 v[210:213], v174 offset:1024
	ds_read_b128 v[214:217], v174 offset:34048
	ds_read_b128 v[218:221], v175 offset:1024
	ds_read_b128 v[222:225], v175 offset:34048
	ds_read_b128 v[226:229], v174 offset:1088
	v_lshlrev_b32_e32 v147, 16, v65
	v_mul_f32_e32 v149, v149, v149
	s_waitcnt lgkmcnt(4)
	v_mfma_f32_16x16x32_bf16 v[134:137], v[62:65], v[210:213], v[134:137]
	v_fmac_f32_e32 v149, v147, v147
	v_add_f32_e32 v145, v149, v145
	s_waitcnt vmcnt(14)
	v_and_b32_e32 v149, 0xffff0000, v58
	s_waitcnt lgkmcnt(3)
	v_mfma_f32_16x16x32_bf16 v[130:133], v[62:65], v[214:217], v[130:133]
	v_lshlrev_b32_e32 v147, 16, v58
	v_mul_f32_e32 v149, v149, v149
	v_fmac_f32_e32 v149, v147, v147
	s_waitcnt lgkmcnt(2)
	v_mfma_f32_16x16x32_bf16 v[134:137], v[62:65], v[218:221], v[134:137]
	ds_read_b128 v[218:221], v174 offset:34112
	ds_read_b128 v[214:217], v175 offset:34112
	v_add_f32_e32 v145, v149, v145
	v_and_b32_e32 v149, 0xffff0000, v59
	s_waitcnt lgkmcnt(3)
	v_mfma_f32_16x16x32_bf16 v[130:133], v[62:65], v[222:225], v[130:133]
	v_lshlrev_b32_e32 v147, 16, v59
	v_mul_f32_e32 v149, v149, v149
	v_fmac_f32_e32 v149, v147, v147
	v_add_f32_e32 v145, v149, v145
	v_and_b32_e32 v149, 0xffff0000, v60
	ds_read_b128 v[210:213], v175 offset:1088
	v_lshlrev_b32_e32 v147, 16, v60
	v_mul_f32_e32 v149, v149, v149
	s_waitcnt lgkmcnt(3)
	v_mfma_f32_16x16x32_bf16 v[134:137], v[58:61], v[226:229], v[134:137]
	v_fmac_f32_e32 v149, v147, v147
	v_add_f32_e32 v145, v149, v145
	v_and_b32_e32 v149, 0xffff0000, v61
	s_waitcnt lgkmcnt(2)
	v_mfma_f32_16x16x32_bf16 v[130:133], v[58:61], v[218:221], v[130:133]
	v_lshlrev_b32_e32 v147, 16, v61
	v_mul_f32_e32 v149, v149, v149
	v_fmac_f32_e32 v149, v147, v147
	s_waitcnt lgkmcnt(0)
	v_mfma_f32_16x16x32_bf16 v[134:137], v[58:61], v[210:213], v[134:137]
	v_add_f32_e32 v145, v149, v145
	v_mfma_f32_16x16x32_bf16 v[130:133], v[58:61], v[214:217], v[130:133]
	s_waitcnt vmcnt(13)
	v_and_b32_e32 v149, 0xffff0000, v54
	v_lshlrev_b32_e32 v147, 16, v54
	v_mul_f32_e32 v149, v149, v149
	v_fmac_f32_e32 v149, v147, v147
	v_add_f32_e32 v145, v149, v145
	v_and_b32_e32 v149, 0xffff0000, v55
	v_lshlrev_b32_e32 v147, 16, v55
	v_mul_f32_e32 v149, v149, v149
	v_fmac_f32_e32 v149, v147, v147
	v_add_f32_e32 v145, v149, v145
	v_and_b32_e32 v149, 0xffff0000, v56
	v_lshlrev_b32_e32 v147, 16, v56
	v_mul_f32_e32 v149, v149, v149
	v_fmac_f32_e32 v149, v147, v147
	v_add_f32_e32 v145, v149, v145
	v_and_b32_e32 v149, 0xffff0000, v57
	ds_read_b128 v[210:213], v174 offset:1152
	ds_read_b128 v[214:217], v174 offset:34176
	ds_read_b128 v[218:221], v175 offset:1152
	ds_read_b128 v[222:225], v175 offset:34176
	ds_read_b128 v[226:229], v174 offset:1216
	v_lshlrev_b32_e32 v147, 16, v57
	v_mul_f32_e32 v149, v149, v149
	s_waitcnt lgkmcnt(4)
	v_mfma_f32_16x16x32_bf16 v[134:137], v[54:57], v[210:213], v[134:137]
	v_fmac_f32_e32 v149, v147, v147
	v_add_f32_e32 v145, v149, v145
	s_waitcnt vmcnt(12)
	v_and_b32_e32 v149, 0xffff0000, v50
	s_waitcnt lgkmcnt(3)
	v_mfma_f32_16x16x32_bf16 v[130:133], v[54:57], v[214:217], v[130:133]
	v_lshlrev_b32_e32 v147, 16, v50
	v_mul_f32_e32 v149, v149, v149
	v_fmac_f32_e32 v149, v147, v147
	s_waitcnt lgkmcnt(2)
	v_mfma_f32_16x16x32_bf16 v[134:137], v[54:57], v[218:221], v[134:137]
	ds_read_b128 v[218:221], v174 offset:34240
	ds_read_b128 v[214:217], v175 offset:34240
	v_add_f32_e32 v145, v149, v145
	v_and_b32_e32 v149, 0xffff0000, v51
	s_waitcnt lgkmcnt(3)
	v_mfma_f32_16x16x32_bf16 v[130:133], v[54:57], v[222:225], v[130:133]
	v_lshlrev_b32_e32 v147, 16, v51
	v_mul_f32_e32 v149, v149, v149
	v_fmac_f32_e32 v149, v147, v147
	v_add_f32_e32 v145, v149, v145
	v_and_b32_e32 v149, 0xffff0000, v52
	ds_read_b128 v[210:213], v175 offset:1216
	v_lshlrev_b32_e32 v147, 16, v52
	v_mul_f32_e32 v149, v149, v149
	s_waitcnt lgkmcnt(3)
	v_mfma_f32_16x16x32_bf16 v[134:137], v[50:53], v[226:229], v[134:137]
	v_fmac_f32_e32 v149, v147, v147
	v_add_f32_e32 v145, v149, v145
	v_and_b32_e32 v149, 0xffff0000, v53
	s_waitcnt lgkmcnt(2)
	v_mfma_f32_16x16x32_bf16 v[130:133], v[50:53], v[218:221], v[130:133]
	v_lshlrev_b32_e32 v147, 16, v53
	v_mul_f32_e32 v149, v149, v149
	v_fmac_f32_e32 v149, v147, v147
	s_waitcnt lgkmcnt(0)
	v_mfma_f32_16x16x32_bf16 v[134:137], v[50:53], v[210:213], v[134:137]
	v_add_f32_e32 v145, v149, v145
	v_mfma_f32_16x16x32_bf16 v[130:133], v[50:53], v[214:217], v[130:133]
	s_waitcnt vmcnt(11)
	v_and_b32_e32 v149, 0xffff0000, v46
	v_lshlrev_b32_e32 v147, 16, v46
	v_mul_f32_e32 v149, v149, v149
	v_fmac_f32_e32 v149, v147, v147
	v_add_f32_e32 v145, v149, v145
	v_and_b32_e32 v149, 0xffff0000, v47
	v_lshlrev_b32_e32 v147, 16, v47
	v_mul_f32_e32 v149, v149, v149
	v_fmac_f32_e32 v149, v147, v147
	v_add_f32_e32 v145, v149, v145
	v_and_b32_e32 v149, 0xffff0000, v48
	v_lshlrev_b32_e32 v147, 16, v48
	v_mul_f32_e32 v149, v149, v149
	v_fmac_f32_e32 v149, v147, v147
	v_add_f32_e32 v145, v149, v145
	v_and_b32_e32 v149, 0xffff0000, v49
	ds_read_b128 v[210:213], v174 offset:1280
	ds_read_b128 v[214:217], v174 offset:34304
	ds_read_b128 v[218:221], v175 offset:1280
	ds_read_b128 v[222:225], v175 offset:34304
	ds_read_b128 v[226:229], v174 offset:1344
	v_lshlrev_b32_e32 v147, 16, v49
	v_mul_f32_e32 v149, v149, v149
	s_waitcnt lgkmcnt(4)
	v_mfma_f32_16x16x32_bf16 v[134:137], v[46:49], v[210:213], v[134:137]
	v_fmac_f32_e32 v149, v147, v147
	v_add_f32_e32 v145, v149, v145
	s_waitcnt vmcnt(10)
	v_and_b32_e32 v149, 0xffff0000, v42
	s_waitcnt lgkmcnt(3)
	v_mfma_f32_16x16x32_bf16 v[130:133], v[46:49], v[214:217], v[130:133]
	v_lshlrev_b32_e32 v147, 16, v42
	v_mul_f32_e32 v149, v149, v149
	v_fmac_f32_e32 v149, v147, v147
	s_waitcnt lgkmcnt(2)
	v_mfma_f32_16x16x32_bf16 v[134:137], v[46:49], v[218:221], v[134:137]
	ds_read_b128 v[218:221], v174 offset:34368
	ds_read_b128 v[214:217], v175 offset:34368
	v_add_f32_e32 v145, v149, v145
	v_and_b32_e32 v149, 0xffff0000, v43
	s_waitcnt lgkmcnt(3)
	v_mfma_f32_16x16x32_bf16 v[130:133], v[46:49], v[222:225], v[130:133]
	v_lshlrev_b32_e32 v147, 16, v43
	v_mul_f32_e32 v149, v149, v149
	v_fmac_f32_e32 v149, v147, v147
	v_add_f32_e32 v145, v149, v145
	v_and_b32_e32 v149, 0xffff0000, v44
	ds_read_b128 v[210:213], v175 offset:1344
	v_lshlrev_b32_e32 v147, 16, v44
	v_mul_f32_e32 v149, v149, v149
	s_waitcnt lgkmcnt(3)
	v_mfma_f32_16x16x32_bf16 v[134:137], v[42:45], v[226:229], v[134:137]
	v_fmac_f32_e32 v149, v147, v147
	v_add_f32_e32 v145, v149, v145
	v_and_b32_e32 v149, 0xffff0000, v45
	s_waitcnt lgkmcnt(2)
	v_mfma_f32_16x16x32_bf16 v[130:133], v[42:45], v[218:221], v[130:133]
	v_lshlrev_b32_e32 v147, 16, v45
	v_mul_f32_e32 v149, v149, v149
	v_fmac_f32_e32 v149, v147, v147
	s_waitcnt lgkmcnt(0)
	v_mfma_f32_16x16x32_bf16 v[134:137], v[42:45], v[210:213], v[134:137]
	v_add_f32_e32 v145, v149, v145
	v_mfma_f32_16x16x32_bf16 v[130:133], v[42:45], v[214:217], v[130:133]
	s_waitcnt vmcnt(9)
	v_and_b32_e32 v149, 0xffff0000, v38
	v_lshlrev_b32_e32 v147, 16, v38
	v_mul_f32_e32 v149, v149, v149
	v_fmac_f32_e32 v149, v147, v147
	v_add_f32_e32 v145, v149, v145
	v_and_b32_e32 v149, 0xffff0000, v39
	v_lshlrev_b32_e32 v147, 16, v39
	v_mul_f32_e32 v149, v149, v149
	v_fmac_f32_e32 v149, v147, v147
	v_add_f32_e32 v145, v149, v145
	v_and_b32_e32 v149, 0xffff0000, v40
	v_lshlrev_b32_e32 v147, 16, v40
	v_mul_f32_e32 v149, v149, v149
	v_fmac_f32_e32 v149, v147, v147
	v_add_f32_e32 v145, v149, v145
	v_and_b32_e32 v149, 0xffff0000, v41
	ds_read_b128 v[210:213], v174 offset:1408
	ds_read_b128 v[214:217], v174 offset:34432
	ds_read_b128 v[218:221], v175 offset:1408
	ds_read_b128 v[222:225], v175 offset:34432
	ds_read_b128 v[226:229], v174 offset:1472
	v_lshlrev_b32_e32 v147, 16, v41
	v_mul_f32_e32 v149, v149, v149
	s_waitcnt lgkmcnt(4)
	v_mfma_f32_16x16x32_bf16 v[134:137], v[38:41], v[210:213], v[134:137]
	v_fmac_f32_e32 v149, v147, v147
	v_add_f32_e32 v145, v149, v145
	s_waitcnt vmcnt(8)
	v_and_b32_e32 v149, 0xffff0000, v34
	s_waitcnt lgkmcnt(3)
	v_mfma_f32_16x16x32_bf16 v[130:133], v[38:41], v[214:217], v[130:133]
	v_lshlrev_b32_e32 v147, 16, v34
	v_mul_f32_e32 v149, v149, v149
	v_fmac_f32_e32 v149, v147, v147
	s_waitcnt lgkmcnt(2)
	v_mfma_f32_16x16x32_bf16 v[134:137], v[38:41], v[218:221], v[134:137]
	ds_read_b128 v[218:221], v174 offset:34496
	ds_read_b128 v[214:217], v175 offset:34496
	v_add_f32_e32 v145, v149, v145
	v_and_b32_e32 v149, 0xffff0000, v35
	s_waitcnt lgkmcnt(3)
	v_mfma_f32_16x16x32_bf16 v[130:133], v[38:41], v[222:225], v[130:133]
	v_lshlrev_b32_e32 v147, 16, v35
	v_mul_f32_e32 v149, v149, v149
	v_fmac_f32_e32 v149, v147, v147
	v_add_f32_e32 v145, v149, v145
	v_and_b32_e32 v149, 0xffff0000, v36
	ds_read_b128 v[210:213], v175 offset:1472
	v_lshlrev_b32_e32 v147, 16, v36
	v_mul_f32_e32 v149, v149, v149
	s_waitcnt lgkmcnt(3)
	v_mfma_f32_16x16x32_bf16 v[134:137], v[34:37], v[226:229], v[134:137]
	v_fmac_f32_e32 v149, v147, v147
	v_add_f32_e32 v145, v149, v145
	v_and_b32_e32 v149, 0xffff0000, v37
	s_waitcnt lgkmcnt(2)
	v_mfma_f32_16x16x32_bf16 v[130:133], v[34:37], v[218:221], v[130:133]
	v_lshlrev_b32_e32 v147, 16, v37
	v_mul_f32_e32 v149, v149, v149
	v_fmac_f32_e32 v149, v147, v147
	s_waitcnt lgkmcnt(0)
	v_mfma_f32_16x16x32_bf16 v[134:137], v[34:37], v[210:213], v[134:137]
	v_add_f32_e32 v145, v149, v145
	v_mfma_f32_16x16x32_bf16 v[130:133], v[34:37], v[214:217], v[130:133]
	s_waitcnt vmcnt(7)
	v_and_b32_e32 v149, 0xffff0000, v30
	v_lshlrev_b32_e32 v147, 16, v30
	v_mul_f32_e32 v149, v149, v149
	v_fmac_f32_e32 v149, v147, v147
	v_add_f32_e32 v145, v149, v145
	v_and_b32_e32 v149, 0xffff0000, v31
	v_lshlrev_b32_e32 v147, 16, v31
	v_mul_f32_e32 v149, v149, v149
	v_fmac_f32_e32 v149, v147, v147
	v_add_f32_e32 v145, v149, v145
	v_and_b32_e32 v149, 0xffff0000, v32
	v_lshlrev_b32_e32 v147, 16, v32
	v_mul_f32_e32 v149, v149, v149
	v_fmac_f32_e32 v149, v147, v147
	v_add_f32_e32 v145, v149, v145
	v_and_b32_e32 v149, 0xffff0000, v33
	ds_read_b128 v[210:213], v174 offset:1536
	ds_read_b128 v[214:217], v174 offset:34560
	ds_read_b128 v[218:221], v175 offset:1536
	ds_read_b128 v[222:225], v175 offset:34560
	ds_read_b128 v[226:229], v174 offset:1600
	v_lshlrev_b32_e32 v147, 16, v33
	v_mul_f32_e32 v149, v149, v149
	s_waitcnt lgkmcnt(4)
	v_mfma_f32_16x16x32_bf16 v[134:137], v[30:33], v[210:213], v[134:137]
	v_fmac_f32_e32 v149, v147, v147
	v_add_f32_e32 v145, v149, v145
	s_waitcnt vmcnt(6)
	v_and_b32_e32 v149, 0xffff0000, v26
	s_waitcnt lgkmcnt(3)
	v_mfma_f32_16x16x32_bf16 v[130:133], v[30:33], v[214:217], v[130:133]
	v_lshlrev_b32_e32 v147, 16, v26
	v_mul_f32_e32 v149, v149, v149
	v_fmac_f32_e32 v149, v147, v147
	s_waitcnt lgkmcnt(2)
	v_mfma_f32_16x16x32_bf16 v[134:137], v[30:33], v[218:221], v[134:137]
	ds_read_b128 v[218:221], v174 offset:34624
	ds_read_b128 v[214:217], v175 offset:34624
	v_add_f32_e32 v145, v149, v145
	v_and_b32_e32 v149, 0xffff0000, v27
	s_waitcnt lgkmcnt(3)
	v_mfma_f32_16x16x32_bf16 v[130:133], v[30:33], v[222:225], v[130:133]
	v_lshlrev_b32_e32 v147, 16, v27
	v_mul_f32_e32 v149, v149, v149
	v_fmac_f32_e32 v149, v147, v147
	v_add_f32_e32 v145, v149, v145
	v_and_b32_e32 v149, 0xffff0000, v28
	ds_read_b128 v[210:213], v175 offset:1600
	v_lshlrev_b32_e32 v147, 16, v28
	v_mul_f32_e32 v149, v149, v149
	s_waitcnt lgkmcnt(3)
	v_mfma_f32_16x16x32_bf16 v[134:137], v[26:29], v[226:229], v[134:137]
	v_fmac_f32_e32 v149, v147, v147
	v_add_f32_e32 v145, v149, v145
	v_and_b32_e32 v149, 0xffff0000, v29
	s_waitcnt lgkmcnt(2)
	v_mfma_f32_16x16x32_bf16 v[130:133], v[26:29], v[218:221], v[130:133]
	v_lshlrev_b32_e32 v147, 16, v29
	v_mul_f32_e32 v149, v149, v149
	v_fmac_f32_e32 v149, v147, v147
	s_waitcnt lgkmcnt(0)
	v_mfma_f32_16x16x32_bf16 v[134:137], v[26:29], v[210:213], v[134:137]
	v_add_f32_e32 v145, v149, v145
	v_mfma_f32_16x16x32_bf16 v[130:133], v[26:29], v[214:217], v[130:133]
	s_waitcnt vmcnt(5)
	v_and_b32_e32 v149, 0xffff0000, v22
	v_lshlrev_b32_e32 v147, 16, v22
	v_mul_f32_e32 v149, v149, v149
	v_fmac_f32_e32 v149, v147, v147
	v_add_f32_e32 v145, v149, v145
	v_and_b32_e32 v149, 0xffff0000, v23
	v_lshlrev_b32_e32 v147, 16, v23
	v_mul_f32_e32 v149, v149, v149
	v_fmac_f32_e32 v149, v147, v147
	v_add_f32_e32 v145, v149, v145
	v_and_b32_e32 v149, 0xffff0000, v24
	v_lshlrev_b32_e32 v147, 16, v24
	v_mul_f32_e32 v149, v149, v149
	v_fmac_f32_e32 v149, v147, v147
	v_add_f32_e32 v145, v149, v145
	v_and_b32_e32 v149, 0xffff0000, v25
	ds_read_b128 v[210:213], v174 offset:1664
	ds_read_b128 v[214:217], v174 offset:34688
	ds_read_b128 v[218:221], v175 offset:1664
	ds_read_b128 v[222:225], v175 offset:34688
	ds_read_b128 v[226:229], v174 offset:1728
	v_lshlrev_b32_e32 v147, 16, v25
	v_mul_f32_e32 v149, v149, v149
	s_waitcnt lgkmcnt(4)
	v_mfma_f32_16x16x32_bf16 v[134:137], v[22:25], v[210:213], v[134:137]
	v_fmac_f32_e32 v149, v147, v147
	v_add_f32_e32 v145, v149, v145
	s_waitcnt vmcnt(4)
	v_and_b32_e32 v149, 0xffff0000, v18
	s_waitcnt lgkmcnt(3)
	v_mfma_f32_16x16x32_bf16 v[130:133], v[22:25], v[214:217], v[130:133]
	v_lshlrev_b32_e32 v147, 16, v18
	v_mul_f32_e32 v149, v149, v149
	v_fmac_f32_e32 v149, v147, v147
	s_waitcnt lgkmcnt(2)
	v_mfma_f32_16x16x32_bf16 v[134:137], v[22:25], v[218:221], v[134:137]
	ds_read_b128 v[218:221], v174 offset:34752
	ds_read_b128 v[214:217], v175 offset:34752
	v_add_f32_e32 v145, v149, v145
	v_and_b32_e32 v149, 0xffff0000, v19
	s_waitcnt lgkmcnt(3)
	v_mfma_f32_16x16x32_bf16 v[130:133], v[22:25], v[222:225], v[130:133]
	v_lshlrev_b32_e32 v147, 16, v19
	v_mul_f32_e32 v149, v149, v149
	v_fmac_f32_e32 v149, v147, v147
	v_add_f32_e32 v145, v149, v145
	v_and_b32_e32 v149, 0xffff0000, v20
	ds_read_b128 v[210:213], v175 offset:1728
	v_lshlrev_b32_e32 v147, 16, v20
	v_mul_f32_e32 v149, v149, v149
	s_waitcnt lgkmcnt(3)
	v_mfma_f32_16x16x32_bf16 v[134:137], v[18:21], v[226:229], v[134:137]
	v_fmac_f32_e32 v149, v147, v147
	v_add_f32_e32 v145, v149, v145
	v_and_b32_e32 v149, 0xffff0000, v21
	s_waitcnt lgkmcnt(2)
	v_mfma_f32_16x16x32_bf16 v[130:133], v[18:21], v[218:221], v[130:133]
	v_lshlrev_b32_e32 v147, 16, v21
	v_mul_f32_e32 v149, v149, v149
	v_fmac_f32_e32 v149, v147, v147
	s_waitcnt lgkmcnt(0)
	v_mfma_f32_16x16x32_bf16 v[134:137], v[18:21], v[210:213], v[134:137]
	v_add_f32_e32 v145, v149, v145
	v_mfma_f32_16x16x32_bf16 v[130:133], v[18:21], v[214:217], v[130:133]
	s_waitcnt vmcnt(3)
	v_and_b32_e32 v149, 0xffff0000, v14
	v_lshlrev_b32_e32 v147, 16, v14
	v_mul_f32_e32 v149, v149, v149
	v_fmac_f32_e32 v149, v147, v147
	v_add_f32_e32 v145, v149, v145
	v_and_b32_e32 v149, 0xffff0000, v15
	v_lshlrev_b32_e32 v147, 16, v15
	v_mul_f32_e32 v149, v149, v149
	v_fmac_f32_e32 v149, v147, v147
	v_add_f32_e32 v145, v149, v145
	v_and_b32_e32 v149, 0xffff0000, v16
	v_lshlrev_b32_e32 v147, 16, v16
	v_mul_f32_e32 v149, v149, v149
	v_fmac_f32_e32 v149, v147, v147
	v_add_f32_e32 v145, v149, v145
	v_and_b32_e32 v149, 0xffff0000, v17
	ds_read_b128 v[210:213], v174 offset:1792
	ds_read_b128 v[214:217], v174 offset:34816
	ds_read_b128 v[218:221], v175 offset:1792
	ds_read_b128 v[222:225], v175 offset:34816
	ds_read_b128 v[226:229], v174 offset:1856
	v_lshlrev_b32_e32 v147, 16, v17
	v_mul_f32_e32 v149, v149, v149
	s_waitcnt lgkmcnt(4)
	v_mfma_f32_16x16x32_bf16 v[134:137], v[14:17], v[210:213], v[134:137]
	v_fmac_f32_e32 v149, v147, v147
	v_add_f32_e32 v145, v149, v145
	s_waitcnt vmcnt(2)
	v_and_b32_e32 v149, 0xffff0000, v10
	s_waitcnt lgkmcnt(3)
	v_mfma_f32_16x16x32_bf16 v[130:133], v[14:17], v[214:217], v[130:133]
	v_lshlrev_b32_e32 v147, 16, v10
	v_mul_f32_e32 v149, v149, v149
	v_fmac_f32_e32 v149, v147, v147
	s_waitcnt lgkmcnt(2)
	v_mfma_f32_16x16x32_bf16 v[134:137], v[14:17], v[218:221], v[134:137]
	ds_read_b128 v[218:221], v174 offset:34880
	ds_read_b128 v[214:217], v175 offset:34880
	v_add_f32_e32 v145, v149, v145
	v_and_b32_e32 v149, 0xffff0000, v11
	s_waitcnt lgkmcnt(3)
	v_mfma_f32_16x16x32_bf16 v[130:133], v[14:17], v[222:225], v[130:133]
	v_lshlrev_b32_e32 v147, 16, v11
	v_mul_f32_e32 v149, v149, v149
	v_fmac_f32_e32 v149, v147, v147
	v_add_f32_e32 v145, v149, v145
	v_and_b32_e32 v149, 0xffff0000, v12
	ds_read_b128 v[210:213], v175 offset:1856
	v_lshlrev_b32_e32 v147, 16, v12
	v_mul_f32_e32 v149, v149, v149
	s_waitcnt lgkmcnt(3)
	v_mfma_f32_16x16x32_bf16 v[134:137], v[10:13], v[226:229], v[134:137]
	v_fmac_f32_e32 v149, v147, v147
	v_add_f32_e32 v145, v149, v145
	v_and_b32_e32 v149, 0xffff0000, v13
	s_waitcnt lgkmcnt(2)
	v_mfma_f32_16x16x32_bf16 v[130:133], v[10:13], v[218:221], v[130:133]
	v_lshlrev_b32_e32 v147, 16, v13
	v_mul_f32_e32 v149, v149, v149
	v_fmac_f32_e32 v149, v147, v147
	s_waitcnt lgkmcnt(0)
	v_mfma_f32_16x16x32_bf16 v[134:137], v[10:13], v[210:213], v[134:137]
	v_add_f32_e32 v145, v149, v145
	v_mfma_f32_16x16x32_bf16 v[130:133], v[10:13], v[214:217], v[130:133]
	s_waitcnt vmcnt(1)
	v_and_b32_e32 v149, 0xffff0000, v6
	ds_read_b128 v[210:213], v174 offset:1920
	ds_read_b128 v[214:217], v174 offset:34944
	ds_read_b128 v[218:221], v175 offset:1920
	ds_read_b128 v[222:225], v175 offset:34944
	ds_read_b128 v[226:229], v174 offset:1984
	v_lshlrev_b32_e32 v147, 16, v6
	v_mul_f32_e32 v149, v149, v149
	s_waitcnt lgkmcnt(4)
	v_mfma_f32_16x16x32_bf16 v[134:137], v[6:9], v[210:213], v[134:137]
	v_fmac_f32_e32 v149, v147, v147
	v_add_f32_e32 v145, v149, v145
	v_and_b32_e32 v149, 0xffff0000, v7
	v_lshlrev_b32_e32 v147, 16, v7
	v_mul_f32_e32 v149, v149, v149
	v_fmac_f32_e32 v149, v147, v147
	s_waitcnt lgkmcnt(2)
	v_mfma_f32_16x16x32_bf16 v[134:137], v[6:9], v[218:221], v[134:137]
	v_add_f32_e32 v145, v149, v145
	v_and_b32_e32 v149, 0xffff0000, v8
	v_lshlrev_b32_e32 v147, 16, v8
	v_mfma_f32_16x16x32_bf16 v[130:133], v[6:9], v[214:217], v[130:133]
	v_mul_f32_e32 v149, v149, v149
	v_fmac_f32_e32 v149, v147, v147
	v_add_f32_e32 v145, v149, v145
	v_and_b32_e32 v149, 0xffff0000, v9
	s_waitcnt lgkmcnt(1)
	v_mfma_f32_16x16x32_bf16 v[222:225], v[6:9], v[222:225], v[130:133]
	v_lshlrev_b32_e32 v147, 16, v9
	ds_read_b128 v[218:221], v174 offset:35008
	ds_read_b128 v[214:217], v175 offset:35008
	s_waitcnt vmcnt(0) lgkmcnt(2)
	v_mfma_f32_16x16x32_bf16 v[130:133], v[2:5], v[226:229], v[134:137]
	ds_read_b128 v[210:213], v175 offset:1984
	s_nop 1
	v_mul_f32_e32 v134, v149, v149
	v_and_b32_e32 v136, 0xffff0000, v2
	v_fmac_f32_e32 v134, v147, v147
	v_lshlrev_b32_e32 v135, 16, v2
	v_mul_f32_e32 v136, v136, v136
	v_add_f32_e32 v134, v134, v145
	v_fmac_f32_e32 v136, v135, v135
	v_add_f32_e32 v134, v136, v134
	v_and_b32_e32 v136, 0xffff0000, v3
	v_lshlrev_b32_e32 v135, 16, v3
	v_mul_f32_e32 v136, v136, v136
	v_fmac_f32_e32 v136, v135, v135
	v_add_f32_e32 v134, v136, v134
	v_and_b32_e32 v136, 0xffff0000, v4
	v_lshlrev_b32_e32 v135, 16, v4
	v_mul_f32_e32 v136, v136, v136
	v_fmac_f32_e32 v136, v135, v135
	v_add_f32_e32 v145, v136, v134
	s_waitcnt lgkmcnt(2)
	v_mfma_f32_16x16x32_bf16 v[134:137], v[2:5], v[218:221], v[222:225]
	v_and_b32_e32 v149, 0xffff0000, v5
	v_lshlrev_b32_e32 v147, 16, v5
	v_mul_f32_e32 v149, v149, v149
	v_fmac_f32_e32 v149, v147, v147
	s_waitcnt lgkmcnt(0)
	v_mfma_f32_16x16x32_bf16 v[130:133], v[2:5], v[210:213], v[130:133]
	v_add_f32_e32 v145, v149, v145
	v_mfma_f32_16x16x32_bf16 v[134:137], v[2:5], v[214:217], v[134:137]
	ds_bpermute_b32 v147, v192, v145
	v_lshlrev_b32_e32 v149, 16, v126
	v_and_b32_e32 v126, 0xffff0000, v126
	s_waitcnt lgkmcnt(0)
	v_add_f32_e32 v145, v145, v147
	ds_bpermute_b32 v147, v193, v145
	s_waitcnt lgkmcnt(0)
	v_add_f32_e32 v145, v145, v147
	v_fmamk_f32 v145, v145, 0x3a800000, v195
	v_mul_f32_e32 v147, 0x4f800000, v145
	v_cmp_gt_f32_e32 vcc, s25, v145
	s_nop 1
	v_cndmask_b32_e32 v145, v145, v147, vcc
	v_sqrt_f32_e32 v147, v145
	s_nop 0
	v_add_u32_e32 v151, -1, v147
	v_add_u32_e32 v153, 1, v147
	v_fma_f32 v155, -v151, v147, v145
	v_fma_f32 v157, -v153, v147, v145
	v_cmp_ge_f32_e64 s[8:9], 0, v155
	s_nop 1
	v_cndmask_b32_e64 v147, v147, v151, s[8:9]
	v_cmp_lt_f32_e64 s[8:9], 0, v157
	s_nop 1
	v_cndmask_b32_e64 v147, v147, v153, s[8:9]
	v_mul_f32_e32 v151, 0x37800000, v147
	v_cndmask_b32_e32 v147, v147, v151, vcc
	v_cmp_class_f32_e32 vcc, v145, v196
	s_nop 1
	v_cndmask_b32_e32 v145, v147, v145, vcc
	v_div_scale_f32 v147, s[8:9], v145, v145, 1.0
	v_rcp_f32_e32 v151, v147
	v_div_scale_f32 v153, vcc, 1.0, v145, 1.0
	v_fma_f32 v155, -v147, v151, 1.0
	v_fmac_f32_e32 v151, v155, v151
	v_mul_f32_e32 v155, v153, v151
	v_fma_f32 v157, -v147, v155, v153
	v_fmac_f32_e32 v155, v157, v151
	v_fma_f32 v147, -v147, v155, v153
	v_div_fmas_f32 v147, v147, v151, v155
	v_div_fixup_f32 v145, v147, v145, 1.0
	v_mul_f32_e32 v147, 0x41800000, v145
	v_mul_f32_e32 v149, v147, v149
	v_mul_f32_e32 v126, v147, v126
	v_cvt_pk_fp8_f32 v168, v149, v126
	v_lshlrev_b32_e32 v151, 16, v127
	v_and_b32_e32 v127, 0xffff0000, v127
	v_mul_f32_e32 v126, v147, v151
	v_mul_f32_e32 v127, v147, v127
	v_cvt_pk_fp8_f32 v168, v126, v127 op_sel:[0,0,1]
	v_lshlrev_b32_e32 v126, 16, v128
	v_and_b32_e32 v127, 0xffff0000, v128
	v_mul_f32_e32 v126, v147, v126
	v_mul_f32_e32 v127, v147, v127
	v_cvt_pk_fp8_f32 v169, v126, v127
	v_lshlrev_b32_e32 v128, 16, v129
	v_and_b32_e32 v127, 0xffff0000, v129
	v_mul_f32_e32 v126, v147, v128
	v_mul_f32_e32 v127, v147, v127
	v_cvt_pk_fp8_f32 v169, v126, v127 op_sel:[0,0,1]
	v_lshl_add_u64 v[126:127], v[142:143], 0, v[166:167]
	global_store_dwordx2 v[126:127], v[168:169], off
	s_nop 0
	v_lshlrev_b32_e32 v128, 16, v122
	v_and_b32_e32 v122, 0xffff0000, v122
	v_mul_f32_e32 v128, v147, v128
	v_mul_f32_e32 v129, v147, v122
	v_cvt_pk_fp8_f32 v122, v128, v129
	v_lshlrev_b32_e32 v149, 16, v123
	v_and_b32_e32 v123, 0xffff0000, v123
	v_mul_f32_e32 v128, v147, v149
	v_mul_f32_e32 v123, v147, v123
	v_cvt_pk_fp8_f32 v122, v128, v123 op_sel:[0,0,1]
	v_lshlrev_b32_e32 v123, 16, v124
	v_mul_f32_e32 v128, v147, v123
	v_and_b32_e32 v123, 0xffff0000, v124
	v_mul_f32_e32 v124, v147, v123
	v_cvt_pk_fp8_f32 v123, v128, v124
	v_lshlrev_b32_e32 v129, 16, v125
	v_and_b32_e32 v125, 0xffff0000, v125
	v_mul_f32_e32 v124, v147, v129
	v_mul_f32_e32 v125, v147, v125
	v_cvt_pk_fp8_f32 v123, v124, v125 op_sel:[0,0,1]
	global_store_dwordx2 v[126:127], v[122:123], off offset:32
	s_nop 0
	v_lshlrev_b32_e32 v122, 16, v118
	v_and_b32_e32 v118, 0xffff0000, v118
	v_mul_f32_e32 v122, v147, v122
	v_mul_f32_e32 v123, v147, v118
	v_cvt_pk_fp8_f32 v118, v122, v123
	v_lshlrev_b32_e32 v124, 16, v119
	v_and_b32_e32 v119, 0xffff0000, v119
	v_mul_f32_e32 v122, v147, v124
	v_mul_f32_e32 v119, v147, v119
	v_cvt_pk_fp8_f32 v118, v122, v119 op_sel:[0,0,1]
	v_lshlrev_b32_e32 v119, 16, v120
	v_mul_f32_e32 v122, v147, v119
	v_and_b32_e32 v119, 0xffff0000, v120
	v_mul_f32_e32 v120, v147, v119
	v_cvt_pk_fp8_f32 v119, v122, v120
	v_lshlrev_b32_e32 v123, 16, v121
	v_and_b32_e32 v121, 0xffff0000, v121
	v_mul_f32_e32 v120, v147, v123
	v_mul_f32_e32 v121, v147, v121
	v_cvt_pk_fp8_f32 v119, v120, v121 op_sel:[0,0,1]
	global_store_dwordx2 v[126:127], v[118:119], off offset:64
	s_nop 0
	v_lshlrev_b32_e32 v118, 16, v114
	v_and_b32_e32 v114, 0xffff0000, v114
	v_mul_f32_e32 v118, v147, v118
	v_mul_f32_e32 v119, v147, v114
	v_cvt_pk_fp8_f32 v114, v118, v119
	v_lshlrev_b32_e32 v120, 16, v115
	v_and_b32_e32 v115, 0xffff0000, v115
	v_mul_f32_e32 v118, v147, v120
	v_mul_f32_e32 v115, v147, v115
	v_cvt_pk_fp8_f32 v114, v118, v115 op_sel:[0,0,1]
	v_lshlrev_b32_e32 v115, 16, v116
	v_mul_f32_e32 v118, v147, v115
	v_and_b32_e32 v115, 0xffff0000, v116
	v_mul_f32_e32 v116, v147, v115
	v_cvt_pk_fp8_f32 v115, v118, v116
	v_lshlrev_b32_e32 v119, 16, v117
	v_and_b32_e32 v117, 0xffff0000, v117
	v_mul_f32_e32 v116, v147, v119
	v_mul_f32_e32 v117, v147, v117
	v_cvt_pk_fp8_f32 v115, v116, v117 op_sel:[0,0,1]
	global_store_dwordx2 v[126:127], v[114:115], off offset:96
	s_nop 0
	v_lshlrev_b32_e32 v114, 16, v110
	v_and_b32_e32 v110, 0xffff0000, v110
	v_mul_f32_e32 v114, v147, v114
	v_mul_f32_e32 v115, v147, v110
	v_cvt_pk_fp8_f32 v110, v114, v115
	v_lshlrev_b32_e32 v116, 16, v111
	v_and_b32_e32 v111, 0xffff0000, v111
	v_mul_f32_e32 v114, v147, v116
	v_mul_f32_e32 v111, v147, v111
	v_cvt_pk_fp8_f32 v110, v114, v111 op_sel:[0,0,1]
	v_lshlrev_b32_e32 v111, 16, v112
	v_mul_f32_e32 v114, v147, v111
	v_and_b32_e32 v111, 0xffff0000, v112
	v_mul_f32_e32 v112, v147, v111
	v_cvt_pk_fp8_f32 v111, v114, v112
	v_lshlrev_b32_e32 v115, 16, v113
	v_and_b32_e32 v113, 0xffff0000, v113
	v_mul_f32_e32 v112, v147, v115
	v_mul_f32_e32 v113, v147, v113
	v_cvt_pk_fp8_f32 v111, v112, v113 op_sel:[0,0,1]
	global_store_dwordx2 v[126:127], v[110:111], off offset:128
	s_nop 0
	v_lshlrev_b32_e32 v110, 16, v106
	v_and_b32_e32 v106, 0xffff0000, v106
	v_mul_f32_e32 v110, v147, v110
	v_mul_f32_e32 v111, v147, v106
	v_cvt_pk_fp8_f32 v106, v110, v111
	v_lshlrev_b32_e32 v112, 16, v107
	v_and_b32_e32 v107, 0xffff0000, v107
	v_mul_f32_e32 v110, v147, v112
	v_mul_f32_e32 v107, v147, v107
	v_cvt_pk_fp8_f32 v106, v110, v107 op_sel:[0,0,1]
	v_lshlrev_b32_e32 v107, 16, v108
	v_mul_f32_e32 v110, v147, v107
	v_and_b32_e32 v107, 0xffff0000, v108
	v_mul_f32_e32 v108, v147, v107
	v_cvt_pk_fp8_f32 v107, v110, v108
	v_lshlrev_b32_e32 v111, 16, v109
	v_and_b32_e32 v109, 0xffff0000, v109
	v_mul_f32_e32 v108, v147, v111
	v_mul_f32_e32 v109, v147, v109
	v_cvt_pk_fp8_f32 v107, v108, v109 op_sel:[0,0,1]
	global_store_dwordx2 v[126:127], v[106:107], off offset:160
	s_nop 0
	v_lshlrev_b32_e32 v106, 16, v102
	v_and_b32_e32 v102, 0xffff0000, v102
	v_mul_f32_e32 v106, v147, v106
	v_mul_f32_e32 v107, v147, v102
	v_cvt_pk_fp8_f32 v102, v106, v107
	v_lshlrev_b32_e32 v108, 16, v103
	v_and_b32_e32 v103, 0xffff0000, v103
	v_mul_f32_e32 v106, v147, v108
	v_mul_f32_e32 v103, v147, v103
	v_cvt_pk_fp8_f32 v102, v106, v103 op_sel:[0,0,1]
	v_lshlrev_b32_e32 v103, 16, v104
	v_mul_f32_e32 v106, v147, v103
	v_and_b32_e32 v103, 0xffff0000, v104
	v_mul_f32_e32 v104, v147, v103
	v_cvt_pk_fp8_f32 v103, v106, v104
	v_lshlrev_b32_e32 v107, 16, v105
	v_and_b32_e32 v105, 0xffff0000, v105
	v_mul_f32_e32 v104, v147, v107
	v_mul_f32_e32 v105, v147, v105
	v_cvt_pk_fp8_f32 v103, v104, v105 op_sel:[0,0,1]
	global_store_dwordx2 v[126:127], v[102:103], off offset:192
	s_nop 0
	v_lshlrev_b32_e32 v102, 16, v98
	v_and_b32_e32 v98, 0xffff0000, v98
	v_mul_f32_e32 v102, v147, v102
	v_mul_f32_e32 v103, v147, v98
	v_cvt_pk_fp8_f32 v98, v102, v103
	v_lshlrev_b32_e32 v104, 16, v99
	v_and_b32_e32 v99, 0xffff0000, v99
	v_mul_f32_e32 v102, v147, v104
	v_mul_f32_e32 v99, v147, v99
	v_cvt_pk_fp8_f32 v98, v102, v99 op_sel:[0,0,1]
	v_lshlrev_b32_e32 v99, 16, v100
	v_mul_f32_e32 v102, v147, v99
	v_and_b32_e32 v99, 0xffff0000, v100
	v_mul_f32_e32 v100, v147, v99
	v_cvt_pk_fp8_f32 v99, v102, v100
	v_lshlrev_b32_e32 v103, 16, v101
	v_and_b32_e32 v101, 0xffff0000, v101
	v_mul_f32_e32 v100, v147, v103
	v_mul_f32_e32 v101, v147, v101
	v_cvt_pk_fp8_f32 v99, v100, v101 op_sel:[0,0,1]
	global_store_dwordx2 v[126:127], v[98:99], off offset:224
	s_nop 0
	v_lshlrev_b32_e32 v98, 16, v94
	v_and_b32_e32 v94, 0xffff0000, v94
	v_mul_f32_e32 v98, v147, v98
	v_mul_f32_e32 v99, v147, v94
	v_cvt_pk_fp8_f32 v94, v98, v99
	v_lshlrev_b32_e32 v100, 16, v95
	v_and_b32_e32 v95, 0xffff0000, v95
	v_mul_f32_e32 v98, v147, v100
	v_mul_f32_e32 v95, v147, v95
	v_cvt_pk_fp8_f32 v94, v98, v95 op_sel:[0,0,1]
	v_lshlrev_b32_e32 v95, 16, v96
	v_mul_f32_e32 v98, v147, v95
	v_and_b32_e32 v95, 0xffff0000, v96
	v_mul_f32_e32 v96, v147, v95
	v_cvt_pk_fp8_f32 v95, v98, v96
	v_lshlrev_b32_e32 v99, 16, v97
	v_and_b32_e32 v97, 0xffff0000, v97
	v_mul_f32_e32 v96, v147, v99
	v_mul_f32_e32 v97, v147, v97
	v_cvt_pk_fp8_f32 v95, v96, v97 op_sel:[0,0,1]
	global_store_dwordx2 v[126:127], v[94:95], off offset:256
	s_nop 0
	v_lshlrev_b32_e32 v94, 16, v90
	v_and_b32_e32 v90, 0xffff0000, v90
	v_mul_f32_e32 v94, v147, v94
	v_mul_f32_e32 v95, v147, v90
	v_cvt_pk_fp8_f32 v90, v94, v95
	v_lshlrev_b32_e32 v96, 16, v91
	v_and_b32_e32 v91, 0xffff0000, v91
	v_mul_f32_e32 v94, v147, v96
	v_mul_f32_e32 v91, v147, v91
	v_cvt_pk_fp8_f32 v90, v94, v91 op_sel:[0,0,1]
	v_lshlrev_b32_e32 v91, 16, v92
	v_mul_f32_e32 v94, v147, v91
	v_and_b32_e32 v91, 0xffff0000, v92
	v_mul_f32_e32 v92, v147, v91
	v_cvt_pk_fp8_f32 v91, v94, v92
	v_lshlrev_b32_e32 v95, 16, v93
	v_and_b32_e32 v93, 0xffff0000, v93
	v_mul_f32_e32 v92, v147, v95
	v_mul_f32_e32 v93, v147, v93
	v_cvt_pk_fp8_f32 v91, v92, v93 op_sel:[0,0,1]
	global_store_dwordx2 v[126:127], v[90:91], off offset:288
	s_nop 0
	v_lshlrev_b32_e32 v90, 16, v86
	v_and_b32_e32 v86, 0xffff0000, v86
	v_mul_f32_e32 v90, v147, v90
	v_mul_f32_e32 v91, v147, v86
	v_cvt_pk_fp8_f32 v86, v90, v91
	v_lshlrev_b32_e32 v92, 16, v87
	v_and_b32_e32 v87, 0xffff0000, v87
	v_mul_f32_e32 v90, v147, v92
	v_mul_f32_e32 v87, v147, v87
	v_cvt_pk_fp8_f32 v86, v90, v87 op_sel:[0,0,1]
	v_lshlrev_b32_e32 v87, 16, v88
	v_mul_f32_e32 v90, v147, v87
	v_and_b32_e32 v87, 0xffff0000, v88
	v_mul_f32_e32 v88, v147, v87
	v_cvt_pk_fp8_f32 v87, v90, v88
	v_lshlrev_b32_e32 v91, 16, v89
	v_and_b32_e32 v89, 0xffff0000, v89
	v_mul_f32_e32 v88, v147, v91
	v_mul_f32_e32 v89, v147, v89
	v_cvt_pk_fp8_f32 v87, v88, v89 op_sel:[0,0,1]
	global_store_dwordx2 v[126:127], v[86:87], off offset:320
	s_nop 0
	v_lshlrev_b32_e32 v86, 16, v82
	v_and_b32_e32 v82, 0xffff0000, v82
	v_mul_f32_e32 v86, v147, v86
	v_mul_f32_e32 v87, v147, v82
	v_cvt_pk_fp8_f32 v82, v86, v87
	v_lshlrev_b32_e32 v88, 16, v83
	v_and_b32_e32 v83, 0xffff0000, v83
	v_mul_f32_e32 v86, v147, v88
	v_mul_f32_e32 v83, v147, v83
	v_cvt_pk_fp8_f32 v82, v86, v83 op_sel:[0,0,1]
	v_lshlrev_b32_e32 v83, 16, v84
	v_mul_f32_e32 v86, v147, v83
	v_and_b32_e32 v83, 0xffff0000, v84
	v_mul_f32_e32 v84, v147, v83
	v_cvt_pk_fp8_f32 v83, v86, v84
	v_lshlrev_b32_e32 v87, 16, v85
	v_and_b32_e32 v85, 0xffff0000, v85
	v_mul_f32_e32 v84, v147, v87
	v_mul_f32_e32 v85, v147, v85
	v_cvt_pk_fp8_f32 v83, v84, v85 op_sel:[0,0,1]
	global_store_dwordx2 v[126:127], v[82:83], off offset:352
	s_nop 0
	v_lshlrev_b32_e32 v82, 16, v78
	v_and_b32_e32 v78, 0xffff0000, v78
	v_mul_f32_e32 v82, v147, v82
	v_mul_f32_e32 v83, v147, v78
	v_cvt_pk_fp8_f32 v78, v82, v83
	v_lshlrev_b32_e32 v84, 16, v79
	v_and_b32_e32 v79, 0xffff0000, v79
	v_mul_f32_e32 v82, v147, v84
	v_mul_f32_e32 v79, v147, v79
	v_cvt_pk_fp8_f32 v78, v82, v79 op_sel:[0,0,1]
	v_lshlrev_b32_e32 v79, 16, v80
	v_mul_f32_e32 v82, v147, v79
	v_and_b32_e32 v79, 0xffff0000, v80
	v_mul_f32_e32 v80, v147, v79
	v_cvt_pk_fp8_f32 v79, v82, v80
	v_lshlrev_b32_e32 v83, 16, v81
	v_and_b32_e32 v81, 0xffff0000, v81
	v_mul_f32_e32 v80, v147, v83
	v_mul_f32_e32 v81, v147, v81
	v_cvt_pk_fp8_f32 v79, v80, v81 op_sel:[0,0,1]
	global_store_dwordx2 v[126:127], v[78:79], off offset:384
	s_nop 0
	v_lshlrev_b32_e32 v78, 16, v74
	v_and_b32_e32 v74, 0xffff0000, v74
	v_mul_f32_e32 v78, v147, v78
	v_mul_f32_e32 v79, v147, v74
	v_cvt_pk_fp8_f32 v74, v78, v79
	v_lshlrev_b32_e32 v80, 16, v75
	v_and_b32_e32 v75, 0xffff0000, v75
	v_mul_f32_e32 v78, v147, v80
	v_mul_f32_e32 v75, v147, v75
	v_cvt_pk_fp8_f32 v74, v78, v75 op_sel:[0,0,1]
	v_lshlrev_b32_e32 v75, 16, v76
	v_mul_f32_e32 v78, v147, v75
	v_and_b32_e32 v75, 0xffff0000, v76
	v_mul_f32_e32 v76, v147, v75
	v_cvt_pk_fp8_f32 v75, v78, v76
	v_lshlrev_b32_e32 v79, 16, v77
	v_and_b32_e32 v77, 0xffff0000, v77
	v_mul_f32_e32 v76, v147, v79
	v_mul_f32_e32 v77, v147, v77
	v_cvt_pk_fp8_f32 v75, v76, v77 op_sel:[0,0,1]
	global_store_dwordx2 v[126:127], v[74:75], off offset:416
	s_nop 0
	v_lshlrev_b32_e32 v74, 16, v70
	v_and_b32_e32 v70, 0xffff0000, v70
	v_mul_f32_e32 v74, v147, v74
	v_mul_f32_e32 v75, v147, v70
	v_cvt_pk_fp8_f32 v70, v74, v75
	v_lshlrev_b32_e32 v76, 16, v71
	v_and_b32_e32 v71, 0xffff0000, v71
	v_mul_f32_e32 v74, v147, v76
	v_mul_f32_e32 v71, v147, v71
	v_cvt_pk_fp8_f32 v70, v74, v71 op_sel:[0,0,1]
	v_lshlrev_b32_e32 v71, 16, v72
	v_mul_f32_e32 v74, v147, v71
	v_and_b32_e32 v71, 0xffff0000, v72
	v_mul_f32_e32 v72, v147, v71
	v_cvt_pk_fp8_f32 v71, v74, v72
	v_lshlrev_b32_e32 v75, 16, v73
	v_and_b32_e32 v73, 0xffff0000, v73
	v_mul_f32_e32 v72, v147, v75
	v_mul_f32_e32 v73, v147, v73
	v_cvt_pk_fp8_f32 v71, v72, v73 op_sel:[0,0,1]
	global_store_dwordx2 v[126:127], v[70:71], off offset:448
	s_nop 0
	v_lshlrev_b32_e32 v70, 16, v66
	v_and_b32_e32 v66, 0xffff0000, v66
	v_mul_f32_e32 v70, v147, v70
	v_mul_f32_e32 v71, v147, v66
	v_cvt_pk_fp8_f32 v66, v70, v71
	v_lshlrev_b32_e32 v72, 16, v67
	v_and_b32_e32 v67, 0xffff0000, v67
	v_mul_f32_e32 v70, v147, v72
	v_mul_f32_e32 v67, v147, v67
	v_cvt_pk_fp8_f32 v66, v70, v67 op_sel:[0,0,1]
	v_lshlrev_b32_e32 v67, 16, v68
	v_mul_f32_e32 v70, v147, v67
	v_and_b32_e32 v67, 0xffff0000, v68
	v_mul_f32_e32 v68, v147, v67
	v_cvt_pk_fp8_f32 v67, v70, v68
	v_lshlrev_b32_e32 v71, 16, v69
	v_and_b32_e32 v69, 0xffff0000, v69
	v_mul_f32_e32 v68, v147, v71
	v_mul_f32_e32 v69, v147, v69
	v_cvt_pk_fp8_f32 v67, v68, v69 op_sel:[0,0,1]
	global_store_dwordx2 v[126:127], v[66:67], off offset:480
	s_nop 0
	v_lshlrev_b32_e32 v66, 16, v62
	v_and_b32_e32 v62, 0xffff0000, v62
	v_mul_f32_e32 v66, v147, v66
	v_mul_f32_e32 v67, v147, v62
	v_cvt_pk_fp8_f32 v62, v66, v67
	v_lshlrev_b32_e32 v68, 16, v63
	v_and_b32_e32 v63, 0xffff0000, v63
	v_mul_f32_e32 v66, v147, v68
	v_mul_f32_e32 v63, v147, v63
	v_cvt_pk_fp8_f32 v62, v66, v63 op_sel:[0,0,1]
	v_lshlrev_b32_e32 v63, 16, v64
	v_mul_f32_e32 v66, v147, v63
	v_and_b32_e32 v63, 0xffff0000, v64
	v_mul_f32_e32 v64, v147, v63
	v_cvt_pk_fp8_f32 v63, v66, v64
	v_lshlrev_b32_e32 v67, 16, v65
	v_and_b32_e32 v65, 0xffff0000, v65
	v_mul_f32_e32 v64, v147, v67
	v_mul_f32_e32 v65, v147, v65
	v_cvt_pk_fp8_f32 v63, v64, v65 op_sel:[0,0,1]
	global_store_dwordx2 v[126:127], v[62:63], off offset:512
	s_nop 0
	v_lshlrev_b32_e32 v62, 16, v58
	v_and_b32_e32 v58, 0xffff0000, v58
	v_mul_f32_e32 v62, v147, v62
	v_mul_f32_e32 v63, v147, v58
	v_cvt_pk_fp8_f32 v58, v62, v63
	v_lshlrev_b32_e32 v64, 16, v59
	v_and_b32_e32 v59, 0xffff0000, v59
	v_mul_f32_e32 v62, v147, v64
	v_mul_f32_e32 v59, v147, v59
	v_cvt_pk_fp8_f32 v58, v62, v59 op_sel:[0,0,1]
	v_lshlrev_b32_e32 v59, 16, v60
	v_mul_f32_e32 v62, v147, v59
	v_and_b32_e32 v59, 0xffff0000, v60
	v_mul_f32_e32 v60, v147, v59
	v_cvt_pk_fp8_f32 v59, v62, v60
	v_lshlrev_b32_e32 v63, 16, v61
	v_and_b32_e32 v61, 0xffff0000, v61
	v_mul_f32_e32 v60, v147, v63
	v_mul_f32_e32 v61, v147, v61
	v_cvt_pk_fp8_f32 v59, v60, v61 op_sel:[0,0,1]
	global_store_dwordx2 v[126:127], v[58:59], off offset:544
	s_nop 0
	v_lshlrev_b32_e32 v58, 16, v54
	v_and_b32_e32 v54, 0xffff0000, v54
	v_mul_f32_e32 v58, v147, v58
	v_mul_f32_e32 v59, v147, v54
	v_cvt_pk_fp8_f32 v54, v58, v59
	v_lshlrev_b32_e32 v60, 16, v55
	v_and_b32_e32 v55, 0xffff0000, v55
	v_mul_f32_e32 v58, v147, v60
	v_mul_f32_e32 v55, v147, v55
	v_cvt_pk_fp8_f32 v54, v58, v55 op_sel:[0,0,1]
	v_lshlrev_b32_e32 v55, 16, v56
	v_mul_f32_e32 v58, v147, v55
	v_and_b32_e32 v55, 0xffff0000, v56
	v_mul_f32_e32 v56, v147, v55
	v_cvt_pk_fp8_f32 v55, v58, v56
	v_lshlrev_b32_e32 v59, 16, v57
	v_and_b32_e32 v57, 0xffff0000, v57
	v_mul_f32_e32 v56, v147, v59
	v_mul_f32_e32 v57, v147, v57
	v_cvt_pk_fp8_f32 v55, v56, v57 op_sel:[0,0,1]
	global_store_dwordx2 v[126:127], v[54:55], off offset:576
	s_nop 0
	v_lshlrev_b32_e32 v54, 16, v50
	v_and_b32_e32 v50, 0xffff0000, v50
	v_mul_f32_e32 v54, v147, v54
	v_mul_f32_e32 v55, v147, v50
	v_cvt_pk_fp8_f32 v50, v54, v55
	v_lshlrev_b32_e32 v56, 16, v51
	v_and_b32_e32 v51, 0xffff0000, v51
	v_mul_f32_e32 v54, v147, v56
	v_mul_f32_e32 v51, v147, v51
	v_cvt_pk_fp8_f32 v50, v54, v51 op_sel:[0,0,1]
	v_lshlrev_b32_e32 v51, 16, v52
	v_mul_f32_e32 v54, v147, v51
	v_and_b32_e32 v51, 0xffff0000, v52
	v_mul_f32_e32 v52, v147, v51
	v_cvt_pk_fp8_f32 v51, v54, v52
	v_lshlrev_b32_e32 v55, 16, v53
	v_and_b32_e32 v53, 0xffff0000, v53
	v_mul_f32_e32 v52, v147, v55
	v_mul_f32_e32 v53, v147, v53
	v_cvt_pk_fp8_f32 v51, v52, v53 op_sel:[0,0,1]
	global_store_dwordx2 v[126:127], v[50:51], off offset:608
	s_nop 0
	v_lshlrev_b32_e32 v50, 16, v46
	v_and_b32_e32 v46, 0xffff0000, v46
	v_mul_f32_e32 v50, v147, v50
	v_mul_f32_e32 v51, v147, v46
	v_cvt_pk_fp8_f32 v46, v50, v51
	v_lshlrev_b32_e32 v52, 16, v47
	v_and_b32_e32 v47, 0xffff0000, v47
	v_mul_f32_e32 v50, v147, v52
	v_mul_f32_e32 v47, v147, v47
	v_cvt_pk_fp8_f32 v46, v50, v47 op_sel:[0,0,1]
	v_lshlrev_b32_e32 v47, 16, v48
	v_mul_f32_e32 v50, v147, v47
	v_and_b32_e32 v47, 0xffff0000, v48
	v_mul_f32_e32 v48, v147, v47
	v_cvt_pk_fp8_f32 v47, v50, v48
	v_lshlrev_b32_e32 v51, 16, v49
	v_and_b32_e32 v49, 0xffff0000, v49
	v_mul_f32_e32 v48, v147, v51
	v_mul_f32_e32 v49, v147, v49
	v_cvt_pk_fp8_f32 v47, v48, v49 op_sel:[0,0,1]
	global_store_dwordx2 v[126:127], v[46:47], off offset:640
	s_nop 0
	v_lshlrev_b32_e32 v46, 16, v42
	v_and_b32_e32 v42, 0xffff0000, v42
	v_mul_f32_e32 v46, v147, v46
	v_mul_f32_e32 v47, v147, v42
	v_cvt_pk_fp8_f32 v42, v46, v47
	v_lshlrev_b32_e32 v48, 16, v43
	v_and_b32_e32 v43, 0xffff0000, v43
	v_mul_f32_e32 v46, v147, v48
	v_mul_f32_e32 v43, v147, v43
	v_cvt_pk_fp8_f32 v42, v46, v43 op_sel:[0,0,1]
	v_lshlrev_b32_e32 v43, 16, v44
	v_mul_f32_e32 v46, v147, v43
	v_and_b32_e32 v43, 0xffff0000, v44
	v_mul_f32_e32 v44, v147, v43
	v_cvt_pk_fp8_f32 v43, v46, v44
	v_lshlrev_b32_e32 v47, 16, v45
	v_and_b32_e32 v45, 0xffff0000, v45
	v_mul_f32_e32 v44, v147, v47
	v_mul_f32_e32 v45, v147, v45
	v_cvt_pk_fp8_f32 v43, v44, v45 op_sel:[0,0,1]
	global_store_dwordx2 v[126:127], v[42:43], off offset:672
	s_nop 0
	v_lshlrev_b32_e32 v42, 16, v38
	v_and_b32_e32 v38, 0xffff0000, v38
	v_mul_f32_e32 v42, v147, v42
	v_mul_f32_e32 v43, v147, v38
	v_cvt_pk_fp8_f32 v38, v42, v43
	v_lshlrev_b32_e32 v44, 16, v39
	v_and_b32_e32 v39, 0xffff0000, v39
	v_mul_f32_e32 v42, v147, v44
	v_mul_f32_e32 v39, v147, v39
	v_cvt_pk_fp8_f32 v38, v42, v39 op_sel:[0,0,1]
	v_lshlrev_b32_e32 v39, 16, v40
	v_mul_f32_e32 v42, v147, v39
	v_and_b32_e32 v39, 0xffff0000, v40
	v_mul_f32_e32 v40, v147, v39
	v_cvt_pk_fp8_f32 v39, v42, v40
	v_lshlrev_b32_e32 v43, 16, v41
	v_and_b32_e32 v41, 0xffff0000, v41
	v_mul_f32_e32 v40, v147, v43
	v_mul_f32_e32 v41, v147, v41
	v_cvt_pk_fp8_f32 v39, v40, v41 op_sel:[0,0,1]
	global_store_dwordx2 v[126:127], v[38:39], off offset:704
	s_nop 0
	v_lshlrev_b32_e32 v38, 16, v34
	v_and_b32_e32 v34, 0xffff0000, v34
	v_mul_f32_e32 v38, v147, v38
	v_mul_f32_e32 v39, v147, v34
	v_cvt_pk_fp8_f32 v34, v38, v39
	v_lshlrev_b32_e32 v40, 16, v35
	v_and_b32_e32 v35, 0xffff0000, v35
	v_mul_f32_e32 v38, v147, v40
	v_mul_f32_e32 v35, v147, v35
	v_cvt_pk_fp8_f32 v34, v38, v35 op_sel:[0,0,1]
	v_lshlrev_b32_e32 v35, 16, v36
	v_mul_f32_e32 v38, v147, v35
	v_and_b32_e32 v35, 0xffff0000, v36
	v_mul_f32_e32 v36, v147, v35
	v_cvt_pk_fp8_f32 v35, v38, v36
	v_lshlrev_b32_e32 v39, 16, v37
	v_and_b32_e32 v37, 0xffff0000, v37
	v_mul_f32_e32 v36, v147, v39
	v_mul_f32_e32 v37, v147, v37
	v_cvt_pk_fp8_f32 v35, v36, v37 op_sel:[0,0,1]
	global_store_dwordx2 v[126:127], v[34:35], off offset:736
	s_nop 0
	v_lshlrev_b32_e32 v34, 16, v30
	v_and_b32_e32 v30, 0xffff0000, v30
	v_mul_f32_e32 v34, v147, v34
	v_mul_f32_e32 v35, v147, v30
	v_cvt_pk_fp8_f32 v30, v34, v35
	v_lshlrev_b32_e32 v36, 16, v31
	v_and_b32_e32 v31, 0xffff0000, v31
	v_mul_f32_e32 v34, v147, v36
	v_mul_f32_e32 v31, v147, v31
	v_cvt_pk_fp8_f32 v30, v34, v31 op_sel:[0,0,1]
	v_lshlrev_b32_e32 v31, 16, v32
	v_mul_f32_e32 v34, v147, v31
	v_and_b32_e32 v31, 0xffff0000, v32
	v_mul_f32_e32 v32, v147, v31
	v_cvt_pk_fp8_f32 v31, v34, v32
	v_lshlrev_b32_e32 v35, 16, v33
	v_and_b32_e32 v33, 0xffff0000, v33
	v_mul_f32_e32 v32, v147, v35
	v_mul_f32_e32 v33, v147, v33
	v_cvt_pk_fp8_f32 v31, v32, v33 op_sel:[0,0,1]
	global_store_dwordx2 v[126:127], v[30:31], off offset:768
	s_nop 0
	v_lshlrev_b32_e32 v30, 16, v26
	v_and_b32_e32 v26, 0xffff0000, v26
	v_mul_f32_e32 v30, v147, v30
	v_mul_f32_e32 v31, v147, v26
	v_cvt_pk_fp8_f32 v26, v30, v31
	v_lshlrev_b32_e32 v32, 16, v27
	v_and_b32_e32 v27, 0xffff0000, v27
	v_mul_f32_e32 v30, v147, v32
	v_mul_f32_e32 v27, v147, v27
	v_cvt_pk_fp8_f32 v26, v30, v27 op_sel:[0,0,1]
	v_lshlrev_b32_e32 v27, 16, v28
	v_mul_f32_e32 v30, v147, v27
	v_and_b32_e32 v27, 0xffff0000, v28
	v_mul_f32_e32 v28, v147, v27
	v_cvt_pk_fp8_f32 v27, v30, v28
	v_lshlrev_b32_e32 v31, 16, v29
	v_and_b32_e32 v29, 0xffff0000, v29
	v_mul_f32_e32 v28, v147, v31
	v_mul_f32_e32 v29, v147, v29
	v_cvt_pk_fp8_f32 v27, v28, v29 op_sel:[0,0,1]
	global_store_dwordx2 v[126:127], v[26:27], off offset:800
	s_nop 0
	v_lshlrev_b32_e32 v26, 16, v22
	v_and_b32_e32 v22, 0xffff0000, v22
	v_mul_f32_e32 v26, v147, v26
	v_mul_f32_e32 v27, v147, v22
	v_cvt_pk_fp8_f32 v22, v26, v27
	v_lshlrev_b32_e32 v28, 16, v23
	v_and_b32_e32 v23, 0xffff0000, v23
	v_mul_f32_e32 v26, v147, v28
	v_mul_f32_e32 v23, v147, v23
	v_cvt_pk_fp8_f32 v22, v26, v23 op_sel:[0,0,1]
	v_lshlrev_b32_e32 v23, 16, v24
	v_mul_f32_e32 v26, v147, v23
	v_and_b32_e32 v23, 0xffff0000, v24
	v_mul_f32_e32 v24, v147, v23
	v_cvt_pk_fp8_f32 v23, v26, v24
	v_lshlrev_b32_e32 v27, 16, v25
	v_and_b32_e32 v25, 0xffff0000, v25
	v_mul_f32_e32 v24, v147, v27
	v_mul_f32_e32 v25, v147, v25
	v_cvt_pk_fp8_f32 v23, v24, v25 op_sel:[0,0,1]
	global_store_dwordx2 v[126:127], v[22:23], off offset:832
	s_nop 0
	v_lshlrev_b32_e32 v22, 16, v18
	v_and_b32_e32 v18, 0xffff0000, v18
	v_mul_f32_e32 v22, v147, v22
	v_mul_f32_e32 v23, v147, v18
	v_cvt_pk_fp8_f32 v18, v22, v23
	v_lshlrev_b32_e32 v24, 16, v19
	v_and_b32_e32 v19, 0xffff0000, v19
	v_mul_f32_e32 v22, v147, v24
	v_mul_f32_e32 v19, v147, v19
	v_cvt_pk_fp8_f32 v18, v22, v19 op_sel:[0,0,1]
	v_lshlrev_b32_e32 v19, 16, v20
	v_mul_f32_e32 v22, v147, v19
	v_and_b32_e32 v19, 0xffff0000, v20
	v_mul_f32_e32 v20, v147, v19
	v_cvt_pk_fp8_f32 v19, v22, v20
	v_lshlrev_b32_e32 v23, 16, v21
	v_and_b32_e32 v21, 0xffff0000, v21
	v_mul_f32_e32 v20, v147, v23
	v_mul_f32_e32 v21, v147, v21
	v_cvt_pk_fp8_f32 v19, v20, v21 op_sel:[0,0,1]
	global_store_dwordx2 v[126:127], v[18:19], off offset:864
	s_nop 0
	v_lshlrev_b32_e32 v18, 16, v14
	v_and_b32_e32 v14, 0xffff0000, v14
	v_mul_f32_e32 v18, v147, v18
	v_mul_f32_e32 v19, v147, v14
	v_cvt_pk_fp8_f32 v14, v18, v19
	v_lshlrev_b32_e32 v20, 16, v15
	v_and_b32_e32 v15, 0xffff0000, v15
	v_mul_f32_e32 v18, v147, v20
	v_mul_f32_e32 v15, v147, v15
	v_cvt_pk_fp8_f32 v14, v18, v15 op_sel:[0,0,1]
	v_lshlrev_b32_e32 v15, 16, v16
	v_mul_f32_e32 v18, v147, v15
	v_and_b32_e32 v15, 0xffff0000, v16
	v_mul_f32_e32 v16, v147, v15
	v_cvt_pk_fp8_f32 v15, v18, v16
	v_lshlrev_b32_e32 v19, 16, v17
	v_and_b32_e32 v17, 0xffff0000, v17
	v_mul_f32_e32 v16, v147, v19
	v_mul_f32_e32 v17, v147, v17
	v_cvt_pk_fp8_f32 v15, v16, v17 op_sel:[0,0,1]
	global_store_dwordx2 v[126:127], v[14:15], off offset:896
	s_nop 0
	v_lshlrev_b32_e32 v14, 16, v10
	v_and_b32_e32 v10, 0xffff0000, v10
	v_mul_f32_e32 v14, v147, v14
	v_mul_f32_e32 v15, v147, v10
	v_cvt_pk_fp8_f32 v10, v14, v15
	v_lshlrev_b32_e32 v16, 16, v11
	v_and_b32_e32 v11, 0xffff0000, v11
	v_mul_f32_e32 v14, v147, v16
	v_mul_f32_e32 v11, v147, v11
	v_cvt_pk_fp8_f32 v10, v14, v11 op_sel:[0,0,1]
	v_lshlrev_b32_e32 v11, 16, v12
	v_mul_f32_e32 v14, v147, v11
	v_and_b32_e32 v11, 0xffff0000, v12
	v_mul_f32_e32 v12, v147, v11
	v_cvt_pk_fp8_f32 v11, v14, v12
	v_lshlrev_b32_e32 v15, 16, v13
	v_and_b32_e32 v13, 0xffff0000, v13
	v_mul_f32_e32 v12, v147, v15
	v_mul_f32_e32 v13, v147, v13
	v_cvt_pk_fp8_f32 v11, v12, v13 op_sel:[0,0,1]
	global_store_dwordx2 v[126:127], v[10:11], off offset:928
	s_nop 0
	v_lshlrev_b32_e32 v10, 16, v6
	v_and_b32_e32 v6, 0xffff0000, v6
	v_mul_f32_e32 v10, v147, v10
	v_mul_f32_e32 v11, v147, v6
	v_cvt_pk_fp8_f32 v6, v10, v11
	v_lshlrev_b32_e32 v12, 16, v7
	v_and_b32_e32 v7, 0xffff0000, v7
	v_mul_f32_e32 v10, v147, v12
	v_mul_f32_e32 v7, v147, v7
	v_cvt_pk_fp8_f32 v6, v10, v7 op_sel:[0,0,1]
	v_lshlrev_b32_e32 v7, 16, v8
	v_mul_f32_e32 v10, v147, v7
	v_and_b32_e32 v7, 0xffff0000, v8
	v_mul_f32_e32 v8, v147, v7
	v_cvt_pk_fp8_f32 v7, v10, v8
	v_lshlrev_b32_e32 v11, 16, v9
	v_and_b32_e32 v9, 0xffff0000, v9
	v_mul_f32_e32 v8, v147, v11
	v_mul_f32_e32 v9, v147, v9
	v_cvt_pk_fp8_f32 v7, v8, v9 op_sel:[0,0,1]
	global_store_dwordx2 v[126:127], v[6:7], off offset:960
	s_nop 0
	v_lshlrev_b32_e32 v6, 16, v2
	v_and_b32_e32 v2, 0xffff0000, v2
	v_mul_f32_e32 v6, v147, v6
	v_mul_f32_e32 v7, v147, v2
	v_cvt_pk_fp8_f32 v2, v6, v7
	v_lshlrev_b32_e32 v8, 16, v3
	v_and_b32_e32 v3, 0xffff0000, v3
	v_mul_f32_e32 v6, v147, v8
	v_mul_f32_e32 v3, v147, v3
	v_cvt_pk_fp8_f32 v2, v6, v3 op_sel:[0,0,1]
	v_lshlrev_b32_e32 v3, 16, v4
	v_mul_f32_e32 v6, v147, v3
	v_and_b32_e32 v3, 0xffff0000, v4
	v_mul_f32_e32 v4, v147, v3
	v_cvt_pk_fp8_f32 v3, v6, v4
	v_lshlrev_b32_e32 v7, 16, v5
	v_and_b32_e32 v5, 0xffff0000, v5
	v_mul_f32_e32 v4, v147, v7
	v_mul_f32_e32 v5, v147, v5
	v_cvt_pk_fp8_f32 v3, v4, v5 op_sel:[0,0,1]
	ds_bpermute_b32 v4, v179, v145
	ds_bpermute_b32 v5, v185, v145
	global_store_dwordx2 v[126:127], v[2:3], off offset:992
	ds_bpermute_b32 v2, v181, v145
	s_waitcnt lgkmcnt(2)
	v_fma_f32 v3, v130, v4, v172
	v_fma_f32 v4, v134, v4, v173
	s_waitcnt lgkmcnt(0)
	ds_write2_b32 v180, v3, v4 offset1:16
	ds_bpermute_b32 v3, v183, v145
	s_waitcnt lgkmcnt(2)
	v_fma_f32 v4, v131, v2, v172
	v_fma_f32 v2, v135, v2, v173
	ds_write2_b32 v182, v4, v2 offset1:16
	s_waitcnt lgkmcnt(1)
	v_fma_f32 v2, v132, v3, v172
	v_fma_f32 v3, v136, v3, v173
	ds_write2_b32 v184, v2, v3 offset1:16
	v_fma_f32 v2, v133, v5, v172
	v_fma_f32 v3, v137, v5, v173
	ds_write2_b32 v186, v2, v3 offset1:16
	s_waitcnt lgkmcnt(0)
	s_and_saveexec_b64 s[20:21], s[6:7]
	s_cbranch_execz .LBB0_439
	v_add_u32_e32 v2, s0, v176
	ds_read2_b32 v[32:33], v2 offset1:1
	ds_read2_b32 v[30:31], v2 offset0:2 offset1:3
	ds_read2_b32 v[28:29], v2 offset0:4 offset1:5
	ds_read2_b32 v[26:27], v2 offset0:6 offset1:7
	ds_read2_b32 v[24:25], v2 offset0:8 offset1:9
	ds_read2_b32 v[22:23], v2 offset0:10 offset1:11
	ds_read2_b32 v[20:21], v2 offset0:12 offset1:13
	ds_read2_b32 v[18:19], v2 offset0:14 offset1:15
	ds_read2_b32 v[16:17], v2 offset0:16 offset1:17
	ds_read2_b32 v[14:15], v2 offset0:18 offset1:19
	ds_read2_b32 v[12:13], v2 offset0:20 offset1:21
	ds_read2_b32 v[10:11], v2 offset0:22 offset1:23
	ds_read2_b32 v[8:9], v2 offset0:24 offset1:25
	ds_read2_b32 v[6:7], v2 offset0:26 offset1:27
	ds_read2_b32 v[4:5], v2 offset0:28 offset1:29
	ds_read2_b32 v[2:3], v2 offset0:30 offset1:31
	s_waitcnt lgkmcnt(14)
	v_cmp_gt_f32_e32 vcc, v33, v32
	s_nop 1
	v_cndmask_b32_e32 v35, v32, v33, vcc
	v_cndmask_b32_e64 v34, 0, 1, vcc
	v_cmp_gt_f32_e32 vcc, v30, v35
	s_nop 1
	v_cndmask_b32_e32 v35, v35, v30, vcc
	v_cndmask_b32_e64 v34, v34, 2, vcc
	v_cmp_gt_f32_e32 vcc, v31, v35
	s_nop 1
	v_cndmask_b32_e32 v35, v35, v31, vcc
	v_cndmask_b32_e64 v34, v34, 3, vcc
	s_waitcnt lgkmcnt(13)
	v_cmp_gt_f32_e32 vcc, v28, v35
	s_nop 1
	v_cndmask_b32_e32 v35, v35, v28, vcc
	v_cndmask_b32_e64 v34, v34, 4, vcc
	v_cmp_gt_f32_e32 vcc, v29, v35
	s_nop 1
	v_cndmask_b32_e32 v35, v35, v29, vcc
	v_cndmask_b32_e64 v34, v34, 5, vcc
	s_waitcnt lgkmcnt(12)
	v_cmp_gt_f32_e32 vcc, v26, v35
	s_nop 1
	v_cndmask_b32_e32 v35, v35, v26, vcc
	v_cndmask_b32_e64 v34, v34, 6, vcc
	v_cmp_gt_f32_e32 vcc, v27, v35
	s_nop 1
	v_cndmask_b32_e32 v35, v35, v27, vcc
	v_cndmask_b32_e64 v34, v34, 7, vcc
	s_waitcnt lgkmcnt(11)
	v_cmp_gt_f32_e32 vcc, v24, v35
	s_nop 1
	v_cndmask_b32_e32 v35, v35, v24, vcc
	v_cndmask_b32_e64 v34, v34, 8, vcc
	v_cmp_gt_f32_e32 vcc, v25, v35
	s_nop 1
	v_cndmask_b32_e32 v35, v35, v25, vcc
	v_cndmask_b32_e64 v34, v34, 9, vcc
	s_waitcnt lgkmcnt(10)
	v_cmp_gt_f32_e32 vcc, v22, v35
	s_nop 1
	v_cndmask_b32_e32 v35, v35, v22, vcc
	v_cndmask_b32_e64 v34, v34, 10, vcc
	v_cmp_gt_f32_e32 vcc, v23, v35
	s_nop 1
	v_cndmask_b32_e32 v35, v35, v23, vcc
	v_cndmask_b32_e64 v34, v34, 11, vcc
	s_waitcnt lgkmcnt(9)
	v_cmp_gt_f32_e32 vcc, v20, v35
	s_nop 1
	v_cndmask_b32_e32 v35, v35, v20, vcc
	v_cndmask_b32_e64 v34, v34, 12, vcc
	v_cmp_gt_f32_e32 vcc, v21, v35
	s_nop 1
	v_cndmask_b32_e32 v35, v35, v21, vcc
	v_cndmask_b32_e64 v34, v34, 13, vcc
	s_waitcnt lgkmcnt(8)
	v_cmp_gt_f32_e32 vcc, v18, v35
	s_nop 1
	v_cndmask_b32_e32 v35, v35, v18, vcc
	v_cndmask_b32_e64 v34, v34, 14, vcc
	v_cmp_gt_f32_e32 vcc, v19, v35
	s_nop 1
	v_cndmask_b32_e32 v35, v35, v19, vcc
	v_cndmask_b32_e64 v34, v34, 15, vcc
	s_waitcnt lgkmcnt(7)
	v_cmp_gt_f32_e32 vcc, v16, v35
	s_nop 1
	v_cndmask_b32_e32 v35, v35, v16, vcc
	v_cndmask_b32_e64 v34, v34, 16, vcc
	v_cmp_gt_f32_e32 vcc, v17, v35
	s_nop 1
	v_cndmask_b32_e32 v35, v35, v17, vcc
	v_cndmask_b32_e64 v34, v34, 17, vcc
	s_waitcnt lgkmcnt(6)
	v_cmp_gt_f32_e32 vcc, v14, v35
	s_nop 1
	v_cndmask_b32_e32 v35, v35, v14, vcc
	v_cndmask_b32_e64 v34, v34, 18, vcc
	v_cmp_gt_f32_e32 vcc, v15, v35
	s_nop 1
	v_cndmask_b32_e32 v35, v35, v15, vcc
	v_cndmask_b32_e64 v34, v34, 19, vcc
	s_waitcnt lgkmcnt(5)
	v_cmp_gt_f32_e32 vcc, v12, v35
	s_nop 1
	v_cndmask_b32_e32 v35, v35, v12, vcc
	v_cndmask_b32_e64 v34, v34, 20, vcc
	v_cmp_gt_f32_e32 vcc, v13, v35
	s_nop 1
	v_cndmask_b32_e32 v35, v35, v13, vcc
	v_cndmask_b32_e64 v34, v34, 21, vcc
	s_waitcnt lgkmcnt(4)
	v_cmp_gt_f32_e32 vcc, v10, v35
	s_nop 1
	v_cndmask_b32_e32 v35, v35, v10, vcc
	v_cndmask_b32_e64 v34, v34, 22, vcc
	v_cmp_gt_f32_e32 vcc, v11, v35
	s_nop 1
	v_cndmask_b32_e32 v35, v35, v11, vcc
	v_cndmask_b32_e64 v34, v34, 23, vcc
	s_waitcnt lgkmcnt(3)
	v_cmp_gt_f32_e32 vcc, v8, v35
	s_nop 1
	v_cndmask_b32_e32 v35, v35, v8, vcc
	v_cndmask_b32_e64 v34, v34, 24, vcc
	v_cmp_gt_f32_e32 vcc, v9, v35
	s_nop 1
	v_cndmask_b32_e32 v35, v35, v9, vcc
	v_cndmask_b32_e64 v34, v34, 25, vcc
	s_waitcnt lgkmcnt(2)
	v_cmp_gt_f32_e32 vcc, v6, v35
	s_nop 1
	v_cndmask_b32_e32 v35, v35, v6, vcc
	v_cndmask_b32_e64 v34, v34, 26, vcc
	v_cmp_gt_f32_e32 vcc, v7, v35
	s_nop 1
	v_cndmask_b32_e32 v35, v35, v7, vcc
	v_cndmask_b32_e64 v34, v34, 27, vcc
	s_waitcnt lgkmcnt(1)
	v_cmp_gt_f32_e32 vcc, v4, v35
	s_nop 1
	v_cndmask_b32_e32 v35, v35, v4, vcc
	v_cndmask_b32_e64 v34, v34, 28, vcc
	v_cmp_gt_f32_e32 vcc, v5, v35
	s_nop 1
	v_cndmask_b32_e32 v35, v35, v5, vcc
	v_cndmask_b32_e64 v34, v34, 29, vcc
	s_waitcnt lgkmcnt(0)
	v_cmp_gt_f32_e32 vcc, v2, v35
	s_nop 1
	v_cndmask_b32_e32 v35, v35, v2, vcc
	v_cndmask_b32_e64 v34, v34, 30, vcc
	v_cmp_gt_f32_e32 vcc, v3, v35
	s_nop 1
	v_cndmask_b32_e64 v144, v34, 31, vcc
	v_cndmask_b32_e32 v34, v35, v3, vcc
	v_cmp_eq_u32_e32 vcc, 0, v144
	v_lshlrev_b32_e64 v36, v144, 1
	v_and_b32_e32 v38, 2, v36
	v_cndmask_b32_e32 v37, v32, v198, vcc
	v_cmp_gt_f32_e64 s[8:9], v33, v37
	v_cndmask_b32_e64 v35, 0, -1, vcc
	s_or_b64 vcc, vcc, s[8:9]
	v_cndmask_b32_e64 v39, 0, 1, vcc
	v_cndmask_b32_e32 v40, v32, v33, vcc
	v_cmp_eq_u32_e32 vcc, 0, v38
	v_and_b32_e32 v38, 4, v36
	s_nop 0
	v_cndmask_b32_e32 v37, v37, v40, vcc
	v_cndmask_b32_e32 v35, v35, v39, vcc
	v_cmp_eq_u32_e32 vcc, 0, v38
	v_cmp_gt_f32_e64 s[8:9], v30, v37
	s_and_b64 vcc, vcc, s[8:9]
	v_cndmask_b32_e64 v35, v35, 2, vcc
	v_cndmask_b32_e32 v37, v37, v30, vcc
	v_and_b32_e32 v38, 8, v36
	v_cmp_gt_i32_e64 s[8:9], 0, v35
	v_cmp_gt_f32_e64 s[10:11], v31, v37
	v_cmp_eq_u32_e32 vcc, 0, v38
	s_or_b64 s[8:9], s[8:9], s[10:11]
	s_and_b64 vcc, vcc, s[8:9]
	v_cndmask_b32_e64 v35, v35, 3, vcc
	v_cndmask_b32_e32 v37, v37, v31, vcc
	v_and_b32_e32 v38, 16, v36
	v_cmp_gt_i32_e64 s[8:9], 0, v35
	v_cmp_gt_f32_e64 s[10:11], v28, v37
	v_cmp_eq_u32_e32 vcc, 0, v38
	s_or_b64 s[8:9], s[8:9], s[10:11]
	s_and_b64 vcc, vcc, s[8:9]
	v_cndmask_b32_e64 v35, v35, 4, vcc
	v_cndmask_b32_e32 v37, v37, v28, vcc
	v_and_b32_e32 v38, 32, v36
	v_cmp_gt_i32_e64 s[8:9], 0, v35
	v_cmp_gt_f32_e64 s[10:11], v29, v37
	v_cmp_eq_u32_e32 vcc, 0, v38
	s_or_b64 s[8:9], s[8:9], s[10:11]
	s_and_b64 vcc, vcc, s[8:9]
	v_cndmask_b32_e64 v35, v35, 5, vcc
	v_cndmask_b32_e32 v37, v37, v29, vcc
	v_and_b32_e32 v38, 64, v36
	v_cmp_gt_i32_e64 s[8:9], 0, v35
	v_cmp_gt_f32_e64 s[10:11], v26, v37
	v_cmp_eq_u32_e32 vcc, 0, v38
	s_or_b64 s[8:9], s[8:9], s[10:11]
	s_and_b64 vcc, vcc, s[8:9]
	v_cndmask_b32_e64 v35, v35, 6, vcc
	v_cndmask_b32_e32 v37, v37, v26, vcc
	v_and_b32_e32 v38, 0x80, v36
	v_cmp_gt_i32_e64 s[8:9], 0, v35
	v_cmp_gt_f32_e64 s[10:11], v27, v37
	v_cmp_eq_u32_e32 vcc, 0, v38
	s_or_b64 s[8:9], s[8:9], s[10:11]
	s_and_b64 vcc, vcc, s[8:9]
	v_cndmask_b32_e64 v35, v35, 7, vcc
	v_cndmask_b32_e32 v37, v37, v27, vcc
	v_and_b32_e32 v38, 0x100, v36
	v_cmp_gt_i32_e64 s[8:9], 0, v35
	v_cmp_gt_f32_e64 s[10:11], v24, v37
	v_cmp_eq_u32_e32 vcc, 0, v38
	s_or_b64 s[8:9], s[8:9], s[10:11]
	s_and_b64 vcc, vcc, s[8:9]
	v_cndmask_b32_e64 v35, v35, 8, vcc
	v_cndmask_b32_e32 v37, v37, v24, vcc
	v_and_b32_e32 v38, 0x200, v36
	v_cmp_gt_i32_e64 s[8:9], 0, v35
	v_cmp_gt_f32_e64 s[10:11], v25, v37
	v_cmp_eq_u32_e32 vcc, 0, v38
	s_or_b64 s[8:9], s[8:9], s[10:11]
	s_and_b64 vcc, vcc, s[8:9]
	v_cndmask_b32_e64 v35, v35, 9, vcc
	v_cndmask_b32_e32 v37, v37, v25, vcc
	v_and_b32_e32 v38, 0x400, v36
	v_cmp_gt_i32_e64 s[8:9], 0, v35
	v_cmp_gt_f32_e64 s[10:11], v22, v37
	v_cmp_eq_u32_e32 vcc, 0, v38
	s_or_b64 s[8:9], s[8:9], s[10:11]
	s_and_b64 vcc, vcc, s[8:9]
	v_cndmask_b32_e64 v35, v35, 10, vcc
	v_cndmask_b32_e32 v37, v37, v22, vcc
	v_and_b32_e32 v38, 0x800, v36
	v_cmp_gt_i32_e64 s[8:9], 0, v35
	v_cmp_gt_f32_e64 s[10:11], v23, v37
	v_cmp_eq_u32_e32 vcc, 0, v38
	s_or_b64 s[8:9], s[8:9], s[10:11]
	s_and_b64 vcc, vcc, s[8:9]
	v_cndmask_b32_e64 v35, v35, 11, vcc
	v_cndmask_b32_e32 v37, v37, v23, vcc
	v_and_b32_e32 v38, 0x1000, v36
	v_cmp_gt_i32_e64 s[8:9], 0, v35
	v_cmp_gt_f32_e64 s[10:11], v20, v37
	v_cmp_eq_u32_e32 vcc, 0, v38
	s_or_b64 s[8:9], s[8:9], s[10:11]
	s_and_b64 vcc, vcc, s[8:9]
	v_cndmask_b32_e64 v35, v35, 12, vcc
	v_cndmask_b32_e32 v37, v37, v20, vcc
	v_and_b32_e32 v38, 0x2000, v36
	v_cmp_gt_i32_e64 s[8:9], 0, v35
	v_cmp_gt_f32_e64 s[10:11], v21, v37
	v_cmp_eq_u32_e32 vcc, 0, v38
	s_or_b64 s[8:9], s[8:9], s[10:11]
	s_and_b64 vcc, vcc, s[8:9]
	v_cndmask_b32_e64 v35, v35, 13, vcc
	v_cndmask_b32_e32 v37, v37, v21, vcc
	v_and_b32_e32 v38, 0x4000, v36
	v_cmp_gt_i32_e64 s[8:9], 0, v35
	v_cmp_gt_f32_e64 s[10:11], v18, v37
	v_cmp_eq_u32_e32 vcc, 0, v38
	s_or_b64 s[8:9], s[8:9], s[10:11]
	s_and_b64 vcc, vcc, s[8:9]
	v_cndmask_b32_e64 v35, v35, 14, vcc
	v_cndmask_b32_e32 v37, v37, v18, vcc
	v_and_b32_e32 v38, 0x8000, v36
	v_cmp_gt_i32_e64 s[8:9], 0, v35
	v_cmp_gt_f32_e64 s[10:11], v19, v37
	v_cmp_eq_u32_e32 vcc, 0, v38
	s_or_b64 s[8:9], s[8:9], s[10:11]
	s_and_b64 vcc, vcc, s[8:9]
	v_cndmask_b32_e64 v35, v35, 15, vcc
	v_cndmask_b32_e32 v37, v37, v19, vcc
	v_and_b32_e32 v38, 0x10000, v36
	v_cmp_gt_i32_e64 s[8:9], 0, v35
	v_cmp_gt_f32_e64 s[10:11], v16, v37
	v_cmp_eq_u32_e32 vcc, 0, v38
	s_or_b64 s[8:9], s[8:9], s[10:11]
	s_and_b64 vcc, vcc, s[8:9]
	v_cndmask_b32_e64 v35, v35, 16, vcc
	v_cndmask_b32_e32 v37, v37, v16, vcc
	v_and_b32_e32 v38, 0x20000, v36
	v_cmp_gt_i32_e64 s[8:9], 0, v35
	v_cmp_gt_f32_e64 s[10:11], v17, v37
	v_cmp_eq_u32_e32 vcc, 0, v38
	s_or_b64 s[8:9], s[8:9], s[10:11]
	s_and_b64 vcc, vcc, s[8:9]
	v_cndmask_b32_e64 v35, v35, 17, vcc
	v_cndmask_b32_e32 v37, v37, v17, vcc
	v_and_b32_e32 v38, 0x40000, v36
	v_cmp_gt_i32_e64 s[8:9], 0, v35
	v_cmp_gt_f32_e64 s[10:11], v14, v37
	v_cmp_eq_u32_e32 vcc, 0, v38
	s_or_b64 s[8:9], s[8:9], s[10:11]
	s_and_b64 vcc, vcc, s[8:9]
	v_cndmask_b32_e64 v35, v35, 18, vcc
	v_cndmask_b32_e32 v37, v37, v14, vcc
	v_and_b32_e32 v38, 0x80000, v36
	v_cmp_gt_i32_e64 s[8:9], 0, v35
	v_cmp_gt_f32_e64 s[10:11], v15, v37
	v_cmp_eq_u32_e32 vcc, 0, v38
	s_or_b64 s[8:9], s[8:9], s[10:11]
	s_and_b64 vcc, vcc, s[8:9]
	v_cndmask_b32_e64 v35, v35, 19, vcc
	v_cndmask_b32_e32 v37, v37, v15, vcc
	v_and_b32_e32 v38, 0x100000, v36
	v_cmp_gt_i32_e64 s[8:9], 0, v35
	v_cmp_gt_f32_e64 s[10:11], v12, v37
	v_cmp_eq_u32_e32 vcc, 0, v38
	s_or_b64 s[8:9], s[8:9], s[10:11]
	s_and_b64 vcc, vcc, s[8:9]
	v_cndmask_b32_e64 v35, v35, 20, vcc
	v_cndmask_b32_e32 v37, v37, v12, vcc
	v_and_b32_e32 v38, 0x200000, v36
	v_cmp_gt_i32_e64 s[8:9], 0, v35
	v_cmp_gt_f32_e64 s[10:11], v13, v37
	v_cmp_eq_u32_e32 vcc, 0, v38
	s_or_b64 s[8:9], s[8:9], s[10:11]
	s_and_b64 vcc, vcc, s[8:9]
	v_cndmask_b32_e64 v35, v35, 21, vcc
	v_cndmask_b32_e32 v37, v37, v13, vcc
	v_and_b32_e32 v38, 0x400000, v36
	v_cmp_gt_i32_e64 s[8:9], 0, v35
	v_cmp_gt_f32_e64 s[10:11], v10, v37
	v_cmp_eq_u32_e32 vcc, 0, v38
	s_or_b64 s[8:9], s[8:9], s[10:11]
	s_and_b64 vcc, vcc, s[8:9]
	v_cndmask_b32_e64 v35, v35, 22, vcc
	v_cndmask_b32_e32 v37, v37, v10, vcc
	v_and_b32_e32 v38, 0x800000, v36
	v_cmp_gt_i32_e64 s[8:9], 0, v35
	v_cmp_gt_f32_e64 s[10:11], v11, v37
	v_cmp_eq_u32_e32 vcc, 0, v38
	s_or_b64 s[8:9], s[8:9], s[10:11]
	s_and_b64 vcc, vcc, s[8:9]
	v_cndmask_b32_e64 v35, v35, 23, vcc
	v_cndmask_b32_e32 v37, v37, v11, vcc
	v_and_b32_e32 v38, 0x1000000, v36
	v_cmp_gt_i32_e64 s[8:9], 0, v35
	v_cmp_gt_f32_e64 s[10:11], v8, v37
	v_cmp_eq_u32_e32 vcc, 0, v38
	s_or_b64 s[8:9], s[8:9], s[10:11]
	s_and_b64 vcc, vcc, s[8:9]
	v_cndmask_b32_e64 v35, v35, 24, vcc
	v_cndmask_b32_e32 v37, v37, v8, vcc
	v_and_b32_e32 v38, 0x2000000, v36
	v_cmp_gt_i32_e64 s[8:9], 0, v35
	v_cmp_gt_f32_e64 s[10:11], v9, v37
	v_cmp_eq_u32_e32 vcc, 0, v38
	s_or_b64 s[8:9], s[8:9], s[10:11]
	s_and_b64 vcc, vcc, s[8:9]
	v_cndmask_b32_e64 v35, v35, 25, vcc
	v_cndmask_b32_e32 v37, v37, v9, vcc
	v_and_b32_e32 v38, 0x4000000, v36
	v_cmp_gt_i32_e64 s[8:9], 0, v35
	v_cmp_gt_f32_e64 s[10:11], v6, v37
	v_cmp_eq_u32_e32 vcc, 0, v38
	s_or_b64 s[8:9], s[8:9], s[10:11]
	s_and_b64 vcc, vcc, s[8:9]
	v_cndmask_b32_e64 v35, v35, 26, vcc
	v_cndmask_b32_e32 v37, v37, v6, vcc
	v_and_b32_e32 v38, 0x8000000, v36
	v_cmp_gt_i32_e64 s[8:9], 0, v35
	v_cmp_gt_f32_e64 s[10:11], v7, v37
	v_cmp_eq_u32_e32 vcc, 0, v38
	s_or_b64 s[8:9], s[8:9], s[10:11]
	s_and_b64 vcc, vcc, s[8:9]
	v_cndmask_b32_e64 v35, v35, 27, vcc
	v_cndmask_b32_e32 v37, v37, v7, vcc
	v_and_b32_e32 v38, 0x10000000, v36
	v_cmp_gt_i32_e64 s[8:9], 0, v35
	v_cmp_gt_f32_e64 s[10:11], v4, v37
	v_cmp_eq_u32_e32 vcc, 0, v38
	s_or_b64 s[8:9], s[8:9], s[10:11]
	s_and_b64 vcc, vcc, s[8:9]
	v_cndmask_b32_e64 v35, v35, 28, vcc
	v_cndmask_b32_e32 v37, v37, v4, vcc
	v_and_b32_e32 v38, 0x20000000, v36
	v_cmp_gt_i32_e64 s[8:9], 0, v35
	v_cmp_gt_f32_e64 s[10:11], v5, v37
	v_cmp_eq_u32_e32 vcc, 0, v38
	s_or_b64 s[8:9], s[8:9], s[10:11]
	s_and_b64 vcc, vcc, s[8:9]
	v_cndmask_b32_e64 v35, v35, 29, vcc
	v_cndmask_b32_e32 v37, v37, v5, vcc
	v_and_b32_e32 v38, 2.0, v36
	v_cmp_gt_i32_e64 s[8:9], 0, v35
	v_cmp_gt_f32_e64 s[10:11], v2, v37
	v_cmp_eq_u32_e32 vcc, 0, v38
	s_or_b64 s[8:9], s[8:9], s[10:11]
	s_and_b64 vcc, vcc, s[8:9]
	v_cndmask_b32_e64 v35, v35, 30, vcc
	v_cndmask_b32_e32 v37, v37, v2, vcc
	v_cmp_gt_i32_e32 vcc, 0, v35
	v_cmp_gt_f32_e64 s[8:9], v3, v37
	s_or_b64 vcc, vcc, s[8:9]
	v_cndmask_b32_e64 v38, v35, 31, vcc
	v_cndmask_b32_e32 v39, v37, v3, vcc
	v_cmp_eq_u32_e32 vcc, 31, v144
	s_nop 1
	v_cndmask_b32_e32 v148, v38, v35, vcc
	v_lshl_or_b32 v36, 1, v148, v36
	v_cndmask_b32_e32 v35, v39, v37, vcc
	v_and_b32_e32 v37, 1, v36
	v_cmp_eq_u32_e32 vcc, 1, v37
	v_and_b32_e32 v39, 2, v36
	v_bfe_i32 v38, v36, 0, 1
	v_cndmask_b32_e32 v37, v32, v198, vcc
	v_cmp_gt_f32_e64 s[8:9], v33, v37
	s_or_b64 vcc, vcc, s[8:9]
	v_cndmask_b32_e64 v40, 0, 1, vcc
	v_cndmask_b32_e32 v41, v32, v33, vcc
	v_cmp_eq_u32_e32 vcc, 0, v39
	v_and_b32_e32 v39, 4, v36
	s_nop 0
	v_cndmask_b32_e32 v38, v38, v40, vcc
	v_cndmask_b32_e32 v37, v37, v41, vcc
	v_cmp_eq_u32_e32 vcc, 0, v39
	v_and_b32_e32 v39, 3, v36
	v_cmp_eq_u32_e64 s[8:9], 3, v39
	v_cmp_gt_f32_e64 s[10:11], v30, v37
	s_or_b64 s[8:9], s[8:9], s[10:11]
	s_and_b64 vcc, vcc, s[8:9]
	v_cndmask_b32_e64 v38, v38, 2, vcc
	v_cndmask_b32_e32 v37, v37, v30, vcc
	v_and_b32_e32 v39, 8, v36
	v_cmp_gt_i32_e64 s[8:9], 0, v38
	v_cmp_gt_f32_e64 s[10:11], v31, v37
	v_cmp_eq_u32_e32 vcc, 0, v39
	s_or_b64 s[8:9], s[8:9], s[10:11]
	s_and_b64 vcc, vcc, s[8:9]
	v_cndmask_b32_e64 v38, v38, 3, vcc
	v_cndmask_b32_e32 v37, v37, v31, vcc
	v_and_b32_e32 v39, 16, v36
	v_cmp_gt_i32_e64 s[8:9], 0, v38
	v_cmp_gt_f32_e64 s[10:11], v28, v37
	v_cmp_eq_u32_e32 vcc, 0, v39
	s_or_b64 s[8:9], s[8:9], s[10:11]
	s_and_b64 vcc, vcc, s[8:9]
	v_cndmask_b32_e64 v38, v38, 4, vcc
	v_cndmask_b32_e32 v37, v37, v28, vcc
	v_and_b32_e32 v39, 32, v36
	v_cmp_gt_i32_e64 s[8:9], 0, v38
	v_cmp_gt_f32_e64 s[10:11], v29, v37
	v_cmp_eq_u32_e32 vcc, 0, v39
	s_or_b64 s[8:9], s[8:9], s[10:11]
	s_and_b64 vcc, vcc, s[8:9]
	v_cndmask_b32_e64 v38, v38, 5, vcc
	v_cndmask_b32_e32 v37, v37, v29, vcc
	v_and_b32_e32 v39, 64, v36
	v_cmp_gt_i32_e64 s[8:9], 0, v38
	v_cmp_gt_f32_e64 s[10:11], v26, v37
	v_cmp_eq_u32_e32 vcc, 0, v39
	s_or_b64 s[8:9], s[8:9], s[10:11]
	s_and_b64 vcc, vcc, s[8:9]
	v_cndmask_b32_e64 v38, v38, 6, vcc
	v_cndmask_b32_e32 v37, v37, v26, vcc
	v_and_b32_e32 v39, 0x80, v36
	v_cmp_gt_i32_e64 s[8:9], 0, v38
	v_cmp_gt_f32_e64 s[10:11], v27, v37
	v_cmp_eq_u32_e32 vcc, 0, v39
	s_or_b64 s[8:9], s[8:9], s[10:11]
	s_and_b64 vcc, vcc, s[8:9]
	v_cndmask_b32_e64 v38, v38, 7, vcc
	v_cndmask_b32_e32 v37, v37, v27, vcc
	v_and_b32_e32 v39, 0x100, v36
	v_cmp_gt_i32_e64 s[8:9], 0, v38
	v_cmp_gt_f32_e64 s[10:11], v24, v37
	v_cmp_eq_u32_e32 vcc, 0, v39
	s_or_b64 s[8:9], s[8:9], s[10:11]
	s_and_b64 vcc, vcc, s[8:9]
	v_cndmask_b32_e64 v38, v38, 8, vcc
	v_cndmask_b32_e32 v37, v37, v24, vcc
	v_and_b32_e32 v39, 0x200, v36
	v_cmp_gt_i32_e64 s[8:9], 0, v38
	v_cmp_gt_f32_e64 s[10:11], v25, v37
	v_cmp_eq_u32_e32 vcc, 0, v39
	s_or_b64 s[8:9], s[8:9], s[10:11]
	s_and_b64 vcc, vcc, s[8:9]
	v_cndmask_b32_e64 v38, v38, 9, vcc
	v_cndmask_b32_e32 v37, v37, v25, vcc
	v_and_b32_e32 v39, 0x400, v36
	v_cmp_gt_i32_e64 s[8:9], 0, v38
	v_cmp_gt_f32_e64 s[10:11], v22, v37
	v_cmp_eq_u32_e32 vcc, 0, v39
	s_or_b64 s[8:9], s[8:9], s[10:11]
	s_and_b64 vcc, vcc, s[8:9]
	v_cndmask_b32_e64 v38, v38, 10, vcc
	v_cndmask_b32_e32 v37, v37, v22, vcc
	v_and_b32_e32 v39, 0x800, v36
	v_cmp_gt_i32_e64 s[8:9], 0, v38
	v_cmp_gt_f32_e64 s[10:11], v23, v37
	v_cmp_eq_u32_e32 vcc, 0, v39
	s_or_b64 s[8:9], s[8:9], s[10:11]
	s_and_b64 vcc, vcc, s[8:9]
	v_cndmask_b32_e64 v38, v38, 11, vcc
	v_cndmask_b32_e32 v37, v37, v23, vcc
	v_and_b32_e32 v39, 0x1000, v36
	v_cmp_gt_i32_e64 s[8:9], 0, v38
	v_cmp_gt_f32_e64 s[10:11], v20, v37
	v_cmp_eq_u32_e32 vcc, 0, v39
	s_or_b64 s[8:9], s[8:9], s[10:11]
	s_and_b64 vcc, vcc, s[8:9]
	v_cndmask_b32_e64 v38, v38, 12, vcc
	v_cndmask_b32_e32 v37, v37, v20, vcc
	v_and_b32_e32 v39, 0x2000, v36
	v_cmp_gt_i32_e64 s[8:9], 0, v38
	v_cmp_gt_f32_e64 s[10:11], v21, v37
	v_cmp_eq_u32_e32 vcc, 0, v39
	s_or_b64 s[8:9], s[8:9], s[10:11]
	s_and_b64 vcc, vcc, s[8:9]
	v_cndmask_b32_e64 v38, v38, 13, vcc
	v_cndmask_b32_e32 v37, v37, v21, vcc
	v_and_b32_e32 v39, 0x4000, v36
	v_cmp_gt_i32_e64 s[8:9], 0, v38
	v_cmp_gt_f32_e64 s[10:11], v18, v37
	v_cmp_eq_u32_e32 vcc, 0, v39
	s_or_b64 s[8:9], s[8:9], s[10:11]
	s_and_b64 vcc, vcc, s[8:9]
	v_cndmask_b32_e64 v38, v38, 14, vcc
	v_cndmask_b32_e32 v37, v37, v18, vcc
	v_and_b32_e32 v39, 0x8000, v36
	v_cmp_gt_i32_e64 s[8:9], 0, v38
	v_cmp_gt_f32_e64 s[10:11], v19, v37
	v_cmp_eq_u32_e32 vcc, 0, v39
	s_or_b64 s[8:9], s[8:9], s[10:11]
	s_and_b64 vcc, vcc, s[8:9]
	v_cndmask_b32_e64 v38, v38, 15, vcc
	v_cndmask_b32_e32 v37, v37, v19, vcc
	v_and_b32_e32 v39, 0x10000, v36
	v_cmp_gt_i32_e64 s[8:9], 0, v38
	v_cmp_gt_f32_e64 s[10:11], v16, v37
	v_cmp_eq_u32_e32 vcc, 0, v39
	s_or_b64 s[8:9], s[8:9], s[10:11]
	s_and_b64 vcc, vcc, s[8:9]
	v_cndmask_b32_e64 v38, v38, 16, vcc
	v_cndmask_b32_e32 v37, v37, v16, vcc
	v_and_b32_e32 v39, 0x20000, v36
	v_cmp_gt_i32_e64 s[8:9], 0, v38
	v_cmp_gt_f32_e64 s[10:11], v17, v37
	v_cmp_eq_u32_e32 vcc, 0, v39
	s_or_b64 s[8:9], s[8:9], s[10:11]
	s_and_b64 vcc, vcc, s[8:9]
	v_cndmask_b32_e64 v38, v38, 17, vcc
	v_cndmask_b32_e32 v37, v37, v17, vcc
	v_and_b32_e32 v39, 0x40000, v36
	v_cmp_gt_i32_e64 s[8:9], 0, v38
	v_cmp_gt_f32_e64 s[10:11], v14, v37
	v_cmp_eq_u32_e32 vcc, 0, v39
	s_or_b64 s[8:9], s[8:9], s[10:11]
	s_and_b64 vcc, vcc, s[8:9]
	v_cndmask_b32_e64 v38, v38, 18, vcc
	v_cndmask_b32_e32 v37, v37, v14, vcc
	v_and_b32_e32 v39, 0x80000, v36
	v_cmp_gt_i32_e64 s[8:9], 0, v38
	v_cmp_gt_f32_e64 s[10:11], v15, v37
	v_cmp_eq_u32_e32 vcc, 0, v39
	s_or_b64 s[8:9], s[8:9], s[10:11]
	s_and_b64 vcc, vcc, s[8:9]
	v_cndmask_b32_e64 v38, v38, 19, vcc
	v_cndmask_b32_e32 v37, v37, v15, vcc
	v_and_b32_e32 v39, 0x100000, v36
	v_cmp_gt_i32_e64 s[8:9], 0, v38
	v_cmp_gt_f32_e64 s[10:11], v12, v37
	v_cmp_eq_u32_e32 vcc, 0, v39
	s_or_b64 s[8:9], s[8:9], s[10:11]
	s_and_b64 vcc, vcc, s[8:9]
	v_cndmask_b32_e64 v38, v38, 20, vcc
	v_cndmask_b32_e32 v37, v37, v12, vcc
	v_and_b32_e32 v39, 0x200000, v36
	v_cmp_gt_i32_e64 s[8:9], 0, v38
	v_cmp_gt_f32_e64 s[10:11], v13, v37
	v_cmp_eq_u32_e32 vcc, 0, v39
	s_or_b64 s[8:9], s[8:9], s[10:11]
	s_and_b64 vcc, vcc, s[8:9]
	v_cndmask_b32_e64 v38, v38, 21, vcc
	v_cndmask_b32_e32 v37, v37, v13, vcc
	v_and_b32_e32 v39, 0x400000, v36
	v_cmp_gt_i32_e64 s[8:9], 0, v38
	v_cmp_gt_f32_e64 s[10:11], v10, v37
	v_cmp_eq_u32_e32 vcc, 0, v39
	s_or_b64 s[8:9], s[8:9], s[10:11]
	s_and_b64 vcc, vcc, s[8:9]
	v_cndmask_b32_e64 v38, v38, 22, vcc
	v_cndmask_b32_e32 v37, v37, v10, vcc
	v_and_b32_e32 v39, 0x800000, v36
	v_cmp_gt_i32_e64 s[8:9], 0, v38
	v_cmp_gt_f32_e64 s[10:11], v11, v37
	v_cmp_eq_u32_e32 vcc, 0, v39
	s_or_b64 s[8:9], s[8:9], s[10:11]
	s_and_b64 vcc, vcc, s[8:9]
	v_cndmask_b32_e64 v38, v38, 23, vcc
	v_cndmask_b32_e32 v37, v37, v11, vcc
	v_and_b32_e32 v39, 0x1000000, v36
	v_cmp_gt_i32_e64 s[8:9], 0, v38
	v_cmp_gt_f32_e64 s[10:11], v8, v37
	v_cmp_eq_u32_e32 vcc, 0, v39
	s_or_b64 s[8:9], s[8:9], s[10:11]
	s_and_b64 vcc, vcc, s[8:9]
	v_cndmask_b32_e64 v38, v38, 24, vcc
	v_cndmask_b32_e32 v37, v37, v8, vcc
	v_and_b32_e32 v39, 0x2000000, v36
	v_cmp_gt_i32_e64 s[8:9], 0, v38
	v_cmp_gt_f32_e64 s[10:11], v9, v37
	v_cmp_eq_u32_e32 vcc, 0, v39
	s_or_b64 s[8:9], s[8:9], s[10:11]
	s_and_b64 vcc, vcc, s[8:9]
	v_cndmask_b32_e64 v38, v38, 25, vcc
	v_cndmask_b32_e32 v37, v37, v9, vcc
	v_and_b32_e32 v39, 0x4000000, v36
	v_cmp_gt_i32_e64 s[8:9], 0, v38
	v_cmp_gt_f32_e64 s[10:11], v6, v37
	v_cmp_eq_u32_e32 vcc, 0, v39
	s_or_b64 s[8:9], s[8:9], s[10:11]
	s_and_b64 vcc, vcc, s[8:9]
	v_cndmask_b32_e64 v38, v38, 26, vcc
	v_cndmask_b32_e32 v37, v37, v6, vcc
	v_and_b32_e32 v39, 0x8000000, v36
	v_cmp_gt_i32_e64 s[8:9], 0, v38
	v_cmp_gt_f32_e64 s[10:11], v7, v37
	v_cmp_eq_u32_e32 vcc, 0, v39
	s_or_b64 s[8:9], s[8:9], s[10:11]
	s_and_b64 vcc, vcc, s[8:9]
	v_cndmask_b32_e64 v38, v38, 27, vcc
	v_cndmask_b32_e32 v37, v37, v7, vcc
	v_and_b32_e32 v39, 0x10000000, v36
	v_cmp_gt_i32_e64 s[8:9], 0, v38
	v_cmp_gt_f32_e64 s[10:11], v4, v37
	v_cmp_eq_u32_e32 vcc, 0, v39
	s_or_b64 s[8:9], s[8:9], s[10:11]
	s_and_b64 vcc, vcc, s[8:9]
	v_cndmask_b32_e64 v38, v38, 28, vcc
	v_cndmask_b32_e32 v37, v37, v4, vcc
	v_and_b32_e32 v39, 0x20000000, v36
	v_cmp_gt_i32_e64 s[8:9], 0, v38
	v_cmp_gt_f32_e64 s[10:11], v5, v37
	v_cmp_eq_u32_e32 vcc, 0, v39
	s_or_b64 s[8:9], s[8:9], s[10:11]
	s_and_b64 vcc, vcc, s[8:9]
	v_cndmask_b32_e64 v38, v38, 29, vcc
	v_cndmask_b32_e32 v37, v37, v5, vcc
	v_and_b32_e32 v39, 2.0, v36
	v_cmp_gt_i32_e64 s[8:9], 0, v38
	v_cmp_gt_f32_e64 s[10:11], v2, v37
	v_cmp_eq_u32_e32 vcc, 0, v39
	s_or_b64 s[8:9], s[8:9], s[10:11]
	s_and_b64 vcc, vcc, s[8:9]
	v_cndmask_b32_e64 v38, v38, 30, vcc
	v_cndmask_b32_e32 v37, v37, v2, vcc
	v_cmp_gt_i32_e64 s[8:9], 0, v38
	v_cmp_gt_f32_e64 s[10:11], v3, v37
	v_cmp_lt_i32_e32 vcc, -1, v36
	s_or_b64 s[8:9], s[8:9], s[10:11]
	s_and_b64 vcc, vcc, s[8:9]
	v_cndmask_b32_e64 v152, v38, 31, vcc
	v_lshlrev_b32_e64 v38, v152, 1
	v_or_b32_e32 v39, v38, v36
	v_and_b32_e32 v40, 1, v39
	v_cndmask_b32_e32 v37, v37, v3, vcc
	v_cmp_eq_u32_e32 vcc, 1, v40
	v_bitop3_b32 v42, v38, 2, v36 bitop3:0xc8
	v_bfe_i32 v41, v39, 0, 1
	v_cndmask_b32_e32 v40, v32, v198, vcc
	v_cmp_gt_f32_e64 s[8:9], v33, v40
	s_or_b64 vcc, vcc, s[8:9]
	v_cndmask_b32_e64 v43, 0, 1, vcc
	v_cndmask_b32_e32 v32, v32, v33, vcc
	v_cmp_eq_u32_e32 vcc, 0, v42
	s_nop 1
	v_cndmask_b32_e32 v32, v40, v32, vcc
	v_bitop3_b32 v40, v38, 4, v36 bitop3:0xc8
	v_cndmask_b32_e32 v33, v41, v43, vcc
	v_cmp_eq_u32_e32 vcc, 0, v40
	v_bitop3_b32 v40, v38, 3, v36 bitop3:0xc8
	v_cmp_eq_u32_e64 s[8:9], 3, v40
	v_cmp_gt_f32_e64 s[10:11], v30, v32
	s_or_b64 s[8:9], s[8:9], s[10:11]
	s_and_b64 vcc, vcc, s[8:9]
	v_cndmask_b32_e64 v33, v33, 2, vcc
	v_cndmask_b32_e32 v30, v32, v30, vcc
	v_bitop3_b32 v32, v38, 8, v36 bitop3:0xc8
	v_cmp_gt_i32_e64 s[8:9], 0, v33
	v_cmp_gt_f32_e64 s[10:11], v31, v30
	v_cmp_eq_u32_e32 vcc, 0, v32
	s_or_b64 s[8:9], s[8:9], s[10:11]
	s_and_b64 vcc, vcc, s[8:9]
	v_cndmask_b32_e64 v32, v33, 3, vcc
	v_cndmask_b32_e32 v30, v30, v31, vcc
	v_bitop3_b32 v31, v38, 16, v36 bitop3:0xc8
	v_cmp_gt_i32_e64 s[8:9], 0, v32
	v_cmp_gt_f32_e64 s[10:11], v28, v30
	v_cmp_eq_u32_e32 vcc, 0, v31
	s_or_b64 s[8:9], s[8:9], s[10:11]
	s_and_b64 vcc, vcc, s[8:9]
	v_cndmask_b32_e64 v31, v32, 4, vcc
	v_cndmask_b32_e32 v28, v30, v28, vcc
	v_bitop3_b32 v30, v38, 32, v36 bitop3:0xc8
	v_cmp_gt_i32_e64 s[8:9], 0, v31
	v_cmp_gt_f32_e64 s[10:11], v29, v28
	v_cmp_eq_u32_e32 vcc, 0, v30
	s_or_b64 s[8:9], s[8:9], s[10:11]
	s_and_b64 vcc, vcc, s[8:9]
	v_cndmask_b32_e64 v30, v31, 5, vcc
	v_cndmask_b32_e32 v28, v28, v29, vcc
	v_bitop3_b32 v29, v38, 64, v36 bitop3:0xc8
	v_cmp_gt_i32_e64 s[8:9], 0, v30
	v_cmp_gt_f32_e64 s[10:11], v26, v28
	v_cmp_eq_u32_e32 vcc, 0, v29
	s_or_b64 s[8:9], s[8:9], s[10:11]
	s_and_b64 vcc, vcc, s[8:9]
	v_cndmask_b32_e64 v29, v30, 6, vcc
	v_cndmask_b32_e32 v26, v28, v26, vcc
	v_bitop3_b32 v28, v38, s26, v36 bitop3:0xc8
	v_cmp_gt_i32_e64 s[8:9], 0, v29
	v_cmp_gt_f32_e64 s[10:11], v27, v26
	v_cmp_eq_u32_e32 vcc, 0, v28
	s_or_b64 s[8:9], s[8:9], s[10:11]
	s_and_b64 vcc, vcc, s[8:9]
	v_cndmask_b32_e64 v28, v29, 7, vcc
	v_cndmask_b32_e32 v26, v26, v27, vcc
	v_bitop3_b32 v27, v38, s27, v36 bitop3:0xc8
	v_cmp_gt_i32_e64 s[8:9], 0, v28
	v_cmp_gt_f32_e64 s[10:11], v24, v26
	v_cmp_eq_u32_e32 vcc, 0, v27
	s_or_b64 s[8:9], s[8:9], s[10:11]
	s_and_b64 vcc, vcc, s[8:9]
	v_cndmask_b32_e64 v27, v28, 8, vcc
	v_cndmask_b32_e32 v24, v26, v24, vcc
	v_bitop3_b32 v26, v38, s28, v36 bitop3:0xc8
	v_cmp_gt_i32_e64 s[8:9], 0, v27
	v_cmp_gt_f32_e64 s[10:11], v25, v24
	v_cmp_eq_u32_e32 vcc, 0, v26
	s_or_b64 s[8:9], s[8:9], s[10:11]
	s_and_b64 vcc, vcc, s[8:9]
	v_cndmask_b32_e64 v26, v27, 9, vcc
	v_cndmask_b32_e32 v24, v24, v25, vcc
	v_bitop3_b32 v25, v38, s29, v36 bitop3:0xc8
	v_cmp_gt_i32_e64 s[8:9], 0, v26
	v_cmp_gt_f32_e64 s[10:11], v22, v24
	v_cmp_eq_u32_e32 vcc, 0, v25
	s_or_b64 s[8:9], s[8:9], s[10:11]
	s_and_b64 vcc, vcc, s[8:9]
	v_cndmask_b32_e64 v25, v26, 10, vcc
	v_cndmask_b32_e32 v22, v24, v22, vcc
	v_bitop3_b32 v24, v38, s30, v36 bitop3:0xc8
	v_cmp_gt_i32_e64 s[8:9], 0, v25
	v_cmp_gt_f32_e64 s[10:11], v23, v22
	v_cmp_eq_u32_e32 vcc, 0, v24
	s_or_b64 s[8:9], s[8:9], s[10:11]
	s_and_b64 vcc, vcc, s[8:9]
	v_cndmask_b32_e64 v24, v25, 11, vcc
	v_cndmask_b32_e32 v22, v22, v23, vcc
	v_bitop3_b32 v23, v38, s31, v36 bitop3:0xc8
	v_cmp_gt_i32_e64 s[8:9], 0, v24
	v_cmp_gt_f32_e64 s[10:11], v20, v22
	v_cmp_eq_u32_e32 vcc, 0, v23
	s_or_b64 s[8:9], s[8:9], s[10:11]
	s_and_b64 vcc, vcc, s[8:9]
	v_cndmask_b32_e64 v23, v24, 12, vcc
	v_cndmask_b32_e32 v20, v22, v20, vcc
	v_bitop3_b32 v22, v38, s33, v36 bitop3:0xc8
	v_cmp_gt_i32_e64 s[8:9], 0, v23
	v_cmp_gt_f32_e64 s[10:11], v21, v20
	v_cmp_eq_u32_e32 vcc, 0, v22
	s_or_b64 s[8:9], s[8:9], s[10:11]
	s_and_b64 vcc, vcc, s[8:9]
	v_cndmask_b32_e64 v22, v23, 13, vcc
	v_cndmask_b32_e32 v20, v20, v21, vcc
	v_bitop3_b32 v21, v38, s34, v36 bitop3:0xc8
	v_cmp_gt_i32_e64 s[8:9], 0, v22
	v_cmp_gt_f32_e64 s[10:11], v18, v20
	v_cmp_eq_u32_e32 vcc, 0, v21
	s_or_b64 s[8:9], s[8:9], s[10:11]
	s_and_b64 vcc, vcc, s[8:9]
	v_cndmask_b32_e64 v21, v22, 14, vcc
	v_cndmask_b32_e32 v18, v20, v18, vcc
	v_bitop3_b32 v20, v38, s35, v36 bitop3:0xc8
	v_cmp_gt_i32_e64 s[8:9], 0, v21
	v_cmp_gt_f32_e64 s[10:11], v19, v18
	v_cmp_eq_u32_e32 vcc, 0, v20
	s_or_b64 s[8:9], s[8:9], s[10:11]
	s_and_b64 vcc, vcc, s[8:9]
	v_cndmask_b32_e64 v20, v21, 15, vcc
	v_cndmask_b32_e32 v18, v18, v19, vcc
	v_bitop3_b32 v19, v38, s36, v36 bitop3:0xc8
	v_cmp_gt_i32_e64 s[8:9], 0, v20
	v_cmp_gt_f32_e64 s[10:11], v16, v18
	v_cmp_eq_u32_e32 vcc, 0, v19
	s_or_b64 s[8:9], s[8:9], s[10:11]
	s_and_b64 vcc, vcc, s[8:9]
	v_cndmask_b32_e64 v19, v20, 16, vcc
	v_cndmask_b32_e32 v16, v18, v16, vcc
	v_bitop3_b32 v18, v38, s37, v36 bitop3:0xc8
	v_cmp_gt_i32_e64 s[8:9], 0, v19
	v_cmp_gt_f32_e64 s[10:11], v17, v16
	v_cmp_eq_u32_e32 vcc, 0, v18
	s_or_b64 s[8:9], s[8:9], s[10:11]
	s_and_b64 vcc, vcc, s[8:9]
	v_cndmask_b32_e64 v18, v19, 17, vcc
	v_cndmask_b32_e32 v16, v16, v17, vcc
	v_bitop3_b32 v17, v38, s38, v36 bitop3:0xc8
	v_cmp_gt_i32_e64 s[8:9], 0, v18
	v_cmp_gt_f32_e64 s[10:11], v14, v16
	v_cmp_eq_u32_e32 vcc, 0, v17
	s_or_b64 s[8:9], s[8:9], s[10:11]
	s_and_b64 vcc, vcc, s[8:9]
	v_cndmask_b32_e64 v17, v18, 18, vcc
	v_cndmask_b32_e32 v14, v16, v14, vcc
	v_bitop3_b32 v16, v38, s39, v36 bitop3:0xc8
	v_cmp_gt_i32_e64 s[8:9], 0, v17
	v_cmp_gt_f32_e64 s[10:11], v15, v14
	v_cmp_eq_u32_e32 vcc, 0, v16
	s_or_b64 s[8:9], s[8:9], s[10:11]
	s_and_b64 vcc, vcc, s[8:9]
	v_cndmask_b32_e64 v16, v17, 19, vcc
	v_cndmask_b32_e32 v14, v14, v15, vcc
	v_bitop3_b32 v15, v38, s40, v36 bitop3:0xc8
	v_cmp_gt_i32_e64 s[8:9], 0, v16
	v_cmp_gt_f32_e64 s[10:11], v12, v14
	v_cmp_eq_u32_e32 vcc, 0, v15
	s_or_b64 s[8:9], s[8:9], s[10:11]
	s_and_b64 vcc, vcc, s[8:9]
	v_cndmask_b32_e64 v15, v16, 20, vcc
	v_cndmask_b32_e32 v12, v14, v12, vcc
	v_bitop3_b32 v14, v38, s41, v36 bitop3:0xc8
	v_cmp_gt_i32_e64 s[8:9], 0, v15
	v_cmp_gt_f32_e64 s[10:11], v13, v12
	v_cmp_eq_u32_e32 vcc, 0, v14
	s_or_b64 s[8:9], s[8:9], s[10:11]
	s_and_b64 vcc, vcc, s[8:9]
	v_cndmask_b32_e64 v14, v15, 21, vcc
	v_cndmask_b32_e32 v12, v12, v13, vcc
	v_bitop3_b32 v13, v38, s42, v36 bitop3:0xc8
	v_cmp_gt_i32_e64 s[8:9], 0, v14
	v_cmp_gt_f32_e64 s[10:11], v10, v12
	v_cmp_eq_u32_e32 vcc, 0, v13
	s_or_b64 s[8:9], s[8:9], s[10:11]
	s_and_b64 vcc, vcc, s[8:9]
	v_cndmask_b32_e64 v13, v14, 22, vcc
	v_cndmask_b32_e32 v10, v12, v10, vcc
	v_bitop3_b32 v12, v38, s43, v36 bitop3:0xc8
	v_cmp_gt_i32_e64 s[8:9], 0, v13
	v_cmp_gt_f32_e64 s[10:11], v11, v10
	v_cmp_eq_u32_e32 vcc, 0, v12
	s_or_b64 s[8:9], s[8:9], s[10:11]
	s_and_b64 vcc, vcc, s[8:9]
	v_cndmask_b32_e64 v12, v13, 23, vcc
	v_cndmask_b32_e32 v10, v10, v11, vcc
	v_bitop3_b32 v11, v38, s44, v36 bitop3:0xc8
	v_cmp_gt_i32_e64 s[8:9], 0, v12
	v_cmp_gt_f32_e64 s[10:11], v8, v10
	v_cmp_eq_u32_e32 vcc, 0, v11
	s_or_b64 s[8:9], s[8:9], s[10:11]
	s_and_b64 vcc, vcc, s[8:9]
	v_cndmask_b32_e64 v11, v12, 24, vcc
	v_cndmask_b32_e32 v8, v10, v8, vcc
	v_bitop3_b32 v10, v38, s45, v36 bitop3:0xc8
	v_cmp_gt_i32_e64 s[8:9], 0, v11
	v_cmp_gt_f32_e64 s[10:11], v9, v8
	v_cmp_eq_u32_e32 vcc, 0, v10
	s_or_b64 s[8:9], s[8:9], s[10:11]
	s_and_b64 vcc, vcc, s[8:9]
	v_cndmask_b32_e64 v10, v11, 25, vcc
	v_cndmask_b32_e32 v8, v8, v9, vcc
	v_bitop3_b32 v9, v38, s46, v36 bitop3:0xc8
	v_cmp_gt_i32_e64 s[8:9], 0, v10
	v_cmp_gt_f32_e64 s[10:11], v6, v8
	v_cmp_eq_u32_e32 vcc, 0, v9
	s_or_b64 s[8:9], s[8:9], s[10:11]
	s_and_b64 vcc, vcc, s[8:9]
	v_cndmask_b32_e64 v9, v10, 26, vcc
	v_cndmask_b32_e32 v6, v8, v6, vcc
	v_bitop3_b32 v8, v38, s47, v36 bitop3:0xc8
	v_cmp_gt_i32_e64 s[8:9], 0, v9
	v_cmp_gt_f32_e64 s[10:11], v7, v6
	v_cmp_eq_u32_e32 vcc, 0, v8
	s_or_b64 s[8:9], s[8:9], s[10:11]
	s_and_b64 vcc, vcc, s[8:9]
	v_cndmask_b32_e64 v8, v9, 27, vcc
	v_cndmask_b32_e32 v6, v6, v7, vcc
	v_bitop3_b32 v7, v38, s48, v36 bitop3:0xc8
	v_cmp_gt_i32_e64 s[8:9], 0, v8
	v_cmp_gt_f32_e64 s[10:11], v4, v6
	v_cmp_eq_u32_e32 vcc, 0, v7
	s_or_b64 s[8:9], s[8:9], s[10:11]
	s_and_b64 vcc, vcc, s[8:9]
	v_cndmask_b32_e64 v7, v8, 28, vcc
	v_cndmask_b32_e32 v4, v6, v4, vcc
	v_bitop3_b32 v6, v38, s49, v36 bitop3:0xc8
	v_cmp_gt_i32_e64 s[8:9], 0, v7
	v_cmp_gt_f32_e64 s[10:11], v5, v4
	v_cmp_eq_u32_e32 vcc, 0, v6
	s_or_b64 s[8:9], s[8:9], s[10:11]
	s_and_b64 vcc, vcc, s[8:9]
	v_cndmask_b32_e64 v6, v7, 29, vcc
	v_cndmask_b32_e32 v4, v4, v5, vcc
	v_bitop3_b32 v5, v38, 2.0, v36 bitop3:0xc8
	v_cmp_gt_i32_e64 s[8:9], 0, v6
	v_cmp_gt_f32_e64 s[10:11], v2, v4
	v_cmp_eq_u32_e32 vcc, 0, v5
	s_or_b64 s[8:9], s[8:9], s[10:11]
	s_and_b64 vcc, vcc, s[8:9]
	v_cndmask_b32_e32 v2, v4, v2, vcc
	v_sub_f32_e32 v4, v35, v34
	v_cndmask_b32_e64 v5, v6, 30, vcc
	v_mul_f32_e32 v6, 0x3fb8aa3b, v4
	v_fma_f32 v7, v4, s50, -v6
	v_rndne_f32_e32 v8, v6
	v_fmac_f32_e32 v7, 0x32a5705f, v4
	v_sub_f32_e32 v6, v6, v8
	v_add_f32_e32 v6, v6, v7
	v_cmp_gt_i32_e64 s[8:9], 0, v5
	v_cmp_gt_f32_e64 s[10:11], v3, v2
	v_exp_f32_e32 v6, v6
	v_cvt_i32_f32_e32 v7, v8
	v_cmp_lt_i32_e32 vcc, -1, v39
	s_or_b64 s[8:9], s[8:9], s[10:11]
	s_and_b64 vcc, vcc, s[8:9]
	v_cndmask_b32_e64 v156, v5, 31, vcc
	v_sub_f32_e32 v5, v37, v34
	v_cndmask_b32_e32 v2, v2, v3, vcc
	v_ldexp_f32 v3, v6, v7
	v_mul_f32_e32 v6, 0x3fb8aa3b, v5
	v_fma_f32 v7, v5, s50, -v6
	v_rndne_f32_e32 v8, v6
	v_fmac_f32_e32 v7, 0x32a5705f, v5
	v_sub_f32_e32 v6, v6, v8
	v_add_f32_e32 v6, v6, v7
	v_exp_f32_e32 v6, v6
	v_cvt_i32_f32_e32 v7, v8
	v_cmp_ngt_f32_e32 vcc, s51, v4
	v_sub_f32_e32 v2, v2, v34
	s_nop 0
	v_cndmask_b32_e32 v3, 0, v3, vcc
	v_cmp_nlt_f32_e32 vcc, s52, v4
	s_nop 1
	v_cndmask_b32_e32 v4, v199, v3, vcc
	v_ldexp_f32 v3, v6, v7
	v_mul_f32_e32 v6, 0x3fb8aa3b, v2
	v_fma_f32 v7, v2, s50, -v6
	v_rndne_f32_e32 v8, v6
	v_fmac_f32_e32 v7, 0x32a5705f, v2
	v_sub_f32_e32 v6, v6, v8
	v_add_f32_e32 v6, v6, v7
	v_exp_f32_e32 v6, v6
	v_cvt_i32_f32_e32 v7, v8
	v_cmp_ngt_f32_e32 vcc, s51, v5
	s_nop 1
	v_cndmask_b32_e32 v3, 0, v3, vcc
	v_cmp_nlt_f32_e32 vcc, s52, v5
	v_ldexp_f32 v5, v6, v7
	s_nop 0
	v_cndmask_b32_e32 v3, v199, v3, vcc
	v_cmp_ngt_f32_e32 vcc, s51, v2
	s_nop 1
	v_cndmask_b32_e32 v5, 0, v5, vcc
	v_cmp_nlt_f32_e32 vcc, s52, v2
	s_nop 1
	v_cndmask_b32_e32 v2, v199, v5, vcc
	v_add_f32_e32 v5, 1.0, v4
	v_add_f32_e32 v5, v5, v3
	v_add_f32_e32 v5, v5, v2
	v_div_scale_f32 v6, s[8:9], v5, v5, 1.0
	v_rcp_f32_e32 v7, v6
	s_nop 0
	v_fma_f32 v8, -v6, v7, 1.0
	v_fmac_f32_e32 v7, v8, v7
	v_div_scale_f32 v8, vcc, 1.0, v5, 1.0
	v_mul_f32_e32 v9, v8, v7
	v_fma_f32 v10, -v6, v9, v8
	v_fmac_f32_e32 v9, v10, v7
	v_fma_f32 v6, -v6, v9, v8
	v_lshl_add_u32 v8, v144, 2, s1
	ds_add_rtn_u32 v200, v8, v197
	v_lshl_add_u32 v8, v148, 2, s1
	ds_add_rtn_u32 v201, v8, v197
	v_lshl_add_u32 v8, v152, 2, s1
	ds_add_rtn_u32 v202, v8, v197
	v_lshl_add_u32 v8, v156, 2, s1
	ds_add_rtn_u32 v204, v8, v197
	v_div_fmas_f32 v6, v6, v7, v9
	v_div_fixup_f32 v138, v6, v5, 1.0
	v_mul_f32_e32 v203, v4, v138
	v_pk_mul_f32 v[162:163], v[2:3], v[138:139] op_sel_hi:[1,0]
